# P12 dot-product loop: the 64 expert ids per lane are read from LDS once before the chunk loop into dead VGPRs (was 64 dependent ds_read_u16 -> wait -> address chains per chunk)
# speedup vs baseline: 1.0231x; 1.0231x over previous
; #define LAS __attribute__((address_space(3)))
; __device__ __forceinline__ float bflo(unsigned w) { return __uint_as_float(w << 16); }
; __device__ __forceinline__ float bfhi(unsigned w) { return __uint_as_float(w & 0xffff0000u); }
; __device__ __forceinline__ float wave_sum(float v) { v = dpp_add16(v); return (rdlane(v, 0) + rdlane(v, 16)) + (rdlane(v, 32) + rdlane(v, 48)); }
; __device__ __forceinline__ float wave_max(float v) { v = dpp_max16(v); return fmaxf(fmaxf(rdlane(v, 0), rdlane(v, 16)), fmaxf(rdlane(v, 32), rdlane(v, 48))); }
; __device__ __forceinline__ void p12_peer(Frame& F) {
;     const bf16* HN = (const bf16*)(F.ws + WS_HN);
;     const unsigned char* U4 = F.ws + WS_U8; const unsigned short* USS = (const unsigned short*)(F.ws + WS_USC); const unsigned char* V8 = F.ws + WS_V8; const float* VSC = (const float*)(F.ws + WS_VSC);
;     const int* PIDX = (const int*)(F.ws + WS_PIDX); const float* PGT = (const float*)(F.ws + WS_PG); const float* PSQ = (const float*)(F.ws + WS_PSQ);
;     const float* lnf = F.in[22];
;     LAS unsigned char* XQ = F.lds + F.wave * 17408;
;     LAS unsigned short* EL = (LAS unsigned short*)(XQ + 16384);
;     LAS float* WL = (LAS float*)XQ;
;     const int g8 = F.lane >> 3, k8 = F.lane & 7;
;     float sx[4];
; #pragma unroll
;     for (int i = 0; i < 4; ++i) {
;         const int t = F.gw + i * F.NGW; v4u xp[8]; float mxa = 0.f;
; #pragma unroll
;         for (int j = 0; j < 8; ++j) { xp[j] = ((const v4u*)(HN + (size_t)t * D_))[F.lane + 64 * j];
;             mxa = fmaxf(fmaxf(fmaxf(mxa, fmaxf(fabsf(bflo(xp[j].x)), fabsf(bfhi(xp[j].x)))), fmaxf(fabsf(bflo(xp[j].y)), fabsf(bfhi(xp[j].y)))), fmaxf(fmaxf(fabsf(bflo(xp[j].z)), fabsf(bfhi(xp[j].z))), fmaxf(fabsf(bflo(xp[j].w)), fabsf(bfhi(xp[j].w))))); }
;         mxa = wave_max(mxa); const float inv = mxa > 0.f ? 127.0f / mxa : 0.f;
;         const float rsn = 1.0f / sqrtf(wave_sum(PSQ[(size_t)t * 64 + F.lane]) * (1.f / D_) + 1e-6f);
.LBB0_3270:
	s_cmp_gt_i32 s84, 12
	s_cselect_b64 s[0:1], -1, 0
	s_cmp_lt_i32 s85, 13
	s_cselect_b64 s[2:3], -1, 0
	s_or_b64 s[0:1], s[0:1], s[2:3]
	s_and_b64 vcc, exec, s[0:1]
	s_cbranch_vccnz .LBB0_3413
	s_add_u32 s6, s68, 0x23400000
	s_addc_u32 s7, s69, 0
	s_add_u32 s0, s68, 0x7000000
	s_addc_u32 s1, s69, 0
	s_waitcnt lgkmcnt(0)
	s_add_u32 s18, s68, 0xe00000
	s_addc_u32 s19, s69, 0
	s_add_u32 s22, s68, 0x800000
	s_addc_u32 s23, s69, 0
	s_mul_i32 s2, s66, 0x4400
	s_ashr_i32 s95, s94, 31
	s_add_i32 s20, s2, 0
	s_lshl_b64 s[2:3], s[94:95], 13
	v_mbcnt_lo_u32_b32 v92, -1, 0
	v_mbcnt_hi_u32_b32 v92, -1, v92
	s_add_u32 s2, s6, s2
	v_ashrrev_i32_e32 v93, 31, v92
	s_addc_u32 s3, s7, s3
	s_waitcnt vmcnt(7)
	v_lshlrev_b64 v[18:19], 4, v[92:93]
	v_lshl_add_u64 v[0:1], s[2:3], 0, v[18:19]
	global_load_dwordx4 v[12:15], v[0:1], off
	global_load_dwordx4 v[26:29], v[0:1], off offset:1024
	global_load_dwordx4 v[60:63], v[0:1], off offset:2048
	global_load_dwordx4 v[64:67], v[0:1], off offset:3072
	s_movk_i32 s28, 0x1000
	s_waitcnt vmcnt(4)
	v_add_co_u32_e32 v46, vcc, s28, v0
	s_lshl_b64 s[2:3], s[94:95], 8
	s_nop 0
	v_addc_co_u32_e32 v47, vcc, 0, v1, vcc
	global_load_dwordx4 v[0:3], v[46:47], off
	global_load_dwordx4 v[4:7], v[46:47], off offset:1024
	global_load_dwordx4 v[8:11], v[46:47], off offset:2048
	s_add_u32 s4, s22, s2
	s_addc_u32 s5, s23, s3
	s_lshl_b64 s[2:3], s[94:95], 9
	v_lshlrev_b64 v[16:17], 2, v[92:93]
	s_add_u32 s8, s18, s2
	v_lshl_add_u64 v[20:21], s[4:5], 0, v[16:17]
	s_addc_u32 s9, s19, s3
	v_lshl_add_u64 v[22:23], s[8:9], 0, v[16:17]
	s_mov_b32 s29, 0x42fe0000
	s_mov_b32 s21, 0x40c0c00
	v_lshl_add_u32 v25, v92, 3, s20
	s_add_i32 s4, s34, s94
	s_ashr_i32 s5, s4, 31
	s_lshl_b64 s[8:9], s[4:5], 13
	s_add_u32 s8, s6, s8
	v_lshl_add_u32 v24, v92, 1, s20
	s_addc_u32 s9, s7, s9
	v_ashrrev_i32_e32 v94, 3, v92
	v_lshl_add_u32 v93, v94, 1, s20
	v_and_b32_e32 v164, 7, v92
	v_lshlrev_b32_e32 v95, 1, v164
	v_lshlrev_b32_e32 v165, 4, v164
	v_mov_b32_e32 v109, 0
	s_mov_b32 s43, 0x5040100
	v_lshl_add_u32 v166, v164, 5, s20
	s_mov_b32 s44, 0
	v_mov_b32_e32 v108, 0
	v_mov_b32_e32 v110, 0
	v_mov_b32_e32 v111, v109
	v_mov_b32_e32 v112, 0
	v_mov_b32_e32 v113, v109
	v_mov_b32_e32 v114, 0
	v_mov_b32_e32 v115, v109
	v_mov_b32_e32 v116, 0
	v_mov_b32_e32 v117, v109
	v_mov_b32_e32 v118, 0
	v_mov_b32_e32 v119, v109
	v_mov_b32_e32 v120, 0
	v_mov_b32_e32 v121, v109
	v_mov_b32_e32 v122, 0
	v_mov_b32_e32 v123, v109
	v_mov_b32_e32 v124, 0
	v_mov_b32_e32 v125, v109
	v_mov_b32_e32 v126, 0
	v_mov_b32_e32 v127, v109
	v_mov_b32_e32 v128, 0
	v_mov_b32_e32 v129, v109
	v_mov_b32_e32 v130, 0
	v_mov_b32_e32 v131, v109
	v_mov_b32_e32 v132, 0
	v_mov_b32_e32 v133, v109
	v_mov_b32_e32 v134, 0
	v_mov_b32_e32 v135, v109
	v_mov_b32_e32 v136, 0
	v_mov_b32_e32 v137, v109
	v_mov_b32_e32 v138, 0
	v_mov_b32_e32 v139, v109
	v_mov_b32_e32 v140, 0
	v_mov_b32_e32 v141, v109
	v_mov_b32_e32 v142, 0
	v_mov_b32_e32 v143, v109
	v_mov_b32_e32 v144, 0
	v_mov_b32_e32 v145, v109
	v_mov_b32_e32 v146, 0
	v_mov_b32_e32 v147, v109
	v_mov_b32_e32 v148, 0
	v_mov_b32_e32 v149, v109
	v_mov_b32_e32 v150, 0
	v_mov_b32_e32 v151, v109
	s_waitcnt vmcnt(6)
	v_lshlrev_b32_e32 v58, 16, v12
	v_and_b32_e32 v57, 0xffff0000, v12
	v_lshlrev_b32_e32 v56, 16, v13
	v_and_b32_e32 v55, 0xffff0000, v13
	v_lshlrev_b32_e32 v52, 16, v15
	v_and_b32_e32 v51, 0xffff0000, v15
	v_lshlrev_b32_e32 v54, 16, v14
	v_and_b32_e32 v53, 0xffff0000, v14
	s_waitcnt vmcnt(5)
	v_lshlrev_b32_e32 v48, 16, v26
	v_and_b32_e32 v45, 0xffff0000, v26
	v_lshlrev_b32_e32 v38, 16, v29
	v_and_b32_e32 v37, 0xffff0000, v29
	v_max_f32_e64 v12, |v57|, |v57|
	v_max_f32_e64 v13, |v58|, |v58|
	v_max_f32_e64 v14, |v55|, |v55|
	v_max_f32_e64 v15, |v56|, |v56|
	v_max_f32_e64 v32, |v51|, |v51|
	v_max_f32_e64 v35, |v52|, |v52|
	v_lshlrev_b32_e32 v43, 16, v27
	v_and_b32_e32 v41, 0xffff0000, v27
	v_max_f32_e64 v36, |v45|, |v45|
	v_max_f32_e64 v42, |v48|, |v48|
	v_max_f32_e64 v50, |v37|, |v37|
	v_max_f32_e64 v59, |v38|, |v38|
	v_max_f32_e32 v12, v13, v12
	v_max_f32_e32 v13, v15, v14
	v_max_f32_e32 v14, v35, v32
	v_lshlrev_b32_e32 v40, 16, v28
	v_and_b32_e32 v39, 0xffff0000, v28
	s_waitcnt vmcnt(4)
	v_lshlrev_b32_e32 v34, 16, v60
	v_and_b32_e32 v33, 0xffff0000, v60
	v_lshlrev_b32_e32 v31, 16, v61
	v_and_b32_e32 v30, 0xffff0000, v61
	v_max_f32_e64 v44, |v41|, |v41|
	v_max_f32_e64 v49, |v43|, |v43|
	v_max_f32_e32 v15, v42, v36
	v_max_f32_e32 v35, v59, v50
	v_max3_f32 v12, v12, 0, v13
	v_max3_f32 v13, |v54|, |v53|, v14
	v_lshlrev_b32_e32 v29, 16, v62
	v_and_b32_e32 v28, 0xffff0000, v62
	v_lshlrev_b32_e32 v27, 16, v63
	v_and_b32_e32 v26, 0xffff0000, v63
	v_max_f32_e64 v60, |v33|, |v33|
	v_max_f32_e64 v61, |v34|, |v34|
	v_max_f32_e64 v62, |v30|, |v30|
	v_max_f32_e64 v63, |v31|, |v31|
	v_max_f32_e32 v32, v49, v44
	v_max3_f32 v14, |v40|, |v39|, v35
	v_max3_f32 v12, v12, v13, v15
	v_max_f32_e32 v36, v61, v60
	v_max_f32_e32 v42, v63, v62
	v_max3_f32 v12, v12, v32, v14
	v_max_f32_e64 v68, |v26|, |v26|
	v_max3_f32 v32, v12, v36, v42
	v_max_f32_e64 v12, |v27|, |v27|
	v_max_f32_e32 v12, v12, v68
	v_max3_f32 v42, |v29|, |v28|, v12
	global_load_dwordx4 v[12:15], v[46:47], off offset:3072
	s_waitcnt vmcnt(4)
	v_lshlrev_b32_e32 v36, 16, v64
	v_and_b32_e32 v35, 0xffff0000, v64
	v_max_f32_e64 v44, |v35|, |v35|
	v_max_f32_e64 v46, |v36|, |v36|
	v_max_f32_e32 v44, v46, v44
	v_lshlrev_b32_e32 v50, 16, v65
	v_and_b32_e32 v47, 0xffff0000, v65
	v_max3_f32 v32, v32, v42, v44
	v_max_f32_e64 v42, |v47|, |v47|
	v_max_f32_e64 v44, |v50|, |v50|
	v_max_f32_e32 v59, v44, v42
	v_lshlrev_b32_e32 v44, 16, v67
	v_and_b32_e32 v42, 0xffff0000, v67
	v_max_f32_e64 v60, |v42|, |v42|
	v_max_f32_e64 v61, |v44|, |v44|
	v_lshlrev_b32_e32 v49, 16, v66
	v_and_b32_e32 v46, 0xffff0000, v66
	v_max_f32_e32 v60, v61, v60
	v_max3_f32 v60, |v49|, |v46|, v60
	v_max3_f32 v59, v32, v59, v60
	global_load_dword v32, v[20:21], off
	global_load_dword v60, v[22:23], off
	global_load_dword v61, v[22:23], off offset:256
	s_waitcnt vmcnt(6)
; #define LAS __attribute__((address_space(3)))
; __device__ __forceinline__ float bflo(unsigned w) { return __uint_as_float(w << 16); }
; __device__ __forceinline__ float bfhi(unsigned w) { return __uint_as_float(w & 0xffff0000u); }
; __device__ __forceinline__ float wave_sum(float v) { v = dpp_add16(v); return (rdlane(v, 0) + rdlane(v, 16)) + (rdlane(v, 32) + rdlane(v, 48)); }
; __device__ __forceinline__ float wave_max(float v) { v = dpp_max16(v); return fmaxf(fmaxf(rdlane(v, 0), rdlane(v, 16)), fmaxf(rdlane(v, 32), rdlane(v, 48))); }
; __device__ __forceinline__ void p12_peer(Frame& F) {
;     ...
;             mxa = fmaxf(fmaxf(fmaxf(mxa, fmaxf(fabsf(bflo(xp[j].x)), fabsf(bfhi(xp[j].x)))), fmaxf(fabsf(bflo(xp[j].y)), fabsf(bfhi(xp[j].y)))), fmaxf(fmaxf(fabsf(bflo(xp[j].z)), fabsf(bfhi(xp[j].z))), fmaxf(fabsf(bflo(xp[j].w)), fabsf(bfhi(xp[j].w))))); }
;         mxa = wave_max(mxa); const float inv = mxa > 0.f ? 127.0f / mxa : 0.f;
;         const float rsn = 1.0f / sqrtf(wave_sum(PSQ[(size_t)t * 64 + F.lane]) * (1.f / D_) + 1e-6f);
;         sx[i] = mxa * rsn * (1.0f / 127.0f);
; #pragma unroll
;         for (int j = 0; j < 8; ++j) {
;             const int q0 = (int)rintf(bflo(xp[j].x) * inv), q1 = (int)rintf(bfhi(xp[j].x) * inv), q2 = (int)rintf(bflo(xp[j].y) * inv), q3 = (int)rintf(bfhi(xp[j].y) * inv);
;             const int q4 = (int)rintf(bflo(xp[j].z) * inv), q5 = (int)rintf(bfhi(xp[j].z) * inv), q6 = (int)rintf(bflo(xp[j].w) * inv), q7 = (int)rintf(bfhi(xp[j].w) * inv);
;             *(LAS v2u*)(XQ + i * 4096 + 8 * (F.lane + 64 * j)) = (v2u){(unsigned)((q0 & 0xff) | ((q1 & 0xff) << 8) | ((q2 & 0xff) << 16) | (q3 << 24)), (unsigned)((q4 & 0xff) | ((q5 & 0xff) << 8) | ((q6 & 0xff) << 16) | (q7 << 24))}; }
	v_lshlrev_b32_e32 v20, 16, v0
	v_and_b32_e32 v21, 0xffff0000, v0
	v_max_f32_e64 v0, |v21|, |v21|
	v_max_f32_e64 v22, |v20|, |v20|
	v_max_f32_e32 v0, v22, v0
	v_lshlrev_b32_e32 v22, 16, v1
	v_and_b32_e32 v23, 0xffff0000, v1
	v_max_f32_e64 v1, |v23|, |v23|
	v_max_f32_e64 v62, |v22|, |v22|
	v_max_f32_e32 v1, v62, v1
	v_lshlrev_b32_e32 v63, 16, v3
	v_and_b32_e32 v64, 0xffff0000, v3
	v_max3_f32 v0, v59, v0, v1
	v_lshlrev_b32_e32 v59, 16, v2
	v_and_b32_e32 v62, 0xffff0000, v2
	v_max_f32_e64 v1, |v64|, |v64|
	v_max_f32_e64 v2, |v63|, |v63|
	s_waitcnt vmcnt(5)
	v_lshlrev_b32_e32 v65, 16, v4
	v_and_b32_e32 v66, 0xffff0000, v4
	v_max_f32_e32 v1, v2, v1
	v_max_f32_e64 v2, |v66|, |v66|
	v_max_f32_e64 v3, |v65|, |v65|
	v_max3_f32 v1, |v59|, |v62|, v1
	v_max_f32_e32 v2, v3, v2
	v_lshlrev_b32_e32 v67, 16, v5
	v_and_b32_e32 v68, 0xffff0000, v5
	v_max3_f32 v0, v0, v1, v2
	v_max_f32_e64 v1, |v68|, |v68|
	v_max_f32_e64 v2, |v67|, |v67|
	v_lshlrev_b32_e32 v70, 16, v7
	v_and_b32_e32 v7, 0xffff0000, v7
	v_max_f32_e32 v1, v2, v1
	v_max_f32_e64 v2, |v7|, |v7|
	v_max_f32_e64 v3, |v70|, |v70|
	v_lshlrev_b32_e32 v69, 16, v6
	v_and_b32_e32 v6, 0xffff0000, v6
	v_max_f32_e32 v2, v3, v2
	v_max3_f32 v2, |v69|, |v6|, v2
	s_waitcnt vmcnt(4)
	v_lshlrev_b32_e32 v71, 16, v8
	v_and_b32_e32 v8, 0xffff0000, v8
	v_max3_f32 v0, v0, v1, v2
	v_max_f32_e64 v1, |v8|, |v8|
	v_max_f32_e64 v2, |v71|, |v71|
	v_lshlrev_b32_e32 v72, 16, v9
	v_and_b32_e32 v9, 0xffff0000, v9
	v_max_f32_e32 v1, v2, v1
	v_max_f32_e64 v2, |v9|, |v9|
	v_max_f32_e64 v3, |v72|, |v72|
	v_max_f32_e32 v2, v3, v2
	v_lshlrev_b32_e32 v74, 16, v11
	v_and_b32_e32 v11, 0xffff0000, v11
	v_max3_f32 v0, v0, v1, v2
	v_max_f32_e64 v1, |v11|, |v11|
	v_max_f32_e64 v2, |v74|, |v74|
	v_lshlrev_b32_e32 v73, 16, v10
	v_and_b32_e32 v10, 0xffff0000, v10
	v_max_f32_e32 v1, v2, v1
	v_max3_f32 v1, |v73|, |v10|, v1
	s_waitcnt vmcnt(3)
	v_lshlrev_b32_e32 v75, 16, v12
	v_and_b32_e32 v12, 0xffff0000, v12
	v_max_f32_e64 v2, |v12|, |v12|
	v_max_f32_e64 v3, |v75|, |v75|
	v_max_f32_e32 v2, v3, v2
	v_lshlrev_b32_e32 v76, 16, v13
	v_and_b32_e32 v13, 0xffff0000, v13
	v_max3_f32 v0, v0, v1, v2
	v_max_f32_e64 v1, |v13|, |v13|
	v_max_f32_e64 v2, |v76|, |v76|
	v_lshlrev_b32_e32 v78, 16, v15
	v_and_b32_e32 v15, 0xffff0000, v15
	v_max_f32_e32 v1, v2, v1
	v_max_f32_e64 v2, |v15|, |v15|
	v_max_f32_e64 v3, |v78|, |v78|
	v_lshlrev_b32_e32 v77, 16, v14
	v_and_b32_e32 v14, 0xffff0000, v14
	v_max_f32_e32 v2, v3, v2
	v_max3_f32 v2, |v77|, |v14|, v2
	v_max3_f32 v0, v0, v1, v2
	v_mov_b32_e32 v1, 0
	s_waitcnt vmcnt(2)
	v_add_f32_dpp v32, v32, v32 quad_perm:[1,0,3,2] row_mask:0xf bank_mask:0xf bound_ctrl:1
	v_mov_b32_e32 v152, 0
	v_mov_b32_dpp v1, v0 quad_perm:[1,0,3,2] row_mask:0xf bank_mask:0xf
	v_max_f32_e32 v1, v1, v1
	v_max_f32_e32 v0, v0, v1
	v_mov_b32_e32 v1, 0
	v_add_f32_dpp v32, v32, v32 quad_perm:[2,3,0,1] row_mask:0xf bank_mask:0xf bound_ctrl:1
	v_mov_b32_e32 v153, v109
	v_mov_b32_dpp v1, v0 quad_perm:[2,3,0,1] row_mask:0xf bank_mask:0xf
	v_max_f32_e32 v1, v1, v1
	v_max_f32_e32 v0, v0, v1
	v_mov_b32_e32 v1, 0
	v_add_f32_dpp v32, v32, v32 row_half_mirror row_mask:0xf bank_mask:0xf bound_ctrl:1
	v_mov_b32_e32 v154, 0
	v_mov_b32_dpp v1, v0 row_half_mirror row_mask:0xf bank_mask:0xf
	v_max_f32_e32 v1, v1, v1
	v_max_f32_e32 v0, v0, v1
	v_mov_b32_e32 v1, 0
	v_add_f32_dpp v32, v32, v32 row_mirror row_mask:0xf bank_mask:0xf bound_ctrl:1
	v_mov_b32_e32 v155, v109
	v_mov_b32_dpp v1, v0 row_mirror row_mask:0xf bank_mask:0xf
	v_max_f32_e32 v1, v1, v1
	v_max_f32_e32 v0, v0, v1
	v_readlane_b32 s39, v32, 0
	v_readlane_b32 s12, v0, 32
	v_readlane_b32 s13, v0, 48
	v_readlane_b32 s10, v0, 0
	v_readlane_b32 s11, v0, 16
	v_max_f32_e64 v0, s13, s13
	v_max_f32_e64 v1, s12, s12
	v_max_f32_e32 v0, v1, v0
	v_mov_b32_e32 v1, s11
	v_max3_f32 v163, s10, v1, v0
	v_div_scale_f32 v2, s[10:11], v163, v163, s29
	v_rcp_f32_e32 v3, v2
	v_lshl_add_u64 v[0:1], s[8:9], 0, v[18:19]
	s_lshl_b64 s[8:9], s[4:5], 8
	s_add_u32 s8, s22, s8
	v_fma_f32 v4, -v2, v3, 1.0
	v_fmac_f32_e32 v3, v4, v3
	v_div_scale_f32 v4, vcc, s29, v163, s29
	v_mul_f32_e32 v5, v4, v3
	v_fma_f32 v79, -v2, v5, v4
	v_fmac_f32_e32 v5, v79, v3
	v_fma_f32 v2, -v2, v5, v4
	v_div_fmas_f32 v2, v2, v3, v5
	v_div_fixup_f32 v2, v2, v163, s29
	v_cmp_lt_f32_e32 vcc, 0, v163
	s_addc_u32 s9, s23, s9
	s_lshl_b64 s[16:17], s[4:5], 9
	v_cndmask_b32_e32 v79, 0, v2, vcc
	v_mul_f32_e32 v3, v79, v57
	v_mul_f32_e32 v2, v79, v58
	v_rndne_f32_e32 v3, v3
	v_mul_f32_e32 v4, v79, v56
	v_mul_f32_e32 v5, v79, v55
	v_rndne_f32_e32 v2, v2
	v_cvt_i32_f32_e32 v3, v3
	v_rndne_f32_e32 v4, v4
	v_rndne_f32_e32 v5, v5
	v_mul_f32_e32 v53, v79, v53
	v_cvt_i32_f32_e32 v2, v2
	v_cvt_i32_f32_sdwa v4, v4 dst_sel:WORD_1 dst_unused:UNUSED_PAD src0_sel:DWORD
	v_cvt_i32_f32_e32 v5, v5
	v_mul_f32_e32 v54, v79, v54
	v_rndne_f32_e32 v53, v53
	v_mul_f32_e32 v52, v79, v52
	v_mul_f32_e32 v51, v79, v51
	v_rndne_f32_e32 v54, v54
	v_cvt_i32_f32_e32 v53, v53
	v_rndne_f32_e32 v52, v52
	v_rndne_f32_e32 v51, v51
	v_cvt_i32_f32_e32 v54, v54
	v_cvt_i32_f32_sdwa v52, v52 dst_sel:WORD_1 dst_unused:UNUSED_PAD src0_sel:DWORD
	v_cvt_i32_f32_e32 v51, v51
	v_lshlrev_b32_e32 v3, 8, v3
	v_and_b32_e32 v3, 0xff00, v3
	v_and_b32_e32 v4, 0xff0000, v4
	v_perm_b32 v2, v5, v2, s21
	v_or3_b32 v2, v2, v3, v4
	v_lshlrev_b32_e32 v3, 8, v53
	v_and_b32_e32 v3, 0xff00, v3
	v_and_b32_e32 v4, 0xff0000, v52
	v_perm_b32 v5, v51, v54, s21
	v_or3_b32 v3, v5, v3, v4
	v_mul_f32_e32 v5, v79, v45
	v_mul_f32_e32 v4, v79, v48
	v_rndne_f32_e32 v5, v5
	v_mul_f32_e32 v43, v79, v43
	v_mul_f32_e32 v41, v79, v41
	v_rndne_f32_e32 v4, v4
	v_cvt_i32_f32_e32 v5, v5
	v_rndne_f32_e32 v43, v43
	v_rndne_f32_e32 v41, v41
; #define LAS __attribute__((address_space(3)))
; __device__ __forceinline__ float bflo(unsigned w) { return __uint_as_float(w << 16); }
; __device__ __forceinline__ float bfhi(unsigned w) { return __uint_as_float(w & 0xffff0000u); }
; __device__ __forceinline__ void p12_peer(Frame& F) {
;     ...
;         for (int j = 0; j < 8; ++j) {
;             const int q0 = (int)rintf(bflo(xp[j].x) * inv), q1 = (int)rintf(bfhi(xp[j].x) * inv), q2 = (int)rintf(bflo(xp[j].y) * inv), q3 = (int)rintf(bfhi(xp[j].y) * inv);
;             const int q4 = (int)rintf(bflo(xp[j].z) * inv), q5 = (int)rintf(bfhi(xp[j].z) * inv), q6 = (int)rintf(bflo(xp[j].w) * inv), q7 = (int)rintf(bfhi(xp[j].w) * inv);
;             *(LAS v2u*)(XQ + i * 4096 + 8 * (F.lane + 64 * j)) = (v2u){(unsigned)((q0 & 0xff) | ((q1 & 0xff) << 8) | ((q2 & 0xff) << 16) | (q3 << 24)), (unsigned)((q4 & 0xff) | ((q5 & 0xff) << 8) | ((q6 & 0xff) << 16) | (q7 << 24))}; }
	v_mul_f32_e32 v39, v79, v39
	v_cvt_i32_f32_e32 v4, v4
	v_cvt_i32_f32_sdwa v43, v43 dst_sel:WORD_1 dst_unused:UNUSED_PAD src0_sel:DWORD
	v_cvt_i32_f32_e32 v41, v41
	v_mul_f32_e32 v40, v79, v40
	v_rndne_f32_e32 v39, v39
	v_mul_f32_e32 v38, v79, v38
	v_mul_f32_e32 v37, v79, v37
	v_rndne_f32_e32 v40, v40
	v_cvt_i32_f32_e32 v39, v39
	v_rndne_f32_e32 v38, v38
	v_rndne_f32_e32 v37, v37
	v_cvt_i32_f32_e32 v40, v40
	v_cvt_i32_f32_sdwa v38, v38 dst_sel:WORD_1 dst_unused:UNUSED_PAD src0_sel:DWORD
	v_cvt_i32_f32_e32 v37, v37
	v_lshlrev_b32_e32 v5, 8, v5
	v_and_b32_e32 v5, 0xff00, v5
	v_and_b32_e32 v43, 0xff0000, v43
	v_perm_b32 v4, v41, v4, s21
	v_or3_b32 v4, v4, v5, v43
	v_lshlrev_b32_e32 v5, 8, v39
	v_and_b32_e32 v5, 0xff00, v5
	v_and_b32_e32 v38, 0xff0000, v38
	v_perm_b32 v37, v37, v40, s21
	v_or3_b32 v5, v37, v5, v38
	ds_write2st64_b64 v25, v[2:3], v[4:5] offset1:1
	v_mul_f32_e32 v3, v79, v33
	v_mul_f32_e32 v2, v79, v34
	v_rndne_f32_e32 v3, v3
	v_mul_f32_e32 v4, v79, v31
	v_mul_f32_e32 v5, v79, v30
	v_rndne_f32_e32 v2, v2
	v_cvt_i32_f32_e32 v3, v3
	v_rndne_f32_e32 v4, v4
	v_rndne_f32_e32 v5, v5
	v_mul_f32_e32 v28, v79, v28
	v_cvt_i32_f32_e32 v2, v2
	v_cvt_i32_f32_sdwa v4, v4 dst_sel:WORD_1 dst_unused:UNUSED_PAD src0_sel:DWORD
	v_cvt_i32_f32_e32 v5, v5
	v_mul_f32_e32 v29, v79, v29
	v_rndne_f32_e32 v28, v28
	v_mul_f32_e32 v27, v79, v27
	v_mul_f32_e32 v26, v79, v26
	v_rndne_f32_e32 v29, v29
	v_cvt_i32_f32_e32 v28, v28
	v_rndne_f32_e32 v27, v27
	v_rndne_f32_e32 v26, v26
	v_cvt_i32_f32_e32 v29, v29
	v_cvt_i32_f32_sdwa v27, v27 dst_sel:WORD_1 dst_unused:UNUSED_PAD src0_sel:DWORD
	v_cvt_i32_f32_e32 v26, v26
	v_lshlrev_b32_e32 v3, 8, v3
	v_and_b32_e32 v3, 0xff00, v3
	v_and_b32_e32 v4, 0xff0000, v4
	v_perm_b32 v2, v5, v2, s21
	v_or3_b32 v2, v2, v3, v4
	v_lshlrev_b32_e32 v3, 8, v28
	v_and_b32_e32 v3, 0xff00, v3
	v_and_b32_e32 v4, 0xff0000, v27
	v_perm_b32 v5, v26, v29, s21
	v_or3_b32 v3, v5, v3, v4
	v_mul_f32_e32 v5, v79, v35
	v_mul_f32_e32 v4, v79, v36
	v_rndne_f32_e32 v5, v5
	v_mul_f32_e32 v26, v79, v50
	v_mul_f32_e32 v27, v79, v47
	v_rndne_f32_e32 v4, v4
	v_cvt_i32_f32_e32 v5, v5
	v_rndne_f32_e32 v26, v26
	v_rndne_f32_e32 v27, v27
	v_mul_f32_e32 v29, v79, v46
	v_cvt_i32_f32_e32 v4, v4
	v_cvt_i32_f32_sdwa v26, v26 dst_sel:WORD_1 dst_unused:UNUSED_PAD src0_sel:DWORD
	v_cvt_i32_f32_e32 v27, v27
	v_mul_f32_e32 v28, v79, v49
	v_rndne_f32_e32 v29, v29
	v_mul_f32_e32 v30, v79, v44
	v_mul_f32_e32 v31, v79, v42
	v_rndne_f32_e32 v28, v28
	v_cvt_i32_f32_e32 v29, v29
	v_rndne_f32_e32 v30, v30
	v_rndne_f32_e32 v31, v31
	v_cvt_i32_f32_e32 v28, v28
	v_cvt_i32_f32_sdwa v30, v30 dst_sel:WORD_1 dst_unused:UNUSED_PAD src0_sel:DWORD
	v_cvt_i32_f32_e32 v31, v31
	v_lshlrev_b32_e32 v5, 8, v5
	v_and_b32_e32 v5, 0xff00, v5
	v_and_b32_e32 v26, 0xff0000, v26
	v_perm_b32 v4, v27, v4, s21
	v_or3_b32 v4, v4, v5, v26
	v_lshlrev_b32_e32 v5, 8, v29
	v_and_b32_e32 v5, 0xff00, v5
	v_and_b32_e32 v26, 0xff0000, v30
	v_perm_b32 v27, v31, v28, s21
	v_or3_b32 v5, v27, v5, v26
	ds_write2st64_b64 v25, v[2:3], v[4:5] offset0:2 offset1:3
	v_mul_f32_e32 v3, v79, v21
	v_mul_f32_e32 v2, v79, v20
	v_rndne_f32_e32 v3, v3
	v_mul_f32_e32 v4, v79, v22
	v_mul_f32_e32 v5, v79, v23
	v_rndne_f32_e32 v2, v2
	v_cvt_i32_f32_e32 v3, v3
	v_rndne_f32_e32 v4, v4
	v_rndne_f32_e32 v5, v5
	v_mul_f32_e32 v21, v79, v62
	v_cvt_i32_f32_e32 v2, v2
	v_cvt_i32_f32_sdwa v4, v4 dst_sel:WORD_1 dst_unused:UNUSED_PAD src0_sel:DWORD
	v_cvt_i32_f32_e32 v5, v5
	v_mul_f32_e32 v20, v79, v59
	v_rndne_f32_e32 v21, v21
	v_mul_f32_e32 v22, v79, v63
	v_mul_f32_e32 v23, v79, v64
	v_rndne_f32_e32 v20, v20
	v_cvt_i32_f32_e32 v21, v21
	v_rndne_f32_e32 v22, v22
	v_rndne_f32_e32 v23, v23
	v_cvt_i32_f32_e32 v20, v20
	v_cvt_i32_f32_sdwa v22, v22 dst_sel:WORD_1 dst_unused:UNUSED_PAD src0_sel:DWORD
	v_cvt_i32_f32_e32 v23, v23
	v_lshlrev_b32_e32 v3, 8, v3
	v_and_b32_e32 v3, 0xff00, v3
	v_and_b32_e32 v4, 0xff0000, v4
	v_perm_b32 v2, v5, v2, s21
	v_or3_b32 v2, v2, v3, v4
	v_lshlrev_b32_e32 v3, 8, v21
	v_and_b32_e32 v3, 0xff00, v3
	v_and_b32_e32 v4, 0xff0000, v22
	v_perm_b32 v5, v23, v20, s21
	v_or3_b32 v3, v5, v3, v4
	v_mul_f32_e32 v5, v79, v66
	v_mul_f32_e32 v4, v79, v65
	v_rndne_f32_e32 v5, v5
	v_mul_f32_e32 v20, v79, v67
	v_mul_f32_e32 v21, v79, v68
	v_rndne_f32_e32 v4, v4
	v_cvt_i32_f32_e32 v5, v5
	v_rndne_f32_e32 v20, v20
	v_rndne_f32_e32 v21, v21
	v_mul_f32_e32 v6, v79, v6
	v_cvt_i32_f32_e32 v4, v4
	v_cvt_i32_f32_sdwa v20, v20 dst_sel:WORD_1 dst_unused:UNUSED_PAD src0_sel:DWORD
	v_cvt_i32_f32_e32 v21, v21
	v_mul_f32_e32 v22, v79, v69
	v_rndne_f32_e32 v6, v6
	v_mul_f32_e32 v23, v79, v70
	v_mul_f32_e32 v7, v79, v7
	v_rndne_f32_e32 v22, v22
	v_cvt_i32_f32_e32 v6, v6
	v_rndne_f32_e32 v23, v23
	v_rndne_f32_e32 v7, v7
	v_cvt_i32_f32_e32 v22, v22
	v_cvt_i32_f32_sdwa v23, v23 dst_sel:WORD_1 dst_unused:UNUSED_PAD src0_sel:DWORD
	v_cvt_i32_f32_e32 v7, v7
	v_lshlrev_b32_e32 v5, 8, v5
	v_and_b32_e32 v5, 0xff00, v5
	v_and_b32_e32 v20, 0xff0000, v20
	v_perm_b32 v4, v21, v4, s21
	v_or3_b32 v4, v4, v5, v20
	v_lshlrev_b32_e32 v5, 8, v6
	v_and_b32_e32 v5, 0xff00, v5
	v_and_b32_e32 v6, 0xff0000, v23
	v_perm_b32 v7, v7, v22, s21
	v_or3_b32 v5, v7, v5, v6
	ds_write2st64_b64 v25, v[2:3], v[4:5] offset0:4 offset1:5
	v_mul_f32_e32 v3, v79, v8
	v_mul_f32_e32 v2, v79, v71
	v_rndne_f32_e32 v3, v3
	v_mul_f32_e32 v4, v79, v72
	v_mul_f32_e32 v5, v79, v9
	v_rndne_f32_e32 v2, v2
	v_cvt_i32_f32_e32 v3, v3
	v_rndne_f32_e32 v4, v4
	v_rndne_f32_e32 v5, v5
	v_mul_f32_e32 v7, v79, v10
	v_cvt_i32_f32_e32 v2, v2
	v_cvt_i32_f32_sdwa v4, v4 dst_sel:WORD_1 dst_unused:UNUSED_PAD src0_sel:DWORD
	v_cvt_i32_f32_e32 v5, v5
	v_mul_f32_e32 v6, v79, v73
	v_rndne_f32_e32 v7, v7
; #define LAS __attribute__((address_space(3)))
; #define LDS_WAIT() asm volatile("s_waitcnt lgkmcnt(0)" ::: "memory")
; __device__ __forceinline__ float bflo(unsigned w) { return __uint_as_float(w << 16); }
; __device__ __forceinline__ float bfhi(unsigned w) { return __uint_as_float(w & 0xffff0000u); }
; __device__ __forceinline__ float wave_sum(float v) { v = dpp_add16(v); return (rdlane(v, 0) + rdlane(v, 16)) + (rdlane(v, 32) + rdlane(v, 48)); }
; __device__ __forceinline__ void p12_peer(Frame& F) {
;     ...
;         const int t = F.gw + i * F.NGW; v4u xp[8]; float mxa = 0.f;
; #pragma unroll
;         for (int j = 0; j < 8; ++j) { xp[j] = ((const v4u*)(HN + (size_t)t * D_))[F.lane + 64 * j];
;             mxa = fmaxf(fmaxf(fmaxf(mxa, fmaxf(fabsf(bflo(xp[j].x)), fabsf(bfhi(xp[j].x)))), fmaxf(fabsf(bflo(xp[j].y)), fabsf(bfhi(xp[j].y)))), fmaxf(fmaxf(fabsf(bflo(xp[j].z)), fabsf(bfhi(xp[j].z))), fmaxf(fabsf(bflo(xp[j].w)), fabsf(bfhi(xp[j].w))))); }
;         mxa = wave_max(mxa); const float inv = mxa > 0.f ? 127.0f / mxa : 0.f;
;         const float rsn = 1.0f / sqrtf(wave_sum(PSQ[(size_t)t * 64 + F.lane]) * (1.f / D_) + 1e-6f);
;         sx[i] = mxa * rsn * (1.0f / 127.0f);
; #pragma unroll
;         for (int j = 0; j < 8; ++j) {
;             const int q0 = (int)rintf(bflo(xp[j].x) * inv), q1 = (int)rintf(bfhi(xp[j].x) * inv), q2 = (int)rintf(bflo(xp[j].y) * inv), q3 = (int)rintf(bfhi(xp[j].y) * inv);
;             const int q4 = (int)rintf(bflo(xp[j].z) * inv), q5 = (int)rintf(bfhi(xp[j].z) * inv), q6 = (int)rintf(bflo(xp[j].w) * inv), q7 = (int)rintf(bfhi(xp[j].w) * inv);
;             *(LAS v2u*)(XQ + i * 4096 + 8 * (F.lane + 64 * j)) = (v2u){(unsigned)((q0 & 0xff) | ((q1 & 0xff) << 8) | ((q2 & 0xff) << 16) | (q3 << 24)), (unsigned)((q4 & 0xff) | ((q5 & 0xff) << 8) | ((q6 & 0xff) << 16) | (q7 << 24))}; }
;         EL[i * 128 + F.lane] = (unsigned short)PIDX[(size_t)t * 128 + F.lane]; EL[i * 128 + 64 + F.lane] = (unsigned short)PIDX[(size_t)t * 128 + 64 + F.lane];
;         asm volatile("" ::: "memory");
;     }
;     LDS_WAIT(); asm volatile("" ::: "memory");
;     float psum[4][16];
; #pragma unroll
;     for (int i = 0; i < 4; ++i)
; #pragma unroll
;         for (int b = 0; b < 16; ++b) psum[i][b] = 0.f;
	v_mul_f32_e32 v8, v79, v74
	v_mul_f32_e32 v9, v79, v11
	v_rndne_f32_e32 v6, v6
	v_cvt_i32_f32_e32 v7, v7
	v_rndne_f32_e32 v8, v8
	v_rndne_f32_e32 v9, v9
	v_cvt_i32_f32_e32 v6, v6
	v_cvt_i32_f32_sdwa v8, v8 dst_sel:WORD_1 dst_unused:UNUSED_PAD src0_sel:DWORD
	v_cvt_i32_f32_e32 v9, v9
	v_lshlrev_b32_e32 v3, 8, v3
	v_and_b32_e32 v3, 0xff00, v3
	v_and_b32_e32 v4, 0xff0000, v4
	v_perm_b32 v2, v5, v2, s21
	v_or3_b32 v2, v2, v3, v4
	v_lshlrev_b32_e32 v3, 8, v7
	v_and_b32_e32 v3, 0xff00, v3
	v_and_b32_e32 v4, 0xff0000, v8
	v_perm_b32 v5, v9, v6, s21
	v_or3_b32 v3, v5, v3, v4
	v_mul_f32_e32 v5, v79, v12
	v_mul_f32_e32 v4, v79, v75
	v_rndne_f32_e32 v5, v5
	v_mul_f32_e32 v6, v79, v76
	v_mul_f32_e32 v7, v79, v13
	v_rndne_f32_e32 v4, v4
	v_cvt_i32_f32_e32 v5, v5
	v_rndne_f32_e32 v6, v6
	v_rndne_f32_e32 v7, v7
	v_mul_f32_e32 v9, v79, v14
	v_cvt_i32_f32_e32 v4, v4
	v_cvt_i32_f32_sdwa v6, v6 dst_sel:WORD_1 dst_unused:UNUSED_PAD src0_sel:DWORD
	v_cvt_i32_f32_e32 v7, v7
	v_mul_f32_e32 v8, v79, v77
	v_rndne_f32_e32 v9, v9
	v_mul_f32_e32 v10, v79, v78
	v_mul_f32_e32 v11, v79, v15
	v_rndne_f32_e32 v8, v8
	v_cvt_i32_f32_e32 v9, v9
	v_rndne_f32_e32 v10, v10
	v_rndne_f32_e32 v11, v11
	v_cvt_i32_f32_e32 v8, v8
	v_cvt_i32_f32_sdwa v10, v10 dst_sel:WORD_1 dst_unused:UNUSED_PAD src0_sel:DWORD
	v_cvt_i32_f32_e32 v11, v11
	v_lshlrev_b32_e32 v5, 8, v5
	v_and_b32_e32 v5, 0xff00, v5
	v_and_b32_e32 v6, 0xff0000, v6
	v_perm_b32 v4, v7, v4, s21
	v_or3_b32 v4, v4, v5, v6
	v_lshlrev_b32_e32 v5, 8, v9
	v_and_b32_e32 v5, 0xff00, v5
	v_and_b32_e32 v6, 0xff0000, v10
	v_perm_b32 v7, v11, v8, s21
	v_or3_b32 v5, v7, v5, v6
	ds_write2st64_b64 v25, v[2:3], v[4:5] offset0:6 offset1:7
	s_waitcnt vmcnt(1)
	ds_write_b16 v24, v60 offset:16384
	s_waitcnt vmcnt(0)
	ds_write_b16 v24, v61 offset:16512
	global_load_dwordx4 v[4:7], v[0:1], off
	global_load_dwordx4 v[8:11], v[0:1], off offset:1024
	global_load_dwordx4 v[12:15], v[0:1], off offset:2048
	global_load_dwordx4 v[60:63], v[0:1], off offset:3072
	v_add_co_u32_e32 v56, vcc, s28, v0
	v_lshl_add_u64 v[20:21], s[8:9], 0, v[16:17]
	s_nop 0
	v_addc_co_u32_e32 v57, vcc, 0, v1, vcc
	s_add_u32 s8, s18, s16
	s_addc_u32 s9, s19, s17
	v_lshl_add_u64 v[22:23], s[8:9], 0, v[16:17]
	s_add_i32 s8, s4, s34
	s_ashr_i32 s9, s8, 31
	s_lshl_b64 s[10:11], s[8:9], 13
	s_add_u32 s10, s6, s10
	s_addc_u32 s11, s7, s11
	v_readlane_b32 s41, v32, 16
	v_readlane_b32 s40, v32, 32
	v_readlane_b32 s42, v32, 48
	v_mov_b32_e32 v156, 0
	v_mov_b32_e32 v157, v109
	v_mov_b32_e32 v158, 0
	v_mov_b32_e32 v159, v109
	v_mov_b32_e32 v106, 0
	v_mov_b32_e32 v107, v109
	v_mov_b32_e32 v104, 0
	v_mov_b32_e32 v105, v109
	v_mov_b32_e32 v102, 0
	v_mov_b32_e32 v103, v109
	v_mov_b32_e32 v100, 0
	v_mov_b32_e32 v101, v109
	v_mov_b32_e32 v98, 0
	v_mov_b32_e32 v99, v109
	v_mov_b32_e32 v96, 0
	v_mov_b32_e32 v97, v109
	s_waitcnt vmcnt(3)
	v_lshlrev_b32_e32 v27, 16, v4
	v_and_b32_e32 v26, 0xffff0000, v4
	v_max_f32_e64 v2, |v26|, |v26|
	v_max_f32_e64 v3, |v27|, |v27|
	v_max_f32_e32 v4, v3, v2
	global_load_dwordx4 v[0:3], v[56:57], off
	v_lshlrev_b32_e32 v41, 16, v5
	v_and_b32_e32 v38, 0xffff0000, v5
	v_max_f32_e64 v5, |v38|, |v38|
	v_max_f32_e64 v28, |v41|, |v41|
	v_max_f32_e32 v5, v28, v5
	v_lshlrev_b32_e32 v36, 16, v7
	v_and_b32_e32 v34, 0xffff0000, v7
	v_max3_f32 v30, v4, 0, v5
	v_max_f32_e64 v4, |v34|, |v34|
	v_max_f32_e64 v5, |v36|, |v36|
	v_lshlrev_b32_e32 v42, 16, v6
	v_and_b32_e32 v39, 0xffff0000, v6
	v_max_f32_e32 v4, v5, v4
	v_max3_f32 v31, |v42|, |v39|, v4
	s_waitcnt vmcnt(3)
	v_lshlrev_b32_e32 v29, 16, v8
	v_and_b32_e32 v28, 0xffff0000, v8
	global_load_dwordx4 v[4:7], v[56:57], off offset:1024
	v_max_f32_e64 v8, |v28|, |v28|
	v_max_f32_e64 v33, |v29|, |v29|
	v_max_f32_e32 v8, v33, v8
	v_lshlrev_b32_e32 v48, 16, v9
	v_and_b32_e32 v45, 0xffff0000, v9
	v_lshlrev_b32_e32 v43, 16, v11
	v_and_b32_e32 v40, 0xffff0000, v11
	v_max3_f32 v8, v30, v31, v8
	v_max_f32_e64 v9, |v45|, |v45|
	v_max_f32_e64 v30, |v48|, |v48|
	v_lshlrev_b32_e32 v46, 16, v10
	v_and_b32_e32 v44, 0xffff0000, v10
	v_max_f32_e64 v10, |v40|, |v40|
	v_max_f32_e64 v11, |v43|, |v43|
	v_max_f32_e32 v9, v30, v9
	v_max_f32_e32 v10, v11, v10
	s_waitcnt vmcnt(3)
	v_lshlrev_b32_e32 v31, 16, v12
	v_and_b32_e32 v30, 0xffff0000, v12
	v_max3_f32 v10, |v46|, |v44|, v10
	v_max_f32_e64 v12, |v30|, |v30|
	v_max_f32_e64 v35, |v31|, |v31|
	v_lshlrev_b32_e32 v53, 16, v13
	v_and_b32_e32 v50, 0xffff0000, v13
	v_max3_f32 v33, v8, v9, v10
	global_load_dwordx4 v[8:11], v[56:57], off offset:2048
	v_max_f32_e32 v12, v35, v12
	v_max_f32_e64 v13, |v50|, |v50|
	v_max_f32_e64 v35, |v53|, |v53|
	v_max_f32_e32 v13, v35, v13
	v_lshlrev_b32_e32 v49, 16, v15
	v_and_b32_e32 v47, 0xffff0000, v15
	v_max3_f32 v33, v33, v12, v13
	v_max_f32_e64 v12, |v47|, |v47|
	v_max_f32_e64 v13, |v49|, |v49|
	v_lshlrev_b32_e32 v54, 16, v14
	v_and_b32_e32 v51, 0xffff0000, v14
	v_max_f32_e32 v12, v13, v12
	v_max3_f32 v52, |v54|, |v51|, v12
	global_load_dwordx4 v[12:15], v[56:57], off offset:3072
	s_waitcnt vmcnt(4)
	v_lshlrev_b32_e32 v37, 16, v60
	v_and_b32_e32 v35, 0xffff0000, v60
	v_max_f32_e64 v55, |v35|, |v35|
	v_max_f32_e64 v56, |v37|, |v37|
	v_max_f32_e32 v55, v56, v55
	v_lshlrev_b32_e32 v59, 16, v61
	v_and_b32_e32 v57, 0xffff0000, v61
	v_max3_f32 v33, v33, v52, v55
	v_max_f32_e64 v52, |v57|, |v57|
	v_max_f32_e64 v55, |v59|, |v59|
	v_max_f32_e32 v60, v55, v52
	v_lshlrev_b32_e32 v55, 16, v63
	v_and_b32_e32 v52, 0xffff0000, v63
	v_lshlrev_b32_e32 v58, 16, v62
	v_and_b32_e32 v56, 0xffff0000, v62
	v_max_f32_e64 v61, |v52|, |v52|
	v_max_f32_e64 v62, |v55|, |v55|
	v_max_f32_e32 v61, v62, v61
	v_max3_f32 v61, |v58|, |v56|, v61
	v_max3_f32 v60, v33, v60, v61
	global_load_dword v33, v[20:21], off
	global_load_dword v61, v[22:23], off
	global_load_dword v62, v[22:23], off offset:256
	s_waitcnt vmcnt(6)
; #define LAS __attribute__((address_space(3)))
; __device__ __forceinline__ float bflo(unsigned w) { return __uint_as_float(w << 16); }
; __device__ __forceinline__ float bfhi(unsigned w) { return __uint_as_float(w & 0xffff0000u); }
; __device__ __forceinline__ float wave_sum(float v) { v = dpp_add16(v); return (rdlane(v, 0) + rdlane(v, 16)) + (rdlane(v, 32) + rdlane(v, 48)); }
; __device__ __forceinline__ float wave_max(float v) { v = dpp_max16(v); return fmaxf(fmaxf(rdlane(v, 0), rdlane(v, 16)), fmaxf(rdlane(v, 32), rdlane(v, 48))); }
; __device__ __forceinline__ void p12_peer(Frame& F) {
;     ...
;         const int t = F.gw + i * F.NGW; v4u xp[8]; float mxa = 0.f;
; #pragma unroll
;         for (int j = 0; j < 8; ++j) { xp[j] = ((const v4u*)(HN + (size_t)t * D_))[F.lane + 64 * j];
;             mxa = fmaxf(fmaxf(fmaxf(mxa, fmaxf(fabsf(bflo(xp[j].x)), fabsf(bfhi(xp[j].x)))), fmaxf(fabsf(bflo(xp[j].y)), fabsf(bfhi(xp[j].y)))), fmaxf(fmaxf(fabsf(bflo(xp[j].z)), fabsf(bfhi(xp[j].z))), fmaxf(fabsf(bflo(xp[j].w)), fabsf(bfhi(xp[j].w))))); }
;         mxa = wave_max(mxa); const float inv = mxa > 0.f ? 127.0f / mxa : 0.f;
;         const float rsn = 1.0f / sqrtf(wave_sum(PSQ[(size_t)t * 64 + F.lane]) * (1.f / D_) + 1e-6f);
;         sx[i] = mxa * rsn * (1.0f / 127.0f);
; #pragma unroll
;         for (int j = 0; j < 8; ++j) {
;             const int q0 = (int)rintf(bflo(xp[j].x) * inv), q1 = (int)rintf(bfhi(xp[j].x) * inv), q2 = (int)rintf(bflo(xp[j].y) * inv), q3 = (int)rintf(bfhi(xp[j].y) * inv);
;             const int q4 = (int)rintf(bflo(xp[j].z) * inv), q5 = (int)rintf(bfhi(xp[j].z) * inv), q6 = (int)rintf(bflo(xp[j].w) * inv), q7 = (int)rintf(bfhi(xp[j].w) * inv);
;             *(LAS v2u*)(XQ + i * 4096 + 8 * (F.lane + 64 * j)) = (v2u){(unsigned)((q0 & 0xff) | ((q1 & 0xff) << 8) | ((q2 & 0xff) << 16) | (q3 << 24)), (unsigned)((q4 & 0xff) | ((q5 & 0xff) << 8) | ((q6 & 0xff) << 16) | (q7 << 24))}; }
	v_lshlrev_b32_e32 v20, 16, v0
	v_and_b32_e32 v21, 0xffff0000, v0
	v_max_f32_e64 v0, |v21|, |v21|
	v_max_f32_e64 v22, |v20|, |v20|
	v_max_f32_e32 v0, v22, v0
	v_lshlrev_b32_e32 v22, 16, v1
	v_and_b32_e32 v23, 0xffff0000, v1
	v_max_f32_e64 v1, |v23|, |v23|
	v_max_f32_e64 v63, |v22|, |v22|
	v_max_f32_e32 v1, v63, v1
	v_lshlrev_b32_e32 v64, 16, v3
	v_and_b32_e32 v65, 0xffff0000, v3
	v_max3_f32 v0, v60, v0, v1
	v_lshlrev_b32_e32 v60, 16, v2
	v_and_b32_e32 v63, 0xffff0000, v2
	v_max_f32_e64 v1, |v65|, |v65|
	v_max_f32_e64 v2, |v64|, |v64|
	s_waitcnt vmcnt(5)
	v_lshlrev_b32_e32 v66, 16, v4
	v_and_b32_e32 v67, 0xffff0000, v4
	v_max_f32_e32 v1, v2, v1
	v_max_f32_e64 v2, |v67|, |v67|
	v_max_f32_e64 v3, |v66|, |v66|
	v_max3_f32 v1, |v60|, |v63|, v1
	v_max_f32_e32 v2, v3, v2
	v_lshlrev_b32_e32 v68, 16, v5
	v_and_b32_e32 v69, 0xffff0000, v5
	v_max3_f32 v0, v0, v1, v2
	v_max_f32_e64 v1, |v69|, |v69|
	v_max_f32_e64 v2, |v68|, |v68|
	v_lshlrev_b32_e32 v71, 16, v7
	v_and_b32_e32 v7, 0xffff0000, v7
	v_max_f32_e32 v1, v2, v1
	v_max_f32_e64 v2, |v7|, |v7|
	v_max_f32_e64 v3, |v71|, |v71|
	v_lshlrev_b32_e32 v70, 16, v6
	v_and_b32_e32 v6, 0xffff0000, v6
	v_max_f32_e32 v2, v3, v2
	v_max3_f32 v2, |v70|, |v6|, v2
	v_max3_f32 v0, v0, v1, v2
	s_waitcnt vmcnt(4)
	v_lshlrev_b32_e32 v72, 16, v8
	v_and_b32_e32 v8, 0xffff0000, v8
	v_max_f32_e64 v1, |v8|, |v8|
	v_max_f32_e64 v2, |v72|, |v72|
	v_lshlrev_b32_e32 v73, 16, v9
	v_and_b32_e32 v9, 0xffff0000, v9
	v_max_f32_e32 v1, v2, v1
	v_max_f32_e64 v2, |v9|, |v9|
	v_max_f32_e64 v3, |v73|, |v73|
	v_max_f32_e32 v2, v3, v2
	v_lshlrev_b32_e32 v75, 16, v11
	v_and_b32_e32 v11, 0xffff0000, v11
	v_max3_f32 v0, v0, v1, v2
	v_max_f32_e64 v1, |v11|, |v11|
	v_max_f32_e64 v2, |v75|, |v75|
	s_waitcnt vmcnt(3)
	v_lshlrev_b32_e32 v76, 16, v12
	v_and_b32_e32 v12, 0xffff0000, v12
	v_lshlrev_b32_e32 v74, 16, v10
	v_and_b32_e32 v10, 0xffff0000, v10
	v_max_f32_e32 v1, v2, v1
	v_max_f32_e64 v2, |v12|, |v12|
	v_max_f32_e64 v3, |v76|, |v76|
	v_max3_f32 v1, |v74|, |v10|, v1
	v_max_f32_e32 v2, v3, v2
	v_lshlrev_b32_e32 v77, 16, v13
	v_and_b32_e32 v13, 0xffff0000, v13
	v_max3_f32 v0, v0, v1, v2
	v_max_f32_e64 v1, |v13|, |v13|
	v_max_f32_e64 v2, |v77|, |v77|
	v_lshlrev_b32_e32 v79, 16, v15
	v_and_b32_e32 v15, 0xffff0000, v15
	v_max_f32_e32 v1, v2, v1
	v_max_f32_e64 v2, |v15|, |v15|
	v_max_f32_e64 v3, |v79|, |v79|
	v_lshlrev_b32_e32 v78, 16, v14
	v_and_b32_e32 v14, 0xffff0000, v14
	v_max_f32_e32 v2, v3, v2
	v_max3_f32 v2, |v78|, |v14|, v2
	v_max3_f32 v0, v0, v1, v2
	v_mov_b32_e32 v1, 0
	s_waitcnt vmcnt(2)
	v_add_f32_dpp v32, v33, v33 quad_perm:[1,0,3,2] row_mask:0xf bank_mask:0xf bound_ctrl:1
	v_mov_b32_dpp v1, v0 quad_perm:[1,0,3,2] row_mask:0xf bank_mask:0xf
	v_max_f32_e32 v1, v1, v1
	v_max_f32_e32 v0, v0, v1
	v_mov_b32_e32 v1, 0
	v_add_f32_dpp v32, v32, v32 quad_perm:[2,3,0,1] row_mask:0xf bank_mask:0xf bound_ctrl:1
	s_nop 0
	v_mov_b32_dpp v1, v0 quad_perm:[2,3,0,1] row_mask:0xf bank_mask:0xf
	v_max_f32_e32 v1, v1, v1
	v_max_f32_e32 v0, v0, v1
	v_mov_b32_e32 v1, 0
	v_add_f32_dpp v32, v32, v32 row_half_mirror row_mask:0xf bank_mask:0xf bound_ctrl:1
	s_nop 0
	v_mov_b32_dpp v1, v0 row_half_mirror row_mask:0xf bank_mask:0xf
	v_max_f32_e32 v1, v1, v1
	v_max_f32_e32 v0, v0, v1
	v_mov_b32_e32 v1, 0
	v_add_f32_dpp v32, v32, v32 row_mirror row_mask:0xf bank_mask:0xf bound_ctrl:1
	s_nop 0
	v_mov_b32_dpp v1, v0 row_mirror row_mask:0xf bank_mask:0xf
	v_max_f32_e32 v1, v1, v1
	v_max_f32_e32 v0, v0, v1
	v_readlane_b32 s37, v32, 16
	v_readlane_b32 s14, v0, 32
	v_readlane_b32 s15, v0, 48
	v_readlane_b32 s12, v0, 0
	v_readlane_b32 s13, v0, 16
	v_max_f32_e64 v0, s15, s15
	v_max_f32_e64 v1, s14, s14
	v_max_f32_e32 v0, v1, v0
	v_mov_b32_e32 v1, s13
	v_max3_f32 v162, s12, v1, v0
	v_div_scale_f32 v2, s[12:13], v162, v162, s29
	v_rcp_f32_e32 v3, v2
	v_lshl_add_u64 v[0:1], s[10:11], 0, v[18:19]
	s_lshl_b64 s[10:11], s[8:9], 8
	s_add_u32 s10, s22, s10
	v_fma_f32 v4, -v2, v3, 1.0
	v_fmac_f32_e32 v3, v4, v3
	v_div_scale_f32 v4, vcc, s29, v162, s29
	v_mul_f32_e32 v5, v4, v3
	v_fma_f32 v80, -v2, v5, v4
	v_fmac_f32_e32 v5, v80, v3
	v_fma_f32 v2, -v2, v5, v4
	v_div_fmas_f32 v2, v2, v3, v5
	v_div_fixup_f32 v2, v2, v162, s29
	v_cmp_lt_f32_e32 vcc, 0, v162
	s_addc_u32 s11, s23, s11
	s_lshl_b64 s[14:15], s[8:9], 9
	v_cndmask_b32_e32 v80, 0, v2, vcc
	v_mul_f32_e32 v3, v80, v26
	v_mul_f32_e32 v2, v80, v27
	v_rndne_f32_e32 v3, v3
	v_mul_f32_e32 v4, v80, v41
	v_mul_f32_e32 v5, v80, v38
	v_rndne_f32_e32 v2, v2
	v_cvt_i32_f32_e32 v3, v3
	v_rndne_f32_e32 v4, v4
	v_rndne_f32_e32 v5, v5
	v_mul_f32_e32 v27, v80, v39
	v_cvt_i32_f32_e32 v2, v2
	v_cvt_i32_f32_sdwa v4, v4 dst_sel:WORD_1 dst_unused:UNUSED_PAD src0_sel:DWORD
	v_cvt_i32_f32_e32 v5, v5
	v_mul_f32_e32 v26, v80, v42
	v_rndne_f32_e32 v27, v27
	v_mul_f32_e32 v36, v80, v36
	v_mul_f32_e32 v34, v80, v34
	v_rndne_f32_e32 v26, v26
	v_cvt_i32_f32_e32 v27, v27
	v_rndne_f32_e32 v36, v36
	v_rndne_f32_e32 v34, v34
	v_cvt_i32_f32_e32 v26, v26
	v_cvt_i32_f32_sdwa v36, v36 dst_sel:WORD_1 dst_unused:UNUSED_PAD src0_sel:DWORD
	v_cvt_i32_f32_e32 v34, v34
	v_lshlrev_b32_e32 v3, 8, v3
	v_and_b32_e32 v3, 0xff00, v3
	v_and_b32_e32 v4, 0xff0000, v4
	v_perm_b32 v2, v5, v2, s21
	v_or3_b32 v2, v2, v3, v4
	v_lshlrev_b32_e32 v3, 8, v27
	v_and_b32_e32 v3, 0xff00, v3
	v_and_b32_e32 v4, 0xff0000, v36
	v_perm_b32 v5, v34, v26, s21
	v_or3_b32 v3, v5, v3, v4
	v_mul_f32_e32 v5, v80, v28
	v_mul_f32_e32 v4, v80, v29
	v_rndne_f32_e32 v5, v5
	v_mul_f32_e32 v26, v80, v48
	v_mul_f32_e32 v27, v80, v45
	v_rndne_f32_e32 v4, v4
	v_cvt_i32_f32_e32 v5, v5
	v_rndne_f32_e32 v26, v26
	v_rndne_f32_e32 v27, v27
	v_mul_f32_e32 v29, v80, v44
	v_cvt_i32_f32_e32 v4, v4
; #define LAS __attribute__((address_space(3)))
; __device__ __forceinline__ float bflo(unsigned w) { return __uint_as_float(w << 16); }
; __device__ __forceinline__ float bfhi(unsigned w) { return __uint_as_float(w & 0xffff0000u); }
; __device__ __forceinline__ void p12_peer(Frame& F) {
;     ...
;         for (int j = 0; j < 8; ++j) {
;             const int q0 = (int)rintf(bflo(xp[j].x) * inv), q1 = (int)rintf(bfhi(xp[j].x) * inv), q2 = (int)rintf(bflo(xp[j].y) * inv), q3 = (int)rintf(bfhi(xp[j].y) * inv);
;             const int q4 = (int)rintf(bflo(xp[j].z) * inv), q5 = (int)rintf(bfhi(xp[j].z) * inv), q6 = (int)rintf(bflo(xp[j].w) * inv), q7 = (int)rintf(bfhi(xp[j].w) * inv);
;             *(LAS v2u*)(XQ + i * 4096 + 8 * (F.lane + 64 * j)) = (v2u){(unsigned)((q0 & 0xff) | ((q1 & 0xff) << 8) | ((q2 & 0xff) << 16) | (q3 << 24)), (unsigned)((q4 & 0xff) | ((q5 & 0xff) << 8) | ((q6 & 0xff) << 16) | (q7 << 24))}; }
	v_cvt_i32_f32_sdwa v26, v26 dst_sel:WORD_1 dst_unused:UNUSED_PAD src0_sel:DWORD
	v_cvt_i32_f32_e32 v27, v27
	v_mul_f32_e32 v28, v80, v46
	v_rndne_f32_e32 v29, v29
	v_mul_f32_e32 v34, v80, v43
	v_mul_f32_e32 v36, v80, v40
	v_rndne_f32_e32 v28, v28
	v_cvt_i32_f32_e32 v29, v29
	v_rndne_f32_e32 v34, v34
	v_rndne_f32_e32 v36, v36
	v_cvt_i32_f32_e32 v28, v28
	v_cvt_i32_f32_sdwa v34, v34 dst_sel:WORD_1 dst_unused:UNUSED_PAD src0_sel:DWORD
	v_cvt_i32_f32_e32 v36, v36
	v_lshlrev_b32_e32 v5, 8, v5
	v_and_b32_e32 v5, 0xff00, v5
	v_and_b32_e32 v26, 0xff0000, v26
	v_perm_b32 v4, v27, v4, s21
	v_or3_b32 v4, v4, v5, v26
	v_lshlrev_b32_e32 v5, 8, v29
	v_and_b32_e32 v5, 0xff00, v5
	v_and_b32_e32 v26, 0xff0000, v34
	v_perm_b32 v27, v36, v28, s21
	v_or3_b32 v5, v27, v5, v26
	ds_write2st64_b64 v25, v[2:3], v[4:5] offset0:8 offset1:9
	v_mul_f32_e32 v3, v80, v30
	v_mul_f32_e32 v2, v80, v31
	v_rndne_f32_e32 v3, v3
	v_mul_f32_e32 v4, v80, v53
	v_mul_f32_e32 v5, v80, v50
	v_rndne_f32_e32 v2, v2
	v_cvt_i32_f32_e32 v3, v3
	v_rndne_f32_e32 v4, v4
	v_rndne_f32_e32 v5, v5
	v_mul_f32_e32 v27, v80, v51
	v_cvt_i32_f32_e32 v2, v2
	v_cvt_i32_f32_sdwa v4, v4 dst_sel:WORD_1 dst_unused:UNUSED_PAD src0_sel:DWORD
	v_cvt_i32_f32_e32 v5, v5
	v_mul_f32_e32 v26, v80, v54
	v_rndne_f32_e32 v27, v27
	v_mul_f32_e32 v28, v80, v49
	v_mul_f32_e32 v29, v80, v47
	v_rndne_f32_e32 v26, v26
	v_cvt_i32_f32_e32 v27, v27
	v_rndne_f32_e32 v28, v28
	v_rndne_f32_e32 v29, v29
	v_cvt_i32_f32_e32 v26, v26
	v_cvt_i32_f32_sdwa v28, v28 dst_sel:WORD_1 dst_unused:UNUSED_PAD src0_sel:DWORD
	v_cvt_i32_f32_e32 v29, v29
	v_lshlrev_b32_e32 v3, 8, v3
	v_and_b32_e32 v3, 0xff00, v3
	v_and_b32_e32 v4, 0xff0000, v4
	v_perm_b32 v2, v5, v2, s21
	v_or3_b32 v2, v2, v3, v4
	v_lshlrev_b32_e32 v3, 8, v27
	v_and_b32_e32 v3, 0xff00, v3
	v_and_b32_e32 v4, 0xff0000, v28
	v_perm_b32 v5, v29, v26, s21
	v_or3_b32 v3, v5, v3, v4
	v_mul_f32_e32 v5, v80, v35
	v_mul_f32_e32 v4, v80, v37
	v_rndne_f32_e32 v5, v5
	v_mul_f32_e32 v26, v80, v59
	v_mul_f32_e32 v27, v80, v57
	v_rndne_f32_e32 v4, v4
	v_cvt_i32_f32_e32 v5, v5
	v_rndne_f32_e32 v26, v26
	v_rndne_f32_e32 v27, v27
	v_mul_f32_e32 v29, v80, v56
	v_cvt_i32_f32_e32 v4, v4
	v_cvt_i32_f32_sdwa v26, v26 dst_sel:WORD_1 dst_unused:UNUSED_PAD src0_sel:DWORD
	v_cvt_i32_f32_e32 v27, v27
	v_mul_f32_e32 v28, v80, v58
	v_rndne_f32_e32 v29, v29
	v_mul_f32_e32 v30, v80, v55
	v_mul_f32_e32 v31, v80, v52
	v_rndne_f32_e32 v28, v28
	v_cvt_i32_f32_e32 v29, v29
	v_rndne_f32_e32 v30, v30
	v_rndne_f32_e32 v31, v31
	v_cvt_i32_f32_e32 v28, v28
	v_cvt_i32_f32_sdwa v30, v30 dst_sel:WORD_1 dst_unused:UNUSED_PAD src0_sel:DWORD
	v_cvt_i32_f32_e32 v31, v31
	v_lshlrev_b32_e32 v5, 8, v5
	v_and_b32_e32 v5, 0xff00, v5
	v_and_b32_e32 v26, 0xff0000, v26
	v_perm_b32 v4, v27, v4, s21
	v_or3_b32 v4, v4, v5, v26
	v_lshlrev_b32_e32 v5, 8, v29
	v_and_b32_e32 v5, 0xff00, v5
	v_and_b32_e32 v26, 0xff0000, v30
	v_perm_b32 v27, v31, v28, s21
	v_or3_b32 v5, v27, v5, v26
	ds_write2st64_b64 v25, v[2:3], v[4:5] offset0:10 offset1:11
	v_mul_f32_e32 v3, v80, v21
	v_mul_f32_e32 v2, v80, v20
	v_rndne_f32_e32 v3, v3
	v_mul_f32_e32 v4, v80, v22
	v_mul_f32_e32 v5, v80, v23
	v_rndne_f32_e32 v2, v2
	v_cvt_i32_f32_e32 v3, v3
	v_rndne_f32_e32 v4, v4
	v_rndne_f32_e32 v5, v5
	v_mul_f32_e32 v21, v80, v63
	v_cvt_i32_f32_e32 v2, v2
	v_cvt_i32_f32_sdwa v4, v4 dst_sel:WORD_1 dst_unused:UNUSED_PAD src0_sel:DWORD
	v_cvt_i32_f32_e32 v5, v5
	v_mul_f32_e32 v20, v80, v60
	v_rndne_f32_e32 v21, v21
	v_mul_f32_e32 v22, v80, v64
	v_mul_f32_e32 v23, v80, v65
	v_rndne_f32_e32 v20, v20
	v_cvt_i32_f32_e32 v21, v21
	v_rndne_f32_e32 v22, v22
	v_rndne_f32_e32 v23, v23
	v_cvt_i32_f32_e32 v20, v20
	v_cvt_i32_f32_sdwa v22, v22 dst_sel:WORD_1 dst_unused:UNUSED_PAD src0_sel:DWORD
	v_cvt_i32_f32_e32 v23, v23
	v_lshlrev_b32_e32 v3, 8, v3
	v_and_b32_e32 v3, 0xff00, v3
	v_and_b32_e32 v4, 0xff0000, v4
	v_perm_b32 v2, v5, v2, s21
	v_or3_b32 v2, v2, v3, v4
	v_lshlrev_b32_e32 v3, 8, v21
	v_and_b32_e32 v3, 0xff00, v3
	v_and_b32_e32 v4, 0xff0000, v22
	v_perm_b32 v5, v23, v20, s21
	v_or3_b32 v3, v5, v3, v4
	v_mul_f32_e32 v5, v80, v67
	v_mul_f32_e32 v4, v80, v66
	v_rndne_f32_e32 v5, v5
	v_mul_f32_e32 v20, v80, v68
	v_mul_f32_e32 v21, v80, v69
	v_rndne_f32_e32 v4, v4
	v_cvt_i32_f32_e32 v5, v5
	v_rndne_f32_e32 v20, v20
	v_rndne_f32_e32 v21, v21
	v_mul_f32_e32 v6, v80, v6
	v_cvt_i32_f32_e32 v4, v4
	v_cvt_i32_f32_sdwa v20, v20 dst_sel:WORD_1 dst_unused:UNUSED_PAD src0_sel:DWORD
	v_cvt_i32_f32_e32 v21, v21
	v_mul_f32_e32 v22, v80, v70
	v_rndne_f32_e32 v6, v6
	v_mul_f32_e32 v23, v80, v71
	v_mul_f32_e32 v7, v80, v7
	v_rndne_f32_e32 v22, v22
	v_cvt_i32_f32_e32 v6, v6
	v_rndne_f32_e32 v23, v23
	v_rndne_f32_e32 v7, v7
	v_cvt_i32_f32_e32 v22, v22
	v_cvt_i32_f32_sdwa v23, v23 dst_sel:WORD_1 dst_unused:UNUSED_PAD src0_sel:DWORD
	v_cvt_i32_f32_e32 v7, v7
	v_lshlrev_b32_e32 v5, 8, v5
	v_and_b32_e32 v5, 0xff00, v5
	v_and_b32_e32 v20, 0xff0000, v20
	v_perm_b32 v4, v21, v4, s21
	v_or3_b32 v4, v4, v5, v20
	v_lshlrev_b32_e32 v5, 8, v6
	v_and_b32_e32 v5, 0xff00, v5
	v_and_b32_e32 v6, 0xff0000, v23
	v_perm_b32 v7, v7, v22, s21
	v_or3_b32 v5, v7, v5, v6
	ds_write2st64_b64 v25, v[2:3], v[4:5] offset0:12 offset1:13
	v_mul_f32_e32 v3, v80, v8
	v_mul_f32_e32 v2, v80, v72
	v_rndne_f32_e32 v3, v3
	v_mul_f32_e32 v4, v80, v73
	v_mul_f32_e32 v5, v80, v9
	v_rndne_f32_e32 v2, v2
	v_cvt_i32_f32_e32 v3, v3
	v_rndne_f32_e32 v4, v4
	v_rndne_f32_e32 v5, v5
	v_mul_f32_e32 v7, v80, v10
	v_cvt_i32_f32_e32 v2, v2
	v_cvt_i32_f32_sdwa v4, v4 dst_sel:WORD_1 dst_unused:UNUSED_PAD src0_sel:DWORD
	v_cvt_i32_f32_e32 v5, v5
	v_mul_f32_e32 v6, v80, v74
	v_rndne_f32_e32 v7, v7
	v_mul_f32_e32 v8, v80, v75
	v_mul_f32_e32 v9, v80, v11
; #define LAS __attribute__((address_space(3)))
; __device__ __forceinline__ float bflo(unsigned w) { return __uint_as_float(w << 16); }
; __device__ __forceinline__ float bfhi(unsigned w) { return __uint_as_float(w & 0xffff0000u); }
; __device__ __forceinline__ float wave_sum(float v) { v = dpp_add16(v); return (rdlane(v, 0) + rdlane(v, 16)) + (rdlane(v, 32) + rdlane(v, 48)); }
; __device__ __forceinline__ float wave_max(float v) { v = dpp_max16(v); return fmaxf(fmaxf(rdlane(v, 0), rdlane(v, 16)), fmaxf(rdlane(v, 32), rdlane(v, 48))); }
; __device__ __forceinline__ void p12_peer(Frame& F) {
;     ...
;         const int t = F.gw + i * F.NGW; v4u xp[8]; float mxa = 0.f;
; #pragma unroll
;         for (int j = 0; j < 8; ++j) { xp[j] = ((const v4u*)(HN + (size_t)t * D_))[F.lane + 64 * j];
;             mxa = fmaxf(fmaxf(fmaxf(mxa, fmaxf(fabsf(bflo(xp[j].x)), fabsf(bfhi(xp[j].x)))), fmaxf(fabsf(bflo(xp[j].y)), fabsf(bfhi(xp[j].y)))), fmaxf(fmaxf(fabsf(bflo(xp[j].z)), fabsf(bfhi(xp[j].z))), fmaxf(fabsf(bflo(xp[j].w)), fabsf(bfhi(xp[j].w))))); }
;         mxa = wave_max(mxa); const float inv = mxa > 0.f ? 127.0f / mxa : 0.f;
;         const float rsn = 1.0f / sqrtf(wave_sum(PSQ[(size_t)t * 64 + F.lane]) * (1.f / D_) + 1e-6f);
;         sx[i] = mxa * rsn * (1.0f / 127.0f);
; #pragma unroll
;         for (int j = 0; j < 8; ++j) {
;             const int q0 = (int)rintf(bflo(xp[j].x) * inv), q1 = (int)rintf(bfhi(xp[j].x) * inv), q2 = (int)rintf(bflo(xp[j].y) * inv), q3 = (int)rintf(bfhi(xp[j].y) * inv);
;             const int q4 = (int)rintf(bflo(xp[j].z) * inv), q5 = (int)rintf(bfhi(xp[j].z) * inv), q6 = (int)rintf(bflo(xp[j].w) * inv), q7 = (int)rintf(bfhi(xp[j].w) * inv);
;             *(LAS v2u*)(XQ + i * 4096 + 8 * (F.lane + 64 * j)) = (v2u){(unsigned)((q0 & 0xff) | ((q1 & 0xff) << 8) | ((q2 & 0xff) << 16) | (q3 << 24)), (unsigned)((q4 & 0xff) | ((q5 & 0xff) << 8) | ((q6 & 0xff) << 16) | (q7 << 24))}; }
;         EL[i * 128 + F.lane] = (unsigned short)PIDX[(size_t)t * 128 + F.lane]; EL[i * 128 + 64 + F.lane] = (unsigned short)PIDX[(size_t)t * 128 + 64 + F.lane];
	v_rndne_f32_e32 v6, v6
	v_cvt_i32_f32_e32 v7, v7
	v_rndne_f32_e32 v8, v8
	v_rndne_f32_e32 v9, v9
	v_cvt_i32_f32_e32 v6, v6
	v_cvt_i32_f32_sdwa v8, v8 dst_sel:WORD_1 dst_unused:UNUSED_PAD src0_sel:DWORD
	v_cvt_i32_f32_e32 v9, v9
	v_lshlrev_b32_e32 v3, 8, v3
	v_and_b32_e32 v3, 0xff00, v3
	v_and_b32_e32 v4, 0xff0000, v4
	v_perm_b32 v2, v5, v2, s21
	v_or3_b32 v2, v2, v3, v4
	v_lshlrev_b32_e32 v3, 8, v7
	v_and_b32_e32 v3, 0xff00, v3
	v_and_b32_e32 v4, 0xff0000, v8
	v_perm_b32 v5, v9, v6, s21
	v_or3_b32 v3, v5, v3, v4
	v_mul_f32_e32 v5, v80, v12
	v_mul_f32_e32 v4, v80, v76
	v_rndne_f32_e32 v5, v5
	v_mul_f32_e32 v6, v80, v77
	v_mul_f32_e32 v7, v80, v13
	v_rndne_f32_e32 v4, v4
	v_cvt_i32_f32_e32 v5, v5
	v_rndne_f32_e32 v6, v6
	v_rndne_f32_e32 v7, v7
	v_mul_f32_e32 v9, v80, v14
	v_cvt_i32_f32_e32 v4, v4
	v_cvt_i32_f32_sdwa v6, v6 dst_sel:WORD_1 dst_unused:UNUSED_PAD src0_sel:DWORD
	v_cvt_i32_f32_e32 v7, v7
	v_mul_f32_e32 v8, v80, v78
	v_rndne_f32_e32 v9, v9
	v_mul_f32_e32 v10, v80, v79
	v_mul_f32_e32 v11, v80, v15
	v_rndne_f32_e32 v8, v8
	v_cvt_i32_f32_e32 v9, v9
	v_rndne_f32_e32 v10, v10
	v_rndne_f32_e32 v11, v11
	v_cvt_i32_f32_e32 v8, v8
	v_cvt_i32_f32_sdwa v10, v10 dst_sel:WORD_1 dst_unused:UNUSED_PAD src0_sel:DWORD
	v_cvt_i32_f32_e32 v11, v11
	v_lshlrev_b32_e32 v5, 8, v5
	v_and_b32_e32 v5, 0xff00, v5
	v_and_b32_e32 v6, 0xff0000, v6
	v_perm_b32 v4, v7, v4, s21
	v_or3_b32 v4, v4, v5, v6
	v_lshlrev_b32_e32 v5, 8, v9
	v_and_b32_e32 v5, 0xff00, v5
	v_and_b32_e32 v6, 0xff0000, v10
	v_perm_b32 v7, v11, v8, s21
	v_or3_b32 v5, v7, v5, v6
	ds_write2st64_b64 v25, v[2:3], v[4:5] offset0:14 offset1:15
	s_waitcnt vmcnt(1)
	ds_write_b16 v24, v61 offset:16640
	s_waitcnt vmcnt(0)
	ds_write_b16 v24, v62 offset:16768
	global_load_dwordx4 v[4:7], v[0:1], off
	global_load_dwordx4 v[8:11], v[0:1], off offset:1024
	global_load_dwordx4 v[12:15], v[0:1], off offset:2048
	global_load_dwordx4 v[60:63], v[0:1], off offset:3072
	v_add_co_u32_e32 v56, vcc, s28, v0
	v_lshl_add_u64 v[20:21], s[10:11], 0, v[16:17]
	s_nop 0
	v_addc_co_u32_e32 v57, vcc, 0, v1, vcc
	s_add_u32 s10, s18, s14
	s_addc_u32 s11, s19, s15
	v_lshl_add_u64 v[22:23], s[10:11], 0, v[16:17]
	s_add_i32 s10, s8, s34
	s_ashr_i32 s11, s10, 31
	s_lshl_b64 s[12:13], s[10:11], 13
	s_add_u32 s12, s6, s12
	s_addc_u32 s13, s7, s13
	v_readlane_b32 s36, v32, 32
	v_readlane_b32 s38, v32, 48
	s_waitcnt vmcnt(3)
	v_lshlrev_b32_e32 v27, 16, v4
	v_and_b32_e32 v26, 0xffff0000, v4
	v_max_f32_e64 v2, |v26|, |v26|
	v_max_f32_e64 v3, |v27|, |v27|
	v_max_f32_e32 v4, v3, v2
	global_load_dwordx4 v[0:3], v[56:57], off
	v_lshlrev_b32_e32 v42, 16, v5
	v_and_b32_e32 v39, 0xffff0000, v5
	v_max_f32_e64 v5, |v39|, |v39|
	v_max_f32_e64 v28, |v42|, |v42|
	v_max_f32_e32 v5, v28, v5
	v_lshlrev_b32_e32 v37, 16, v7
	v_and_b32_e32 v35, 0xffff0000, v7
	v_max3_f32 v30, v4, 0, v5
	v_max_f32_e64 v4, |v35|, |v35|
	v_max_f32_e64 v5, |v37|, |v37|
	v_lshlrev_b32_e32 v43, 16, v6
	v_and_b32_e32 v40, 0xffff0000, v6
	v_max_f32_e32 v4, v5, v4
	v_max3_f32 v31, |v43|, |v40|, v4
	s_waitcnt vmcnt(3)
	v_lshlrev_b32_e32 v29, 16, v8
	v_and_b32_e32 v28, 0xffff0000, v8
	global_load_dwordx4 v[4:7], v[56:57], off offset:1024
	v_max_f32_e64 v8, |v28|, |v28|
	v_max_f32_e64 v34, |v29|, |v29|
	v_max_f32_e32 v8, v34, v8
	v_lshlrev_b32_e32 v49, 16, v9
	v_and_b32_e32 v46, 0xffff0000, v9
	v_lshlrev_b32_e32 v44, 16, v11
	v_and_b32_e32 v41, 0xffff0000, v11
	v_max3_f32 v8, v30, v31, v8
	v_max_f32_e64 v9, |v46|, |v46|
	v_max_f32_e64 v30, |v49|, |v49|
	v_lshlrev_b32_e32 v47, 16, v10
	v_and_b32_e32 v45, 0xffff0000, v10
	v_max_f32_e64 v10, |v41|, |v41|
	v_max_f32_e64 v11, |v44|, |v44|
	v_max_f32_e32 v9, v30, v9
	v_max_f32_e32 v10, v11, v10
	s_waitcnt vmcnt(3)
	v_lshlrev_b32_e32 v31, 16, v12
	v_and_b32_e32 v30, 0xffff0000, v12
	v_max3_f32 v10, |v47|, |v45|, v10
	v_max_f32_e64 v12, |v30|, |v30|
	v_max_f32_e64 v36, |v31|, |v31|
	v_lshlrev_b32_e32 v54, 16, v13
	v_and_b32_e32 v51, 0xffff0000, v13
	v_max3_f32 v34, v8, v9, v10
	global_load_dwordx4 v[8:11], v[56:57], off offset:2048
	v_max_f32_e32 v12, v36, v12
	v_max_f32_e64 v13, |v51|, |v51|
	v_max_f32_e64 v36, |v54|, |v54|
	v_max_f32_e32 v13, v36, v13
	v_lshlrev_b32_e32 v50, 16, v15
	v_and_b32_e32 v48, 0xffff0000, v15
	v_max3_f32 v34, v34, v12, v13
	v_max_f32_e64 v12, |v48|, |v48|
	v_max_f32_e64 v13, |v50|, |v50|
	v_lshlrev_b32_e32 v55, 16, v14
	v_and_b32_e32 v52, 0xffff0000, v14
	v_max_f32_e32 v12, v13, v12
	v_max3_f32 v53, |v55|, |v52|, v12
	global_load_dwordx4 v[12:15], v[56:57], off offset:3072
	s_waitcnt vmcnt(4)
	v_lshlrev_b32_e32 v38, 16, v60
	v_and_b32_e32 v36, 0xffff0000, v60
	v_max_f32_e64 v56, |v36|, |v36|
	v_max_f32_e64 v57, |v38|, |v38|
	v_max_f32_e32 v56, v57, v56
	v_lshlrev_b32_e32 v60, 16, v61
	v_and_b32_e32 v58, 0xffff0000, v61
	v_max3_f32 v34, v34, v53, v56
	v_max_f32_e64 v53, |v58|, |v58|
	v_max_f32_e64 v56, |v60|, |v60|
	v_max_f32_e32 v61, v56, v53
	v_lshlrev_b32_e32 v56, 16, v63
	v_and_b32_e32 v53, 0xffff0000, v63
	v_lshlrev_b32_e32 v59, 16, v62
	v_and_b32_e32 v57, 0xffff0000, v62
	v_max_f32_e64 v62, |v53|, |v53|
	v_max_f32_e64 v63, |v56|, |v56|
	v_max_f32_e32 v62, v63, v62
	v_max3_f32 v62, |v59|, |v57|, v62
	v_max3_f32 v61, v34, v61, v62
	global_load_dword v34, v[20:21], off
	global_load_dword v62, v[22:23], off
	global_load_dword v63, v[22:23], off offset:256
	s_waitcnt vmcnt(6)
	v_lshlrev_b32_e32 v20, 16, v0
	v_and_b32_e32 v21, 0xffff0000, v0
	v_max_f32_e64 v0, |v21|, |v21|
	v_max_f32_e64 v22, |v20|, |v20|
	v_max_f32_e32 v0, v22, v0
	v_lshlrev_b32_e32 v22, 16, v1
	v_and_b32_e32 v23, 0xffff0000, v1
	v_max_f32_e64 v1, |v23|, |v23|
	v_max_f32_e64 v64, |v22|, |v22|
	v_max_f32_e32 v1, v64, v1
	v_lshlrev_b32_e32 v65, 16, v3
	v_and_b32_e32 v66, 0xffff0000, v3
	v_max3_f32 v0, v61, v0, v1
	v_lshlrev_b32_e32 v61, 16, v2
	v_and_b32_e32 v64, 0xffff0000, v2
	v_max_f32_e64 v1, |v66|, |v66|
	v_max_f32_e64 v2, |v65|, |v65|
	s_waitcnt vmcnt(5)
; #define LAS __attribute__((address_space(3)))
; __device__ __forceinline__ float bflo(unsigned w) { return __uint_as_float(w << 16); }
; __device__ __forceinline__ float bfhi(unsigned w) { return __uint_as_float(w & 0xffff0000u); }
; __device__ __forceinline__ float wave_sum(float v) { v = dpp_add16(v); return (rdlane(v, 0) + rdlane(v, 16)) + (rdlane(v, 32) + rdlane(v, 48)); }
; __device__ __forceinline__ float wave_max(float v) { v = dpp_max16(v); return fmaxf(fmaxf(rdlane(v, 0), rdlane(v, 16)), fmaxf(rdlane(v, 32), rdlane(v, 48))); }
; __device__ __forceinline__ void p12_peer(Frame& F) {
;     ...
;             mxa = fmaxf(fmaxf(fmaxf(mxa, fmaxf(fabsf(bflo(xp[j].x)), fabsf(bfhi(xp[j].x)))), fmaxf(fabsf(bflo(xp[j].y)), fabsf(bfhi(xp[j].y)))), fmaxf(fmaxf(fabsf(bflo(xp[j].z)), fabsf(bfhi(xp[j].z))), fmaxf(fabsf(bflo(xp[j].w)), fabsf(bfhi(xp[j].w))))); }
;         mxa = wave_max(mxa); const float inv = mxa > 0.f ? 127.0f / mxa : 0.f;
;         const float rsn = 1.0f / sqrtf(wave_sum(PSQ[(size_t)t * 64 + F.lane]) * (1.f / D_) + 1e-6f);
;         sx[i] = mxa * rsn * (1.0f / 127.0f);
; #pragma unroll
;         for (int j = 0; j < 8; ++j) {
;             const int q0 = (int)rintf(bflo(xp[j].x) * inv), q1 = (int)rintf(bfhi(xp[j].x) * inv), q2 = (int)rintf(bflo(xp[j].y) * inv), q3 = (int)rintf(bfhi(xp[j].y) * inv);
;             const int q4 = (int)rintf(bflo(xp[j].z) * inv), q5 = (int)rintf(bfhi(xp[j].z) * inv), q6 = (int)rintf(bflo(xp[j].w) * inv), q7 = (int)rintf(bfhi(xp[j].w) * inv);
;             *(LAS v2u*)(XQ + i * 4096 + 8 * (F.lane + 64 * j)) = (v2u){(unsigned)((q0 & 0xff) | ((q1 & 0xff) << 8) | ((q2 & 0xff) << 16) | (q3 << 24)), (unsigned)((q4 & 0xff) | ((q5 & 0xff) << 8) | ((q6 & 0xff) << 16) | (q7 << 24))}; }
	v_lshlrev_b32_e32 v67, 16, v4
	v_and_b32_e32 v68, 0xffff0000, v4
	v_max_f32_e32 v1, v2, v1
	v_max_f32_e64 v2, |v68|, |v68|
	v_max_f32_e64 v3, |v67|, |v67|
	v_max3_f32 v1, |v61|, |v64|, v1
	v_max_f32_e32 v2, v3, v2
	v_lshlrev_b32_e32 v69, 16, v5
	v_and_b32_e32 v70, 0xffff0000, v5
	v_max3_f32 v0, v0, v1, v2
	v_max_f32_e64 v1, |v70|, |v70|
	v_max_f32_e64 v2, |v69|, |v69|
	v_lshlrev_b32_e32 v72, 16, v7
	v_and_b32_e32 v7, 0xffff0000, v7
	v_max_f32_e32 v1, v2, v1
	v_max_f32_e64 v2, |v7|, |v7|
	v_max_f32_e64 v3, |v72|, |v72|
	v_lshlrev_b32_e32 v71, 16, v6
	v_and_b32_e32 v6, 0xffff0000, v6
	v_max_f32_e32 v2, v3, v2
	v_max3_f32 v2, |v71|, |v6|, v2
	v_max3_f32 v0, v0, v1, v2
	s_waitcnt vmcnt(4)
	v_lshlrev_b32_e32 v73, 16, v8
	v_and_b32_e32 v8, 0xffff0000, v8
	v_max_f32_e64 v1, |v8|, |v8|
	v_max_f32_e64 v2, |v73|, |v73|
	v_lshlrev_b32_e32 v74, 16, v9
	v_and_b32_e32 v9, 0xffff0000, v9
	v_max_f32_e32 v1, v2, v1
	v_max_f32_e64 v2, |v9|, |v9|
	v_max_f32_e64 v3, |v74|, |v74|
	v_max_f32_e32 v2, v3, v2
	v_lshlrev_b32_e32 v76, 16, v11
	v_and_b32_e32 v11, 0xffff0000, v11
	v_max3_f32 v0, v0, v1, v2
	v_max_f32_e64 v1, |v11|, |v11|
	v_max_f32_e64 v2, |v76|, |v76|
	s_waitcnt vmcnt(3)
	v_lshlrev_b32_e32 v77, 16, v12
	v_and_b32_e32 v12, 0xffff0000, v12
	v_lshlrev_b32_e32 v75, 16, v10
	v_and_b32_e32 v10, 0xffff0000, v10
	v_max_f32_e32 v1, v2, v1
	v_max_f32_e64 v2, |v12|, |v12|
	v_max_f32_e64 v3, |v77|, |v77|
	v_max3_f32 v1, |v75|, |v10|, v1
	v_max_f32_e32 v2, v3, v2
	v_lshlrev_b32_e32 v78, 16, v13
	v_and_b32_e32 v13, 0xffff0000, v13
	v_max3_f32 v0, v0, v1, v2
	v_max_f32_e64 v1, |v13|, |v13|
	v_max_f32_e64 v2, |v78|, |v78|
	v_lshlrev_b32_e32 v80, 16, v15
	v_and_b32_e32 v15, 0xffff0000, v15
	v_max_f32_e32 v1, v2, v1
	v_max_f32_e64 v2, |v15|, |v15|
	v_max_f32_e64 v3, |v80|, |v80|
	v_lshlrev_b32_e32 v79, 16, v14
	v_and_b32_e32 v14, 0xffff0000, v14
	v_max_f32_e32 v2, v3, v2
	v_max3_f32 v2, |v79|, |v14|, v2
	v_max3_f32 v0, v0, v1, v2
	v_mov_b32_e32 v1, 0
	s_nop 1
	v_mov_b32_dpp v1, v0 quad_perm:[1,0,3,2] row_mask:0xf bank_mask:0xf
	v_max_f32_e32 v1, v1, v1
	v_max_f32_e32 v0, v0, v1
	v_mov_b32_e32 v1, 0
	s_nop 1
	v_mov_b32_dpp v1, v0 quad_perm:[2,3,0,1] row_mask:0xf bank_mask:0xf
	v_max_f32_e32 v1, v1, v1
	v_max_f32_e32 v0, v0, v1
	v_mov_b32_e32 v1, 0
	s_nop 1
	v_mov_b32_dpp v1, v0 row_half_mirror row_mask:0xf bank_mask:0xf
	v_max_f32_e32 v1, v1, v1
	v_max_f32_e32 v0, v0, v1
	v_mov_b32_e32 v1, 0
	s_nop 1
	v_mov_b32_dpp v1, v0 row_mirror row_mask:0xf bank_mask:0xf
	v_max_f32_e32 v1, v1, v1
	v_max_f32_e32 v0, v0, v1
	s_nop 0
	v_readlane_b32 s33, v0, 32
	v_readlane_b32 s35, v0, 48
	v_readlane_b32 s30, v0, 0
	v_readlane_b32 s31, v0, 16
	v_max_f32_e64 v0, s35, s35
	v_max_f32_e64 v1, s33, s33
	v_max_f32_e32 v0, v1, v0
	v_mov_b32_e32 v1, s31
	v_max3_f32 v161, s30, v1, v0
	v_div_scale_f32 v2, s[30:31], v161, v161, s29
	v_rcp_f32_e32 v3, v2
	v_lshl_add_u64 v[0:1], s[12:13], 0, v[18:19]
	s_lshl_b64 s[12:13], s[10:11], 8
	s_add_u32 s12, s22, s12
	v_fma_f32 v4, -v2, v3, 1.0
	v_fmac_f32_e32 v3, v4, v3
	v_div_scale_f32 v4, vcc, s29, v161, s29
	v_mul_f32_e32 v5, v4, v3
	v_fma_f32 v18, -v2, v5, v4
	v_fmac_f32_e32 v5, v18, v3
	v_fma_f32 v2, -v2, v5, v4
	v_div_fmas_f32 v2, v2, v3, v5
	v_div_fixup_f32 v2, v2, v161, s29
	v_cmp_lt_f32_e32 vcc, 0, v161
	s_addc_u32 s13, s23, s13
	v_readlane_b32 s35, v32, 0
	v_cndmask_b32_e32 v18, 0, v2, vcc
	v_mul_f32_e32 v3, v18, v26
	v_mul_f32_e32 v2, v18, v27
	v_rndne_f32_e32 v3, v3
	v_mul_f32_e32 v4, v18, v42
	v_mul_f32_e32 v5, v18, v39
	v_rndne_f32_e32 v2, v2
	v_cvt_i32_f32_e32 v3, v3
	v_rndne_f32_e32 v4, v4
	v_rndne_f32_e32 v5, v5
	v_mul_f32_e32 v26, v18, v40
	v_cvt_i32_f32_e32 v2, v2
	v_cvt_i32_f32_sdwa v4, v4 dst_sel:WORD_1 dst_unused:UNUSED_PAD src0_sel:DWORD
	v_cvt_i32_f32_e32 v5, v5
	v_mul_f32_e32 v19, v18, v43
	v_rndne_f32_e32 v26, v26
	v_mul_f32_e32 v27, v18, v37
	v_mul_f32_e32 v35, v18, v35
	v_rndne_f32_e32 v19, v19
	v_cvt_i32_f32_e32 v26, v26
	v_rndne_f32_e32 v27, v27
	v_rndne_f32_e32 v35, v35
	v_cvt_i32_f32_e32 v19, v19
	v_cvt_i32_f32_sdwa v27, v27 dst_sel:WORD_1 dst_unused:UNUSED_PAD src0_sel:DWORD
	v_cvt_i32_f32_e32 v35, v35
	v_lshlrev_b32_e32 v3, 8, v3
	v_and_b32_e32 v3, 0xff00, v3
	v_and_b32_e32 v4, 0xff0000, v4
	v_perm_b32 v2, v5, v2, s21
	v_or3_b32 v2, v2, v3, v4
	v_lshlrev_b32_e32 v3, 8, v26
	v_and_b32_e32 v3, 0xff00, v3
	v_and_b32_e32 v4, 0xff0000, v27
	v_perm_b32 v5, v35, v19, s21
	v_or3_b32 v3, v5, v3, v4
	v_mul_f32_e32 v5, v18, v28
	v_mul_f32_e32 v4, v18, v29
	v_rndne_f32_e32 v5, v5
	v_mul_f32_e32 v19, v18, v49
	v_mul_f32_e32 v26, v18, v46
	v_rndne_f32_e32 v4, v4
	v_cvt_i32_f32_e32 v5, v5
	v_rndne_f32_e32 v19, v19
	v_rndne_f32_e32 v26, v26
	v_mul_f32_e32 v28, v18, v45
	v_cvt_i32_f32_e32 v4, v4
	v_cvt_i32_f32_sdwa v19, v19 dst_sel:WORD_1 dst_unused:UNUSED_PAD src0_sel:DWORD
	v_cvt_i32_f32_e32 v26, v26
	v_mul_f32_e32 v27, v18, v47
	v_rndne_f32_e32 v28, v28
	v_mul_f32_e32 v29, v18, v44
	v_mul_f32_e32 v35, v18, v41
	v_rndne_f32_e32 v27, v27
	v_cvt_i32_f32_e32 v28, v28
	v_rndne_f32_e32 v29, v29
	v_rndne_f32_e32 v35, v35
	v_cvt_i32_f32_e32 v27, v27
	v_cvt_i32_f32_sdwa v29, v29 dst_sel:WORD_1 dst_unused:UNUSED_PAD src0_sel:DWORD
	v_cvt_i32_f32_e32 v35, v35
	v_lshlrev_b32_e32 v5, 8, v5
	v_and_b32_e32 v5, 0xff00, v5
	v_and_b32_e32 v19, 0xff0000, v19
	v_perm_b32 v4, v26, v4, s21
	v_or3_b32 v4, v4, v5, v19
	v_lshlrev_b32_e32 v5, 8, v28
	v_and_b32_e32 v5, 0xff00, v5
	v_and_b32_e32 v19, 0xff0000, v29
	v_perm_b32 v26, v35, v27, s21
	v_or3_b32 v5, v26, v5, v19
	ds_write2st64_b64 v25, v[2:3], v[4:5] offset0:16 offset1:17
	v_mul_f32_e32 v3, v18, v30
	v_mul_f32_e32 v2, v18, v31
	v_rndne_f32_e32 v3, v3
	v_mul_f32_e32 v4, v18, v54
	v_mul_f32_e32 v5, v18, v51
; #define LAS __attribute__((address_space(3)))
; __device__ __forceinline__ float bflo(unsigned w) { return __uint_as_float(w << 16); }
; __device__ __forceinline__ float bfhi(unsigned w) { return __uint_as_float(w & 0xffff0000u); }
; __device__ __forceinline__ void p12_peer(Frame& F) {
;     ...
;         for (int j = 0; j < 8; ++j) {
;             const int q0 = (int)rintf(bflo(xp[j].x) * inv), q1 = (int)rintf(bfhi(xp[j].x) * inv), q2 = (int)rintf(bflo(xp[j].y) * inv), q3 = (int)rintf(bfhi(xp[j].y) * inv);
;             const int q4 = (int)rintf(bflo(xp[j].z) * inv), q5 = (int)rintf(bfhi(xp[j].z) * inv), q6 = (int)rintf(bflo(xp[j].w) * inv), q7 = (int)rintf(bfhi(xp[j].w) * inv);
;             *(LAS v2u*)(XQ + i * 4096 + 8 * (F.lane + 64 * j)) = (v2u){(unsigned)((q0 & 0xff) | ((q1 & 0xff) << 8) | ((q2 & 0xff) << 16) | (q3 << 24)), (unsigned)((q4 & 0xff) | ((q5 & 0xff) << 8) | ((q6 & 0xff) << 16) | (q7 << 24))}; }
;         EL[i * 128 + F.lane] = (unsigned short)PIDX[(size_t)t * 128 + F.lane]; EL[i * 128 + 64 + F.lane] = (unsigned short)PIDX[(size_t)t * 128 + 64 + F.lane];
	v_rndne_f32_e32 v2, v2
	v_cvt_i32_f32_e32 v3, v3
	v_rndne_f32_e32 v4, v4
	v_rndne_f32_e32 v5, v5
	v_mul_f32_e32 v26, v18, v52
	v_cvt_i32_f32_e32 v2, v2
	v_cvt_i32_f32_sdwa v4, v4 dst_sel:WORD_1 dst_unused:UNUSED_PAD src0_sel:DWORD
	v_cvt_i32_f32_e32 v5, v5
	v_mul_f32_e32 v19, v18, v55
	v_rndne_f32_e32 v26, v26
	v_mul_f32_e32 v27, v18, v50
	v_mul_f32_e32 v28, v18, v48
	v_rndne_f32_e32 v19, v19
	v_cvt_i32_f32_e32 v26, v26
	v_rndne_f32_e32 v27, v27
	v_rndne_f32_e32 v28, v28
	v_cvt_i32_f32_e32 v19, v19
	v_cvt_i32_f32_sdwa v27, v27 dst_sel:WORD_1 dst_unused:UNUSED_PAD src0_sel:DWORD
	v_cvt_i32_f32_e32 v28, v28
	v_lshlrev_b32_e32 v3, 8, v3
	v_and_b32_e32 v3, 0xff00, v3
	v_and_b32_e32 v4, 0xff0000, v4
	v_perm_b32 v2, v5, v2, s21
	v_or3_b32 v2, v2, v3, v4
	v_lshlrev_b32_e32 v3, 8, v26
	v_and_b32_e32 v3, 0xff00, v3
	v_and_b32_e32 v4, 0xff0000, v27
	v_perm_b32 v5, v28, v19, s21
	v_or3_b32 v3, v5, v3, v4
	v_mul_f32_e32 v5, v18, v36
	v_mul_f32_e32 v4, v18, v38
	v_rndne_f32_e32 v5, v5
	v_mul_f32_e32 v19, v18, v60
	v_mul_f32_e32 v26, v18, v58
	v_rndne_f32_e32 v4, v4
	v_cvt_i32_f32_e32 v5, v5
	v_rndne_f32_e32 v19, v19
	v_rndne_f32_e32 v26, v26
	v_mul_f32_e32 v28, v18, v57
	v_cvt_i32_f32_e32 v4, v4
	v_cvt_i32_f32_sdwa v19, v19 dst_sel:WORD_1 dst_unused:UNUSED_PAD src0_sel:DWORD
	v_cvt_i32_f32_e32 v26, v26
	v_mul_f32_e32 v27, v18, v59
	v_rndne_f32_e32 v28, v28
	v_mul_f32_e32 v29, v18, v56
	v_mul_f32_e32 v30, v18, v53
	v_rndne_f32_e32 v27, v27
	v_cvt_i32_f32_e32 v28, v28
	v_rndne_f32_e32 v29, v29
	v_rndne_f32_e32 v30, v30
	v_cvt_i32_f32_e32 v27, v27
	v_cvt_i32_f32_sdwa v29, v29 dst_sel:WORD_1 dst_unused:UNUSED_PAD src0_sel:DWORD
	v_cvt_i32_f32_e32 v30, v30
	v_lshlrev_b32_e32 v5, 8, v5
	v_and_b32_e32 v5, 0xff00, v5
	v_and_b32_e32 v19, 0xff0000, v19
	v_perm_b32 v4, v26, v4, s21
	v_or3_b32 v4, v4, v5, v19
	v_lshlrev_b32_e32 v5, 8, v28
	v_and_b32_e32 v5, 0xff00, v5
	v_and_b32_e32 v19, 0xff0000, v29
	v_perm_b32 v26, v30, v27, s21
	v_or3_b32 v5, v26, v5, v19
	ds_write2st64_b64 v25, v[2:3], v[4:5] offset0:18 offset1:19
	v_mul_f32_e32 v3, v18, v21
	v_mul_f32_e32 v2, v18, v20
	v_rndne_f32_e32 v3, v3
	v_mul_f32_e32 v4, v18, v22
	v_mul_f32_e32 v5, v18, v23
	v_rndne_f32_e32 v2, v2
	v_cvt_i32_f32_e32 v3, v3
	v_rndne_f32_e32 v4, v4
	v_rndne_f32_e32 v5, v5
	v_mul_f32_e32 v20, v18, v64
	v_cvt_i32_f32_e32 v2, v2
	v_cvt_i32_f32_sdwa v4, v4 dst_sel:WORD_1 dst_unused:UNUSED_PAD src0_sel:DWORD
	v_cvt_i32_f32_e32 v5, v5
	v_mul_f32_e32 v19, v18, v61
	v_rndne_f32_e32 v20, v20
	v_mul_f32_e32 v21, v18, v65
	v_mul_f32_e32 v22, v18, v66
	v_rndne_f32_e32 v19, v19
	v_cvt_i32_f32_e32 v20, v20
	v_rndne_f32_e32 v21, v21
	v_rndne_f32_e32 v22, v22
	v_cvt_i32_f32_e32 v19, v19
	v_cvt_i32_f32_sdwa v21, v21 dst_sel:WORD_1 dst_unused:UNUSED_PAD src0_sel:DWORD
	v_cvt_i32_f32_e32 v22, v22
	v_lshlrev_b32_e32 v3, 8, v3
	v_and_b32_e32 v3, 0xff00, v3
	v_and_b32_e32 v4, 0xff0000, v4
	v_perm_b32 v2, v5, v2, s21
	v_or3_b32 v2, v2, v3, v4
	v_lshlrev_b32_e32 v3, 8, v20
	v_and_b32_e32 v3, 0xff00, v3
	v_and_b32_e32 v4, 0xff0000, v21
	v_perm_b32 v5, v22, v19, s21
	v_or3_b32 v3, v5, v3, v4
	v_mul_f32_e32 v5, v18, v68
	v_mul_f32_e32 v4, v18, v67
	v_rndne_f32_e32 v5, v5
	v_mul_f32_e32 v19, v18, v69
	v_mul_f32_e32 v20, v18, v70
	v_rndne_f32_e32 v4, v4
	v_cvt_i32_f32_e32 v5, v5
	v_rndne_f32_e32 v19, v19
	v_rndne_f32_e32 v20, v20
	v_mul_f32_e32 v6, v18, v6
	v_cvt_i32_f32_e32 v4, v4
	v_cvt_i32_f32_sdwa v19, v19 dst_sel:WORD_1 dst_unused:UNUSED_PAD src0_sel:DWORD
	v_cvt_i32_f32_e32 v20, v20
	v_mul_f32_e32 v21, v18, v71
	v_rndne_f32_e32 v6, v6
	v_mul_f32_e32 v22, v18, v72
	v_mul_f32_e32 v7, v18, v7
	v_rndne_f32_e32 v21, v21
	v_cvt_i32_f32_e32 v6, v6
	v_rndne_f32_e32 v22, v22
	v_rndne_f32_e32 v7, v7
	v_cvt_i32_f32_e32 v21, v21
	v_cvt_i32_f32_sdwa v22, v22 dst_sel:WORD_1 dst_unused:UNUSED_PAD src0_sel:DWORD
	v_cvt_i32_f32_e32 v7, v7
	v_lshlrev_b32_e32 v5, 8, v5
	v_and_b32_e32 v5, 0xff00, v5
	v_and_b32_e32 v19, 0xff0000, v19
	v_perm_b32 v4, v20, v4, s21
	v_or3_b32 v4, v4, v5, v19
	v_lshlrev_b32_e32 v5, 8, v6
	v_and_b32_e32 v5, 0xff00, v5
	v_and_b32_e32 v6, 0xff0000, v22
	v_perm_b32 v7, v7, v21, s21
	v_or3_b32 v5, v7, v5, v6
	ds_write2st64_b64 v25, v[2:3], v[4:5] offset0:20 offset1:21
	v_mul_f32_e32 v3, v18, v8
	v_mul_f32_e32 v2, v18, v73
	v_rndne_f32_e32 v3, v3
	v_mul_f32_e32 v4, v18, v74
	v_mul_f32_e32 v5, v18, v9
	v_rndne_f32_e32 v2, v2
	v_cvt_i32_f32_e32 v3, v3
	v_rndne_f32_e32 v4, v4
	v_rndne_f32_e32 v5, v5
	v_mul_f32_e32 v7, v18, v10
	v_cvt_i32_f32_e32 v2, v2
	v_cvt_i32_f32_sdwa v4, v4 dst_sel:WORD_1 dst_unused:UNUSED_PAD src0_sel:DWORD
	v_cvt_i32_f32_e32 v5, v5
	v_mul_f32_e32 v6, v18, v75
	v_rndne_f32_e32 v7, v7
	v_mul_f32_e32 v8, v18, v76
	v_mul_f32_e32 v9, v18, v11
	v_rndne_f32_e32 v6, v6
	v_cvt_i32_f32_e32 v7, v7
	v_rndne_f32_e32 v8, v8
	v_rndne_f32_e32 v9, v9
	v_cvt_i32_f32_e32 v6, v6
	v_cvt_i32_f32_sdwa v8, v8 dst_sel:WORD_1 dst_unused:UNUSED_PAD src0_sel:DWORD
	v_cvt_i32_f32_e32 v9, v9
	v_lshlrev_b32_e32 v3, 8, v3
	v_and_b32_e32 v3, 0xff00, v3
	v_and_b32_e32 v4, 0xff0000, v4
	v_perm_b32 v2, v5, v2, s21
	v_or3_b32 v2, v2, v3, v4
	v_lshlrev_b32_e32 v3, 8, v7
	v_and_b32_e32 v3, 0xff00, v3
	v_and_b32_e32 v4, 0xff0000, v8
	v_perm_b32 v5, v9, v6, s21
	v_or3_b32 v3, v5, v3, v4
	v_mul_f32_e32 v5, v18, v12
	v_mul_f32_e32 v4, v18, v77
	v_rndne_f32_e32 v5, v5
	v_mul_f32_e32 v6, v18, v78
	v_mul_f32_e32 v7, v18, v13
	v_rndne_f32_e32 v4, v4
	v_cvt_i32_f32_e32 v5, v5
	v_rndne_f32_e32 v6, v6
	v_rndne_f32_e32 v7, v7
	v_mul_f32_e32 v9, v18, v14
	v_cvt_i32_f32_e32 v4, v4
	v_cvt_i32_f32_sdwa v6, v6 dst_sel:WORD_1 dst_unused:UNUSED_PAD src0_sel:DWORD
	v_cvt_i32_f32_e32 v7, v7
	v_mul_f32_e32 v8, v18, v79
	v_rndne_f32_e32 v9, v9
	v_mul_f32_e32 v10, v18, v80
	v_mul_f32_e32 v11, v18, v15
	v_rndne_f32_e32 v8, v8
	v_cvt_i32_f32_e32 v9, v9
	v_rndne_f32_e32 v10, v10
	v_rndne_f32_e32 v11, v11
	v_cvt_i32_f32_e32 v8, v8
	v_cvt_i32_f32_sdwa v10, v10 dst_sel:WORD_1 dst_unused:UNUSED_PAD src0_sel:DWORD
	v_cvt_i32_f32_e32 v11, v11
	v_lshlrev_b32_e32 v5, 8, v5
	v_and_b32_e32 v5, 0xff00, v5
	v_and_b32_e32 v6, 0xff0000, v6
	v_perm_b32 v4, v7, v4, s21
	v_or3_b32 v4, v4, v5, v6
	v_lshlrev_b32_e32 v5, 8, v9
	v_and_b32_e32 v5, 0xff00, v5
	v_and_b32_e32 v6, 0xff0000, v10
	v_perm_b32 v7, v11, v8, s21
	v_or3_b32 v5, v7, v5, v6
	ds_write2st64_b64 v25, v[2:3], v[4:5] offset0:22 offset1:23
	s_waitcnt vmcnt(1)
; #define LAS __attribute__((address_space(3)))
; __device__ __forceinline__ float bflo(unsigned w) { return __uint_as_float(w << 16); }
; __device__ __forceinline__ float bfhi(unsigned w) { return __uint_as_float(w & 0xffff0000u); }
; __device__ __forceinline__ float wave_sum(float v) { v = dpp_add16(v); return (rdlane(v, 0) + rdlane(v, 16)) + (rdlane(v, 32) + rdlane(v, 48)); }
; __device__ __forceinline__ float wave_max(float v) { v = dpp_max16(v); return fmaxf(fmaxf(rdlane(v, 0), rdlane(v, 16)), fmaxf(rdlane(v, 32), rdlane(v, 48))); }
; __device__ __forceinline__ void p12_peer(Frame& F) {
;     ...
;         const int t = F.gw + i * F.NGW; v4u xp[8]; float mxa = 0.f;
; #pragma unroll
;         for (int j = 0; j < 8; ++j) { xp[j] = ((const v4u*)(HN + (size_t)t * D_))[F.lane + 64 * j];
;             mxa = fmaxf(fmaxf(fmaxf(mxa, fmaxf(fabsf(bflo(xp[j].x)), fabsf(bfhi(xp[j].x)))), fmaxf(fabsf(bflo(xp[j].y)), fabsf(bfhi(xp[j].y)))), fmaxf(fmaxf(fabsf(bflo(xp[j].z)), fabsf(bfhi(xp[j].z))), fmaxf(fabsf(bflo(xp[j].w)), fabsf(bfhi(xp[j].w))))); }
;         mxa = wave_max(mxa); const float inv = mxa > 0.f ? 127.0f / mxa : 0.f;
;         const float rsn = 1.0f / sqrtf(wave_sum(PSQ[(size_t)t * 64 + F.lane]) * (1.f / D_) + 1e-6f);
;         sx[i] = mxa * rsn * (1.0f / 127.0f);
; #pragma unroll
;         for (int j = 0; j < 8; ++j) {
;             const int q0 = (int)rintf(bflo(xp[j].x) * inv), q1 = (int)rintf(bfhi(xp[j].x) * inv), q2 = (int)rintf(bflo(xp[j].y) * inv), q3 = (int)rintf(bfhi(xp[j].y) * inv);
;             const int q4 = (int)rintf(bflo(xp[j].z) * inv), q5 = (int)rintf(bfhi(xp[j].z) * inv), q6 = (int)rintf(bflo(xp[j].w) * inv), q7 = (int)rintf(bfhi(xp[j].w) * inv);
;             *(LAS v2u*)(XQ + i * 4096 + 8 * (F.lane + 64 * j)) = (v2u){(unsigned)((q0 & 0xff) | ((q1 & 0xff) << 8) | ((q2 & 0xff) << 16) | (q3 << 24)), (unsigned)((q4 & 0xff) | ((q5 & 0xff) << 8) | ((q6 & 0xff) << 16) | (q7 << 24))}; }
;         EL[i * 128 + F.lane] = (unsigned short)PIDX[(size_t)t * 128 + F.lane]; EL[i * 128 + 64 + F.lane] = (unsigned short)PIDX[(size_t)t * 128 + 64 + F.lane];
	ds_write_b16 v24, v62 offset:16896
	s_waitcnt vmcnt(0)
	ds_write_b16 v24, v63 offset:17024
	global_load_dwordx4 v[4:7], v[0:1], off
	global_load_dwordx4 v[8:11], v[0:1], off offset:1024
	global_load_dwordx4 v[12:15], v[0:1], off offset:2048
	global_load_dwordx4 v[58:61], v[0:1], off offset:3072
	v_add_co_u32_e32 v54, vcc, s28, v0
	v_lshl_add_u64 v[18:19], s[12:13], 0, v[16:17]
	s_nop 0
	v_addc_co_u32_e32 v55, vcc, 0, v1, vcc
	s_lshl_b64 s[12:13], s[10:11], 9
	s_add_u32 s18, s18, s12
	s_addc_u32 s19, s19, s13
	v_lshl_add_u64 v[16:17], s[18:19], 0, v[16:17]
	s_add_u32 s18, s68, 0xf400000
	v_add_f32_dpp v32, v34, v34 quad_perm:[1,0,3,2] row_mask:0xf bank_mask:0xf bound_ctrl:1
	s_waitcnt vmcnt(3)
	v_lshlrev_b32_e32 v21, 16, v4
	v_and_b32_e32 v20, 0xffff0000, v4
	v_max_f32_e64 v2, |v20|, |v20|
	v_max_f32_e64 v3, |v21|, |v21|
	v_max_f32_e32 v4, v3, v2
	global_load_dwordx4 v[0:3], v[54:55], off
	v_lshlrev_b32_e32 v39, 16, v5
	v_and_b32_e32 v36, 0xffff0000, v5
	v_max_f32_e64 v5, |v36|, |v36|
	v_max_f32_e64 v22, |v39|, |v39|
	v_max_f32_e32 v5, v22, v5
	v_lshlrev_b32_e32 v30, 16, v7
	v_and_b32_e32 v28, 0xffff0000, v7
	v_max3_f32 v26, v4, 0, v5
	v_max_f32_e64 v4, |v28|, |v28|
	v_max_f32_e64 v5, |v30|, |v30|
	v_lshlrev_b32_e32 v40, 16, v6
	v_and_b32_e32 v37, 0xffff0000, v6
	v_max_f32_e32 v4, v5, v4
	v_max3_f32 v27, |v40|, |v37|, v4
	s_waitcnt vmcnt(3)
	v_lshlrev_b32_e32 v23, 16, v8
	v_and_b32_e32 v22, 0xffff0000, v8
	global_load_dwordx4 v[4:7], v[54:55], off offset:1024
	v_max_f32_e64 v8, |v22|, |v22|
	v_max_f32_e64 v29, |v23|, |v23|
	v_max_f32_e32 v8, v29, v8
	v_lshlrev_b32_e32 v46, 16, v9
	v_and_b32_e32 v43, 0xffff0000, v9
	v_lshlrev_b32_e32 v41, 16, v11
	v_and_b32_e32 v38, 0xffff0000, v11
	v_max3_f32 v8, v26, v27, v8
	v_max_f32_e64 v9, |v43|, |v43|
	v_max_f32_e64 v26, |v46|, |v46|
	v_lshlrev_b32_e32 v44, 16, v10
	v_and_b32_e32 v42, 0xffff0000, v10
	v_max_f32_e64 v10, |v38|, |v38|
	v_max_f32_e64 v11, |v41|, |v41|
	v_max_f32_e32 v9, v26, v9
	v_max_f32_e32 v10, v11, v10
	s_waitcnt vmcnt(3)
	v_lshlrev_b32_e32 v27, 16, v12
	v_and_b32_e32 v26, 0xffff0000, v12
	v_max3_f32 v10, |v44|, |v42|, v10
	v_max_f32_e64 v12, |v26|, |v26|
	v_max_f32_e64 v31, |v27|, |v27|
	v_lshlrev_b32_e32 v51, 16, v13
	v_and_b32_e32 v48, 0xffff0000, v13
	v_max3_f32 v29, v8, v9, v10
	global_load_dwordx4 v[8:11], v[54:55], off offset:2048
	v_max_f32_e32 v12, v31, v12
	v_max_f32_e64 v13, |v48|, |v48|
	v_max_f32_e64 v31, |v51|, |v51|
	v_max_f32_e32 v13, v31, v13
	v_lshlrev_b32_e32 v47, 16, v15
	v_and_b32_e32 v45, 0xffff0000, v15
	v_max3_f32 v35, v29, v12, v13
	v_max_f32_e64 v12, |v45|, |v45|
	v_max_f32_e64 v13, |v47|, |v47|
	v_lshlrev_b32_e32 v52, 16, v14
	v_and_b32_e32 v49, 0xffff0000, v14
	v_max_f32_e32 v12, v13, v12
	v_max3_f32 v50, |v52|, |v49|, v12
	global_load_dwordx4 v[12:15], v[54:55], off offset:3072
	s_waitcnt vmcnt(4)
	v_lshlrev_b32_e32 v31, 16, v58
	v_and_b32_e32 v29, 0xffff0000, v58
	v_max_f32_e64 v53, |v29|, |v29|
	v_max_f32_e64 v54, |v31|, |v31|
	v_max_f32_e32 v53, v54, v53
	v_lshlrev_b32_e32 v57, 16, v59
	v_and_b32_e32 v55, 0xffff0000, v59
	v_max3_f32 v35, v35, v50, v53
	v_max_f32_e64 v50, |v55|, |v55|
	v_max_f32_e64 v53, |v57|, |v57|
	v_max_f32_e32 v58, v53, v50
	v_lshlrev_b32_e32 v53, 16, v61
	v_and_b32_e32 v50, 0xffff0000, v61
	v_lshlrev_b32_e32 v56, 16, v60
	v_and_b32_e32 v54, 0xffff0000, v60
	v_max_f32_e64 v59, |v50|, |v50|
	v_max_f32_e64 v60, |v53|, |v53|
	v_max_f32_e32 v59, v60, v59
	v_max3_f32 v59, |v56|, |v54|, v59
	v_max3_f32 v58, v35, v58, v59
	global_load_dword v35, v[18:19], off
	global_load_dword v59, v[16:17], off
	global_load_dword v60, v[16:17], off offset:256
	v_add_f32_dpp v32, v32, v32 quad_perm:[2,3,0,1] row_mask:0xf bank_mask:0xf bound_ctrl:1
	s_waitcnt vmcnt(6)
	v_lshlrev_b32_e32 v16, 16, v0
	v_and_b32_e32 v17, 0xffff0000, v0
	v_max_f32_e64 v0, |v17|, |v17|
	v_max_f32_e64 v18, |v16|, |v16|
	v_max_f32_e32 v0, v18, v0
	v_lshlrev_b32_e32 v18, 16, v1
	v_and_b32_e32 v19, 0xffff0000, v1
	v_max_f32_e64 v1, |v19|, |v19|
	v_max_f32_e64 v61, |v18|, |v18|
	v_max_f32_e32 v1, v61, v1
	v_lshlrev_b32_e32 v62, 16, v3
	v_and_b32_e32 v63, 0xffff0000, v3
	v_max3_f32 v0, v58, v0, v1
	v_lshlrev_b32_e32 v58, 16, v2
	v_and_b32_e32 v61, 0xffff0000, v2
	v_max_f32_e64 v1, |v63|, |v63|
	v_max_f32_e64 v2, |v62|, |v62|
	s_waitcnt vmcnt(5)
	v_lshlrev_b32_e32 v64, 16, v4
	v_and_b32_e32 v4, 0xffff0000, v4
	v_max_f32_e32 v1, v2, v1
	v_max_f32_e64 v2, |v4|, |v4|
	v_max_f32_e64 v3, |v64|, |v64|
	v_max3_f32 v1, |v58|, |v61|, v1
	v_max_f32_e32 v2, v3, v2
	v_lshlrev_b32_e32 v65, 16, v5
	v_and_b32_e32 v5, 0xffff0000, v5
	v_max3_f32 v0, v0, v1, v2
	v_max_f32_e64 v1, |v5|, |v5|
	v_max_f32_e64 v2, |v65|, |v65|
	v_lshlrev_b32_e32 v67, 16, v7
	v_and_b32_e32 v7, 0xffff0000, v7
	v_max_f32_e32 v1, v2, v1
	v_max_f32_e64 v2, |v7|, |v7|
	v_max_f32_e64 v3, |v67|, |v67|
	v_lshlrev_b32_e32 v66, 16, v6
	v_and_b32_e32 v6, 0xffff0000, v6
	v_max_f32_e32 v2, v3, v2
	v_max3_f32 v2, |v66|, |v6|, v2
	v_max3_f32 v0, v0, v1, v2
	v_add_f32_dpp v32, v32, v32 row_half_mirror row_mask:0xf bank_mask:0xf bound_ctrl:1
	s_waitcnt vmcnt(4)
	v_lshlrev_b32_e32 v68, 16, v8
	v_and_b32_e32 v8, 0xffff0000, v8
	v_max_f32_e64 v1, |v8|, |v8|
	v_max_f32_e64 v2, |v68|, |v68|
	v_lshlrev_b32_e32 v69, 16, v9
	v_and_b32_e32 v9, 0xffff0000, v9
	v_max_f32_e32 v1, v2, v1
	v_max_f32_e64 v2, |v9|, |v9|
	v_max_f32_e64 v3, |v69|, |v69|
	v_max_f32_e32 v2, v3, v2
	v_lshlrev_b32_e32 v71, 16, v11
	v_and_b32_e32 v11, 0xffff0000, v11
	v_max3_f32 v0, v0, v1, v2
	v_max_f32_e64 v1, |v11|, |v11|
	v_max_f32_e64 v2, |v71|, |v71|
	s_waitcnt vmcnt(3)
; #define LAS __attribute__((address_space(3)))
; __device__ __forceinline__ float bflo(unsigned w) { return __uint_as_float(w << 16); }
; __device__ __forceinline__ float bfhi(unsigned w) { return __uint_as_float(w & 0xffff0000u); }
; __device__ __forceinline__ float wave_sum(float v) { v = dpp_add16(v); return (rdlane(v, 0) + rdlane(v, 16)) + (rdlane(v, 32) + rdlane(v, 48)); }
; __device__ __forceinline__ float wave_max(float v) { v = dpp_max16(v); return fmaxf(fmaxf(rdlane(v, 0), rdlane(v, 16)), fmaxf(rdlane(v, 32), rdlane(v, 48))); }
; __device__ __forceinline__ void p12_peer(Frame& F) {
;     ...
;             mxa = fmaxf(fmaxf(fmaxf(mxa, fmaxf(fabsf(bflo(xp[j].x)), fabsf(bfhi(xp[j].x)))), fmaxf(fabsf(bflo(xp[j].y)), fabsf(bfhi(xp[j].y)))), fmaxf(fmaxf(fabsf(bflo(xp[j].z)), fabsf(bfhi(xp[j].z))), fmaxf(fabsf(bflo(xp[j].w)), fabsf(bfhi(xp[j].w))))); }
;         mxa = wave_max(mxa); const float inv = mxa > 0.f ? 127.0f / mxa : 0.f;
;         const float rsn = 1.0f / sqrtf(wave_sum(PSQ[(size_t)t * 64 + F.lane]) * (1.f / D_) + 1e-6f);
;         sx[i] = mxa * rsn * (1.0f / 127.0f);
; #pragma unroll
;         for (int j = 0; j < 8; ++j) {
;             const int q0 = (int)rintf(bflo(xp[j].x) * inv), q1 = (int)rintf(bfhi(xp[j].x) * inv), q2 = (int)rintf(bflo(xp[j].y) * inv), q3 = (int)rintf(bfhi(xp[j].y) * inv);
;             const int q4 = (int)rintf(bflo(xp[j].z) * inv), q5 = (int)rintf(bfhi(xp[j].z) * inv), q6 = (int)rintf(bflo(xp[j].w) * inv), q7 = (int)rintf(bfhi(xp[j].w) * inv);
;             *(LAS v2u*)(XQ + i * 4096 + 8 * (F.lane + 64 * j)) = (v2u){(unsigned)((q0 & 0xff) | ((q1 & 0xff) << 8) | ((q2 & 0xff) << 16) | (q3 << 24)), (unsigned)((q4 & 0xff) | ((q5 & 0xff) << 8) | ((q6 & 0xff) << 16) | (q7 << 24))}; }
	v_lshlrev_b32_e32 v72, 16, v12
	v_and_b32_e32 v12, 0xffff0000, v12
	v_lshlrev_b32_e32 v70, 16, v10
	v_and_b32_e32 v10, 0xffff0000, v10
	v_max_f32_e32 v1, v2, v1
	v_max_f32_e64 v2, |v12|, |v12|
	v_max_f32_e64 v3, |v72|, |v72|
	v_max3_f32 v1, |v70|, |v10|, v1
	v_max_f32_e32 v2, v3, v2
	v_lshlrev_b32_e32 v73, 16, v13
	v_and_b32_e32 v13, 0xffff0000, v13
	v_max3_f32 v0, v0, v1, v2
	v_max_f32_e64 v1, |v13|, |v13|
	v_max_f32_e64 v2, |v73|, |v73|
	v_lshlrev_b32_e32 v75, 16, v15
	v_and_b32_e32 v15, 0xffff0000, v15
	v_max_f32_e32 v1, v2, v1
	v_max_f32_e64 v2, |v15|, |v15|
	v_max_f32_e64 v3, |v75|, |v75|
	v_lshlrev_b32_e32 v74, 16, v14
	v_and_b32_e32 v14, 0xffff0000, v14
	v_max_f32_e32 v2, v3, v2
	v_max3_f32 v2, |v74|, |v14|, v2
	v_max3_f32 v0, v0, v1, v2
	v_mov_b32_e32 v1, 0
	v_add_f32_dpp v32, v32, v32 row_mirror row_mask:0xf bank_mask:0xf bound_ctrl:1
	s_nop 0
	v_mov_b32_dpp v1, v0 quad_perm:[1,0,3,2] row_mask:0xf bank_mask:0xf
	v_max_f32_e32 v1, v1, v1
	v_max_f32_e32 v0, v0, v1
	v_mov_b32_e32 v1, 0
	v_readlane_b32 s31, v32, 16
	v_readlane_b32 s30, v32, 32
	v_mov_b32_dpp v1, v0 quad_perm:[2,3,0,1] row_mask:0xf bank_mask:0xf
	v_max_f32_e32 v1, v1, v1
	v_max_f32_e32 v0, v0, v1
	v_mov_b32_e32 v1, 0
	v_readlane_b32 s33, v32, 48
	s_nop 0
	v_mov_b32_dpp v1, v0 row_half_mirror row_mask:0xf bank_mask:0xf
	v_max_f32_e32 v1, v1, v1
	v_max_f32_e32 v0, v0, v1
	v_mov_b32_e32 v1, 0
	s_nop 1
	v_mov_b32_dpp v1, v0 row_mirror row_mask:0xf bank_mask:0xf
	v_max_f32_e32 v1, v1, v1
	v_max_f32_e32 v0, v0, v1
	s_nop 0
	v_readlane_b32 s23, v0, 32
	v_readlane_b32 s28, v0, 48
	v_readlane_b32 s19, v0, 0
	v_readlane_b32 s22, v0, 16
	v_max_f32_e64 v0, s28, s28
	v_max_f32_e64 v1, s23, s23
	v_max_f32_e32 v0, v1, v0
	v_mov_b32_e32 v1, s22
	v_max3_f32 v160, s19, v1, v0
	v_div_scale_f32 v0, s[22:23], v160, v160, s29
	v_rcp_f32_e32 v1, v0
	s_addc_u32 s19, s69, 0
	v_fma_f32 v2, -v0, v1, 1.0
	v_fmac_f32_e32 v1, v2, v1
	v_div_scale_f32 v2, vcc, s29, v160, s29
	v_mul_f32_e32 v3, v2, v1
	v_fma_f32 v76, -v0, v3, v2
	v_fmac_f32_e32 v3, v76, v1
	v_fma_f32 v0, -v0, v3, v2
	v_div_fmas_f32 v0, v0, v1, v3
	v_div_fixup_f32 v0, v0, v160, s29
	v_cmp_lt_f32_e32 vcc, 0, v160
	v_readlane_b32 s29, v32, 0
	s_waitcnt vmcnt(2)
	v_add_f32_dpp v32, v35, v35 quad_perm:[1,0,3,2] row_mask:0xf bank_mask:0xf bound_ctrl:1
	v_cndmask_b32_e32 v76, 0, v0, vcc
	v_mul_f32_e32 v1, v76, v20
	v_mul_f32_e32 v0, v76, v21
	v_rndne_f32_e32 v1, v1
	v_mul_f32_e32 v2, v76, v39
	v_mul_f32_e32 v3, v76, v36
	v_rndne_f32_e32 v0, v0
	v_cvt_i32_f32_e32 v1, v1
	v_rndne_f32_e32 v2, v2
	v_rndne_f32_e32 v3, v3
	v_mul_f32_e32 v21, v76, v37
	v_cvt_i32_f32_e32 v0, v0
	v_cvt_i32_f32_sdwa v2, v2 dst_sel:WORD_1 dst_unused:UNUSED_PAD src0_sel:DWORD
	v_cvt_i32_f32_e32 v3, v3
	v_mul_f32_e32 v20, v76, v40
	v_rndne_f32_e32 v21, v21
	v_mul_f32_e32 v30, v76, v30
	v_mul_f32_e32 v28, v76, v28
	v_rndne_f32_e32 v20, v20
	v_cvt_i32_f32_e32 v21, v21
	v_rndne_f32_e32 v30, v30
	v_rndne_f32_e32 v28, v28
	v_cvt_i32_f32_e32 v20, v20
	v_cvt_i32_f32_sdwa v30, v30 dst_sel:WORD_1 dst_unused:UNUSED_PAD src0_sel:DWORD
	v_cvt_i32_f32_e32 v28, v28
	v_lshlrev_b32_e32 v1, 8, v1
	v_and_b32_e32 v1, 0xff00, v1
	v_and_b32_e32 v2, 0xff0000, v2
	v_perm_b32 v0, v3, v0, s21
	v_or3_b32 v0, v0, v1, v2
	v_lshlrev_b32_e32 v1, 8, v21
	v_and_b32_e32 v1, 0xff00, v1
	v_and_b32_e32 v2, 0xff0000, v30
	v_perm_b32 v3, v28, v20, s21
	v_or3_b32 v1, v3, v1, v2
	v_mul_f32_e32 v3, v76, v22
	v_mul_f32_e32 v2, v76, v23
	v_rndne_f32_e32 v3, v3
	v_mul_f32_e32 v20, v76, v46
	v_mul_f32_e32 v21, v76, v43
	v_rndne_f32_e32 v2, v2
	v_cvt_i32_f32_e32 v3, v3
	v_rndne_f32_e32 v20, v20
	v_rndne_f32_e32 v21, v21
	v_mul_f32_e32 v23, v76, v42
	v_cvt_i32_f32_e32 v2, v2
	v_cvt_i32_f32_sdwa v20, v20 dst_sel:WORD_1 dst_unused:UNUSED_PAD src0_sel:DWORD
	v_cvt_i32_f32_e32 v21, v21
	v_mul_f32_e32 v22, v76, v44
	v_rndne_f32_e32 v23, v23
	v_mul_f32_e32 v28, v76, v41
	v_mul_f32_e32 v30, v76, v38
	v_rndne_f32_e32 v22, v22
	v_cvt_i32_f32_e32 v23, v23
	v_rndne_f32_e32 v28, v28
	v_rndne_f32_e32 v30, v30
	v_cvt_i32_f32_e32 v22, v22
	v_cvt_i32_f32_sdwa v28, v28 dst_sel:WORD_1 dst_unused:UNUSED_PAD src0_sel:DWORD
	v_cvt_i32_f32_e32 v30, v30
	v_lshlrev_b32_e32 v3, 8, v3
	v_and_b32_e32 v3, 0xff00, v3
	v_and_b32_e32 v20, 0xff0000, v20
	v_perm_b32 v2, v21, v2, s21
	v_or3_b32 v2, v2, v3, v20
	v_lshlrev_b32_e32 v3, 8, v23
	v_and_b32_e32 v3, 0xff00, v3
	v_and_b32_e32 v20, 0xff0000, v28
	v_perm_b32 v21, v30, v22, s21
	v_or3_b32 v3, v21, v3, v20
	ds_write2st64_b64 v25, v[0:1], v[2:3] offset0:24 offset1:25
	v_mul_f32_e32 v1, v76, v26
	v_mul_f32_e32 v0, v76, v27
	v_rndne_f32_e32 v1, v1
	v_mul_f32_e32 v2, v76, v51
	v_mul_f32_e32 v3, v76, v48
	v_rndne_f32_e32 v0, v0
	v_cvt_i32_f32_e32 v1, v1
	v_rndne_f32_e32 v2, v2
	v_rndne_f32_e32 v3, v3
	v_mul_f32_e32 v21, v76, v49
	v_cvt_i32_f32_e32 v0, v0
	v_cvt_i32_f32_sdwa v2, v2 dst_sel:WORD_1 dst_unused:UNUSED_PAD src0_sel:DWORD
	v_cvt_i32_f32_e32 v3, v3
	v_mul_f32_e32 v20, v76, v52
	v_rndne_f32_e32 v21, v21
	v_mul_f32_e32 v22, v76, v47
	v_mul_f32_e32 v23, v76, v45
	v_rndne_f32_e32 v20, v20
	v_cvt_i32_f32_e32 v21, v21
	v_rndne_f32_e32 v22, v22
	v_rndne_f32_e32 v23, v23
	v_cvt_i32_f32_e32 v20, v20
	v_cvt_i32_f32_sdwa v22, v22 dst_sel:WORD_1 dst_unused:UNUSED_PAD src0_sel:DWORD
	v_cvt_i32_f32_e32 v23, v23
	v_lshlrev_b32_e32 v1, 8, v1
	v_and_b32_e32 v1, 0xff00, v1
	v_and_b32_e32 v2, 0xff0000, v2
	v_perm_b32 v0, v3, v0, s21
	v_or3_b32 v0, v0, v1, v2
	v_lshlrev_b32_e32 v1, 8, v21
	v_and_b32_e32 v1, 0xff00, v1
	v_and_b32_e32 v2, 0xff0000, v22
	v_perm_b32 v3, v23, v20, s21
	v_or3_b32 v1, v3, v1, v2
	v_mul_f32_e32 v3, v76, v29
	v_mul_f32_e32 v2, v76, v31
	v_rndne_f32_e32 v3, v3
	v_mul_f32_e32 v20, v76, v57
; #define LAS __attribute__((address_space(3)))
; #define LDS_WAIT() asm volatile("s_waitcnt lgkmcnt(0)" ::: "memory")
; __device__ __forceinline__ float bflo(unsigned w) { return __uint_as_float(w << 16); }
; __device__ __forceinline__ float bfhi(unsigned w) { return __uint_as_float(w & 0xffff0000u); }
; __device__ __forceinline__ void p12_peer(Frame& F) {
;     ...
;         for (int j = 0; j < 8; ++j) {
;             const int q0 = (int)rintf(bflo(xp[j].x) * inv), q1 = (int)rintf(bfhi(xp[j].x) * inv), q2 = (int)rintf(bflo(xp[j].y) * inv), q3 = (int)rintf(bfhi(xp[j].y) * inv);
;             const int q4 = (int)rintf(bflo(xp[j].z) * inv), q5 = (int)rintf(bfhi(xp[j].z) * inv), q6 = (int)rintf(bflo(xp[j].w) * inv), q7 = (int)rintf(bfhi(xp[j].w) * inv);
;             *(LAS v2u*)(XQ + i * 4096 + 8 * (F.lane + 64 * j)) = (v2u){(unsigned)((q0 & 0xff) | ((q1 & 0xff) << 8) | ((q2 & 0xff) << 16) | (q3 << 24)), (unsigned)((q4 & 0xff) | ((q5 & 0xff) << 8) | ((q6 & 0xff) << 16) | (q7 << 24))}; }
;         EL[i * 128 + F.lane] = (unsigned short)PIDX[(size_t)t * 128 + F.lane]; EL[i * 128 + 64 + F.lane] = (unsigned short)PIDX[(size_t)t * 128 + 64 + F.lane];
;         asm volatile("" ::: "memory");
;     }
;     LDS_WAIT(); asm volatile("" ::: "memory");
	v_mul_f32_e32 v21, v76, v55
	v_rndne_f32_e32 v2, v2
	v_cvt_i32_f32_e32 v3, v3
	v_rndne_f32_e32 v20, v20
	v_rndne_f32_e32 v21, v21
	v_mul_f32_e32 v23, v76, v54
	v_cvt_i32_f32_e32 v2, v2
	v_cvt_i32_f32_sdwa v20, v20 dst_sel:WORD_1 dst_unused:UNUSED_PAD src0_sel:DWORD
	v_cvt_i32_f32_e32 v21, v21
	v_mul_f32_e32 v22, v76, v56
	v_rndne_f32_e32 v23, v23
	v_mul_f32_e32 v26, v76, v53
	v_mul_f32_e32 v27, v76, v50
	v_rndne_f32_e32 v22, v22
	v_cvt_i32_f32_e32 v23, v23
	v_rndne_f32_e32 v26, v26
	v_rndne_f32_e32 v27, v27
	v_cvt_i32_f32_e32 v22, v22
	v_cvt_i32_f32_sdwa v26, v26 dst_sel:WORD_1 dst_unused:UNUSED_PAD src0_sel:DWORD
	v_cvt_i32_f32_e32 v27, v27
	v_lshlrev_b32_e32 v3, 8, v3
	v_and_b32_e32 v3, 0xff00, v3
	v_and_b32_e32 v20, 0xff0000, v20
	v_perm_b32 v2, v21, v2, s21
	v_or3_b32 v2, v2, v3, v20
	v_lshlrev_b32_e32 v3, 8, v23
	v_and_b32_e32 v3, 0xff00, v3
	v_and_b32_e32 v20, 0xff0000, v26
	v_perm_b32 v21, v27, v22, s21
	v_or3_b32 v3, v21, v3, v20
	ds_write2st64_b64 v25, v[0:1], v[2:3] offset0:26 offset1:27
	v_mul_f32_e32 v1, v76, v17
	v_mul_f32_e32 v0, v76, v16
	v_rndne_f32_e32 v1, v1
	v_mul_f32_e32 v2, v76, v18
	v_mul_f32_e32 v3, v76, v19
	v_rndne_f32_e32 v0, v0
	v_cvt_i32_f32_e32 v1, v1
	v_rndne_f32_e32 v2, v2
	v_rndne_f32_e32 v3, v3
	v_mul_f32_e32 v17, v76, v61
	v_cvt_i32_f32_e32 v0, v0
	v_cvt_i32_f32_sdwa v2, v2 dst_sel:WORD_1 dst_unused:UNUSED_PAD src0_sel:DWORD
	v_cvt_i32_f32_e32 v3, v3
	v_mul_f32_e32 v16, v76, v58
	v_rndne_f32_e32 v17, v17
	v_mul_f32_e32 v18, v76, v62
	v_mul_f32_e32 v19, v76, v63
	v_rndne_f32_e32 v16, v16
	v_cvt_i32_f32_e32 v17, v17
	v_rndne_f32_e32 v18, v18
	v_rndne_f32_e32 v19, v19
	v_cvt_i32_f32_e32 v16, v16
	v_cvt_i32_f32_sdwa v18, v18 dst_sel:WORD_1 dst_unused:UNUSED_PAD src0_sel:DWORD
	v_cvt_i32_f32_e32 v19, v19
	v_lshlrev_b32_e32 v1, 8, v1
	v_and_b32_e32 v1, 0xff00, v1
	v_and_b32_e32 v2, 0xff0000, v2
	v_perm_b32 v0, v3, v0, s21
	v_or3_b32 v0, v0, v1, v2
	v_lshlrev_b32_e32 v1, 8, v17
	v_and_b32_e32 v1, 0xff00, v1
	v_and_b32_e32 v2, 0xff0000, v18
	v_perm_b32 v3, v19, v16, s21
	v_or3_b32 v1, v3, v1, v2
	v_mul_f32_e32 v3, v76, v4
	v_mul_f32_e32 v2, v76, v64
	v_rndne_f32_e32 v3, v3
	v_mul_f32_e32 v4, v76, v65
	v_mul_f32_e32 v5, v76, v5
	v_rndne_f32_e32 v2, v2
	v_cvt_i32_f32_e32 v3, v3
	v_rndne_f32_e32 v4, v4
	v_rndne_f32_e32 v5, v5
	v_mul_f32_e32 v6, v76, v6
	v_cvt_i32_f32_e32 v2, v2
	v_cvt_i32_f32_sdwa v4, v4 dst_sel:WORD_1 dst_unused:UNUSED_PAD src0_sel:DWORD
	v_cvt_i32_f32_e32 v5, v5
	v_mul_f32_e32 v16, v76, v66
	v_rndne_f32_e32 v6, v6
	v_mul_f32_e32 v17, v76, v67
	v_mul_f32_e32 v7, v76, v7
	v_rndne_f32_e32 v16, v16
	v_cvt_i32_f32_e32 v6, v6
	v_rndne_f32_e32 v17, v17
	v_rndne_f32_e32 v7, v7
	v_cvt_i32_f32_e32 v16, v16
	v_cvt_i32_f32_sdwa v17, v17 dst_sel:WORD_1 dst_unused:UNUSED_PAD src0_sel:DWORD
	v_cvt_i32_f32_e32 v7, v7
	v_lshlrev_b32_e32 v3, 8, v3
	v_and_b32_e32 v3, 0xff00, v3
	v_and_b32_e32 v4, 0xff0000, v4
	v_perm_b32 v2, v5, v2, s21
	v_or3_b32 v2, v2, v3, v4
	v_lshlrev_b32_e32 v3, 8, v6
	v_and_b32_e32 v3, 0xff00, v3
	v_and_b32_e32 v4, 0xff0000, v17
	v_perm_b32 v5, v7, v16, s21
	v_or3_b32 v3, v5, v3, v4
	ds_write2st64_b64 v25, v[0:1], v[2:3] offset0:28 offset1:29
	v_mul_f32_e32 v1, v76, v8
	v_mul_f32_e32 v0, v76, v68
	v_rndne_f32_e32 v1, v1
	v_mul_f32_e32 v2, v76, v69
	v_mul_f32_e32 v3, v76, v9
	v_rndne_f32_e32 v0, v0
	v_cvt_i32_f32_e32 v1, v1
	v_rndne_f32_e32 v2, v2
	v_rndne_f32_e32 v3, v3
	v_mul_f32_e32 v5, v76, v10
	v_cvt_i32_f32_e32 v0, v0
	v_cvt_i32_f32_sdwa v2, v2 dst_sel:WORD_1 dst_unused:UNUSED_PAD src0_sel:DWORD
	v_cvt_i32_f32_e32 v3, v3
	v_mul_f32_e32 v4, v76, v70
	v_rndne_f32_e32 v5, v5
	v_mul_f32_e32 v6, v76, v71
	v_mul_f32_e32 v7, v76, v11
	v_rndne_f32_e32 v4, v4
	v_cvt_i32_f32_e32 v5, v5
	v_rndne_f32_e32 v6, v6
	v_rndne_f32_e32 v7, v7
	v_cvt_i32_f32_e32 v4, v4
	v_cvt_i32_f32_sdwa v6, v6 dst_sel:WORD_1 dst_unused:UNUSED_PAD src0_sel:DWORD
	v_cvt_i32_f32_e32 v7, v7
	v_lshlrev_b32_e32 v1, 8, v1
	v_and_b32_e32 v1, 0xff00, v1
	v_and_b32_e32 v2, 0xff0000, v2
	v_perm_b32 v0, v3, v0, s21
	v_or3_b32 v0, v0, v1, v2
	v_lshlrev_b32_e32 v1, 8, v5
	v_and_b32_e32 v1, 0xff00, v1
	v_and_b32_e32 v2, 0xff0000, v6
	v_perm_b32 v3, v7, v4, s21
	v_or3_b32 v1, v3, v1, v2
	v_mul_f32_e32 v3, v76, v12
	v_mul_f32_e32 v2, v76, v72
	v_rndne_f32_e32 v3, v3
	v_mul_f32_e32 v4, v76, v73
	v_mul_f32_e32 v5, v76, v13
	v_rndne_f32_e32 v2, v2
	v_cvt_i32_f32_e32 v3, v3
	v_rndne_f32_e32 v4, v4
	v_rndne_f32_e32 v5, v5
	v_mul_f32_e32 v7, v76, v14
	v_cvt_i32_f32_e32 v2, v2
	v_cvt_i32_f32_sdwa v4, v4 dst_sel:WORD_1 dst_unused:UNUSED_PAD src0_sel:DWORD
	v_cvt_i32_f32_e32 v5, v5
	v_mul_f32_e32 v6, v76, v74
	v_rndne_f32_e32 v7, v7
	v_mul_f32_e32 v8, v76, v75
	v_mul_f32_e32 v9, v76, v15
	v_rndne_f32_e32 v6, v6
	v_cvt_i32_f32_e32 v7, v7
	v_rndne_f32_e32 v8, v8
	v_rndne_f32_e32 v9, v9
	v_cvt_i32_f32_e32 v6, v6
	v_cvt_i32_f32_sdwa v8, v8 dst_sel:WORD_1 dst_unused:UNUSED_PAD src0_sel:DWORD
	v_cvt_i32_f32_e32 v9, v9
	v_lshlrev_b32_e32 v3, 8, v3
	v_and_b32_e32 v3, 0xff00, v3
	v_and_b32_e32 v4, 0xff0000, v4
	v_perm_b32 v2, v5, v2, s21
	v_or3_b32 v2, v2, v3, v4
	v_lshlrev_b32_e32 v3, 8, v7
	v_and_b32_e32 v3, 0xff00, v3
	v_and_b32_e32 v4, 0xff0000, v8
	v_perm_b32 v5, v9, v6, s21
	v_or3_b32 v3, v5, v3, v4
	ds_write2st64_b64 v25, v[0:1], v[2:3] offset0:30 offset1:31
	s_waitcnt vmcnt(1)
	ds_write_b16 v24, v59 offset:17152
	s_waitcnt vmcnt(0)
	ds_write_b16 v24, v60 offset:17280
	s_waitcnt lgkmcnt(0)
	ds_read_u16 v0, v93 offset:16384
	ds_read_u16 v1, v93 offset:16400
	ds_read_u16 v2, v93 offset:16416
	ds_read_u16 v3, v93 offset:16432
	ds_read_u16 v4, v93 offset:16448
	ds_read_u16 v5, v93 offset:16464
	ds_read_u16 v6, v93 offset:16480
	ds_read_u16 v36, v93 offset:16496
	s_waitcnt lgkmcnt(7)
; #define P12_ISSUE(c_, i_, h_, CW_, SC_) do { _Pragma("unroll") for (int bb = 0; bb < 8; ++bb) { const unsigned ro = (unsigned)(c_) * 16384u + (unsigned)EL[(i_) * 128 + ((h_) * 8 + bb) * 8 + g8]; \
;         CW_[bb] = *(const v4u*)(U4 + (size_t)(ro * 128u + 16u * (unsigned)k8)); SC_[bb] = USS[(size_t)(ro * 8u + (unsigned)k8)]; } } while (0)
; #define P12_COMP(i_, h_, CW_, SC_) do { _Pragma("unroll") for (int bb = 0; bb < 8; ++bb) { int a0 = 0, a1 = 0; P12_U4(CW_[bb].x, xa.x, xa.y, a0); P12_U4(CW_[bb].y, xa.z, xa.w, a1); P12_U4(CW_[bb].z, xb.x, xb.y, a0); P12_U4(CW_[bb].w, xb.z, xb.w, a1); \
;         psum[(i_)][(h_) * 8 + bb] += __uint_as_float(SC_[bb] << 16) * (float)((a0 + a1) - xo); } } while (0)
; #define P12_BAR() asm volatile("" ::: "memory")
; __device__ __forceinline__ void p12_peer(Frame& F) {
;     ...
;     { v4u cwA[8], cwB[8]; unsigned scA[8], scB[8]; v4u xa, xb; int xo;
;       P12_ISSUE(0, 0, 0, cwA, scA);
; _Pragma("nounroll")
;       for (int c = 0; c < 16; ++c) { const int cn = c + 1 < 16 ? c + 1 : 15;
;           P12_XQ(c, 0); P12_ISSUE(c, 0, 1, cwB, scB); P12_BAR(); P12_COMP(0, 0, cwA, scA); P12_ISSUE(c, 1, 0, cwA, scA); P12_BAR(); P12_COMP(0, 1, cwB, scB);
	v_lshl_or_b32 v7, v0, 4, v95
	s_waitcnt lgkmcnt(5)
	v_lshl_or_b32 v8, v2, 4, v95
	s_waitcnt lgkmcnt(3)
	v_lshl_or_b32 v9, v4, 4, v95
	s_waitcnt lgkmcnt(1)
	v_lshl_or_b32 v10, v6, 4, v95
	global_load_ushort v37, v7, s[18:19]
	global_load_ushort v38, v8, s[18:19]
	global_load_ushort v39, v9, s[18:19]
	global_load_ushort v40, v10, s[18:19]
	s_waitcnt lgkmcnt(0)
	v_lshl_or_b32 v10, v36, 4, v95
	v_lshl_or_b32 v0, v0, 7, v165
	v_lshl_or_b32 v7, v1, 4, v95
	v_lshl_or_b32 v8, v3, 4, v95
	v_lshl_or_b32 v9, v5, 4, v95
	global_load_ushort v41, v10, s[18:19]
	global_load_ushort v42, v9, s[18:19]
	global_load_ushort v43, v8, s[18:19]
	global_load_ushort v44, v7, s[18:19]
	global_load_dwordx4 v[28:31], v0, s[0:1]
	v_lshl_or_b32 v0, v1, 7, v165
	global_load_dwordx4 v[24:27], v0, s[0:1]
	v_lshl_or_b32 v0, v2, 7, v165
	global_load_dwordx4 v[20:23], v0, s[0:1]
	v_lshl_or_b32 v0, v3, 7, v165
	global_load_dwordx4 v[16:19], v0, s[0:1]
	v_lshl_or_b32 v0, v4, 7, v165
	global_load_dwordx4 v[12:15], v0, s[0:1]
	v_lshl_or_b32 v0, v5, 7, v165
	global_load_dwordx4 v[8:11], v0, s[0:1]
	v_lshl_or_b32 v0, v6, 7, v165
	global_load_dwordx4 v[4:7], v0, s[0:1]
	v_lshl_or_b32 v0, v36, 7, v165
	global_load_dwordx4 v[0:3], v0, s[0:1]
	v_add_f32_dpp v32, v32, v32 quad_perm:[2,3,0,1] row_mask:0xf bank_mask:0xf bound_ctrl:1
	s_waitcnt vmcnt(11)
	v_perm_b32 v40, v40, v41, s43
	v_add_f32_dpp v32, v32, v32 row_half_mirror row_mask:0xf bank_mask:0xf bound_ctrl:1
	s_waitcnt vmcnt(10)
	v_perm_b32 v41, v39, v42, s43
	s_waitcnt vmcnt(9)
	v_perm_b32 v42, v38, v43, s43
	v_add_f32_dpp v32, v32, v32 row_mirror row_mask:0xf bank_mask:0xf bound_ctrl:1
	s_waitcnt vmcnt(8)
	v_perm_b32 v43, v37, v44, s43
	v_readlane_b32 s21, v32, 0
	v_readlane_b32 s23, v32, 16
	v_readlane_b32 s22, v32, 32
	v_readlane_b32 s28, v32, 48
	ds_read_u16 v184, v93 offset:16384
	ds_read_u16 v185, v93 offset:16400
	ds_read_u16 v186, v93 offset:16416
	ds_read_u16 v187, v93 offset:16432
	ds_read_u16 v188, v93 offset:16448
	ds_read_u16 v189, v93 offset:16464
	ds_read_u16 v190, v93 offset:16480
	ds_read_u16 v191, v93 offset:16496
	ds_read_u16 v192, v93 offset:16512
	ds_read_u16 v193, v93 offset:16528
	ds_read_u16 v194, v93 offset:16544
	ds_read_u16 v195, v93 offset:16560
	s_waitcnt lgkmcnt(0)
	ds_read_u16 v196, v93 offset:16576
	ds_read_u16 v197, v93 offset:16592
	ds_read_u16 v198, v93 offset:16608
	ds_read_u16 v199, v93 offset:16624
	ds_read_u16 v200, v93 offset:16640
	ds_read_u16 v201, v93 offset:16656
	ds_read_u16 v202, v93 offset:16672
	ds_read_u16 v203, v93 offset:16688
	ds_read_u16 v204, v93 offset:16704
	ds_read_u16 v205, v93 offset:16720
	ds_read_u16 v206, v93 offset:16736
	ds_read_u16 v207, v93 offset:16752
	s_waitcnt lgkmcnt(0)
	ds_read_u16 v208, v93 offset:16768
	ds_read_u16 v209, v93 offset:16784
	ds_read_u16 v210, v93 offset:16800
	ds_read_u16 v211, v93 offset:16816
	ds_read_u16 v212, v93 offset:16832
	ds_read_u16 v213, v93 offset:16848
	ds_read_u16 v214, v93 offset:16864
	ds_read_u16 v215, v93 offset:16880
	ds_read_u16 v216, v93 offset:16896
	ds_read_u16 v217, v93 offset:16912
	ds_read_u16 v218, v93 offset:16928
	ds_read_u16 v219, v93 offset:16944
	s_waitcnt lgkmcnt(0)
	ds_read_u16 v220, v93 offset:16960
	ds_read_u16 v221, v93 offset:16976
	ds_read_u16 v222, v93 offset:16992
	ds_read_u16 v223, v93 offset:17008
	ds_read_u16 v224, v93 offset:17024
	ds_read_u16 v225, v93 offset:17040
	ds_read_u16 v226, v93 offset:17056
	ds_read_u16 v227, v93 offset:17072
	ds_read_u16 v228, v93 offset:17088
	ds_read_u16 v229, v93 offset:17104
	ds_read_u16 v230, v93 offset:17120
	ds_read_u16 v231, v93 offset:17136
	s_waitcnt lgkmcnt(0)
	ds_read_u16 v232, v93 offset:17152
	ds_read_u16 v233, v93 offset:17168
	ds_read_u16 v234, v93 offset:17184
	ds_read_u16 v235, v93 offset:17200
	ds_read_u16 v236, v93 offset:17216
	ds_read_u16 v237, v93 offset:17232
	ds_read_u16 v238, v93 offset:17248
	ds_read_u16 v239, v93 offset:17264
	ds_read_u16 v240, v93 offset:17280
	ds_read_u16 v241, v93 offset:17296
	ds_read_u16 v242, v93 offset:17312
	ds_read_u16 v243, v93 offset:17328
	s_waitcnt lgkmcnt(0)
	ds_read_u16 v244, v93 offset:17344
	ds_read_u16 v245, v93 offset:17360
	ds_read_u16 v246, v93 offset:17376
	ds_read_u16 v247, v93 offset:17392
	s_waitcnt lgkmcnt(0)
.LBB0_3272:
	ds_read_b128 v[36:39], v166
	ds_read_b128 v[32:35], v166 offset:16
	v_mov_b32_e32 v48, 0
	v_add_u32_e32 v44, s44, v192
	v_lshl_or_b32 v49, v44, 7, v165
	global_load_dwordx4 v[88:91], v49, s[0:1]
	v_lshl_or_b32 v49, v44, 4, v95
	v_add_u32_e32 v44, s44, v193
	v_lshl_or_b32 v45, v44, 7, v165
	v_lshl_or_b32 v50, v44, 4, v95
	v_add_u32_e32 v44, s44, v194
	global_load_dwordx4 v[84:87], v45, s[0:1]
	v_lshl_or_b32 v45, v44, 7, v165
	v_lshl_or_b32 v51, v44, 4, v95
	v_add_u32_e32 v44, s44, v195
	global_load_dwordx4 v[80:83], v45, s[0:1]
	v_lshl_or_b32 v45, v44, 7, v165
	v_lshl_or_b32 v56, v44, 4, v95
	global_load_dwordx4 v[76:79], v45, s[0:1]
	s_waitcnt lgkmcnt(0)
	v_dot4c_i32_i8_e32 v48, 0x1010101, v36
	v_dot4c_i32_i8_e32 v48, 0x1010101, v37
	v_dot4c_i32_i8_e32 v48, 0x1010101, v38
	v_add_u32_e32 v44, s44, v196
	v_lshl_or_b32 v45, v44, 7, v165
	v_lshl_or_b32 v57, v44, 4, v95
	global_load_dwordx4 v[68:71], v45, s[0:1]
	v_dot4c_i32_i8_e32 v48, 0x1010101, v39
	v_dot4c_i32_i8_e32 v48, 0x1010101, v32
	v_dot4c_i32_i8_e32 v48, 0x1010101, v33
	v_add_u32_e32 v44, s44, v197
	v_lshl_or_b32 v45, v44, 7, v165
	v_lshl_or_b32 v58, v44, 4, v95
	global_load_dwordx4 v[60:63], v45, s[0:1]
	v_dot4c_i32_i8_e32 v48, 0x1010101, v34
	v_dot4c_i32_i8_e32 v48, 0x1010101, v35
	s_add_i32 s45, s44, 0x4000
	v_add_u32_e32 v44, s44, v198
	v_lshl_or_b32 v45, v44, 7, v165
	v_lshl_or_b32 v59, v44, 4, v95
	global_load_dwordx4 v[52:55], v45, s[0:1]
	v_lshlrev_b32_e32 v171, 3, v48
	s_waitcnt vmcnt(14)
; #define P12_ISSUE(c_, i_, h_, CW_, SC_) do { _Pragma("unroll") for (int bb = 0; bb < 8; ++bb) { const unsigned ro = (unsigned)(c_) * 16384u + (unsigned)EL[(i_) * 128 + ((h_) * 8 + bb) * 8 + g8]; \
;         CW_[bb] = *(const v4u*)(U4 + (size_t)(ro * 128u + 16u * (unsigned)k8)); SC_[bb] = USS[(size_t)(ro * 8u + (unsigned)k8)]; } } while (0)
; #define P12_COMP(i_, h_, CW_, SC_) do { _Pragma("unroll") for (int bb = 0; bb < 8; ++bb) { int a0 = 0, a1 = 0; P12_U4(CW_[bb].x, xa.x, xa.y, a0); P12_U4(CW_[bb].y, xa.z, xa.w, a1); P12_U4(CW_[bb].z, xb.x, xb.y, a0); P12_U4(CW_[bb].w, xb.z, xb.w, a1); \
;         psum[(i_)][(h_) * 8 + bb] += __uint_as_float(SC_[bb] << 16) * (float)((a0 + a1) - xo); } } while (0)
; #define P12_BAR() asm volatile("" ::: "memory")
; __device__ __forceinline__ void p12_peer(Frame& F) {
;     ...
;     { v4u cwA[8], cwB[8]; unsigned scA[8], scB[8]; v4u xa, xb; int xo;
;       P12_ISSUE(0, 0, 0, cwA, scA);
; _Pragma("nounroll")
;       for (int c = 0; c < 16; ++c) { const int cn = c + 1 < 16 ? c + 1 : 15;
;           P12_XQ(c, 0); P12_ISSUE(c, 0, 1, cwB, scB); P12_BAR(); P12_COMP(0, 0, cwA, scA); P12_ISSUE(c, 1, 0, cwA, scA); P12_BAR(); P12_COMP(0, 1, cwB, scB);
	v_and_b32_e32 v48, 0xf0f0f0f, v28
	v_lshrrev_b32_e32 v28, 4, v28
	v_add_u32_e32 v64, s44, v199
	v_lshl_or_b32 v44, v64, 7, v165
	global_load_dwordx4 v[44:47], v44, s[0:1]
	v_lshl_or_b32 v64, v64, 4, v95
	global_load_ushort v182, v50, s[18:19]
	global_load_ushort v183, v49, s[18:19]
	global_load_ushort v180, v56, s[18:19]
	global_load_ushort v181, v51, s[18:19]
	global_load_ushort v176, v58, s[18:19]
	global_load_ushort v177, v57, s[18:19]
	global_load_ushort v172, v64, s[18:19]
	global_load_ushort v173, v59, s[18:19]
	v_mov_b32_e32 v49, 0
	v_dot4c_i32_i8_e32 v49, v48, v36
	v_and_b32_e32 v28, 0xf0f0f0f, v28
	v_dot4c_i32_i8_e32 v49, v28, v37
	v_and_b32_e32 v28, 0xf0f0f0f, v29
	v_mov_b32_e32 v48, 0
	v_dot4c_i32_i8_e32 v48, v28, v38
	v_lshrrev_b32_e32 v28, 4, v29
	v_and_b32_e32 v28, 0xf0f0f0f, v28
	v_dot4c_i32_i8_e32 v48, v28, v39
	v_and_b32_e32 v28, 0xf0f0f0f, v30
	v_dot4c_i32_i8_e32 v49, v28, v32
	v_lshrrev_b32_e32 v28, 4, v30
	v_and_b32_e32 v28, 0xf0f0f0f, v28
	v_dot4c_i32_i8_e32 v49, v28, v33
	v_and_b32_e32 v28, 0xf0f0f0f, v31
	v_dot4c_i32_i8_e32 v48, v28, v34
	v_lshrrev_b32_e32 v28, 4, v31
	v_and_b32_e32 v28, 0xf0f0f0f, v28
	v_dot4c_i32_i8_e32 v48, v28, v35
	s_waitcnt vmcnt(22)
	v_and_b32_e32 v28, 0xf0f0f0f, v24
	v_mov_b32_e32 v29, 0
	v_lshrrev_b32_e32 v24, 4, v24
	v_dot4c_i32_i8_e32 v29, v28, v36
	v_and_b32_e32 v24, 0xf0f0f0f, v24
	v_dot4c_i32_i8_e32 v29, v24, v37
	v_and_b32_e32 v24, 0xf0f0f0f, v25
	v_mov_b32_e32 v28, 0
	v_dot4c_i32_i8_e32 v28, v24, v38
	v_lshrrev_b32_e32 v24, 4, v25
	v_and_b32_e32 v24, 0xf0f0f0f, v24
	v_dot4c_i32_i8_e32 v28, v24, v39
	v_and_b32_e32 v24, 0xf0f0f0f, v26
	v_dot4c_i32_i8_e32 v29, v24, v32
	v_lshrrev_b32_e32 v24, 4, v26
	v_and_b32_e32 v24, 0xf0f0f0f, v24
	v_dot4c_i32_i8_e32 v29, v24, v33
	v_and_b32_e32 v24, 0xf0f0f0f, v27
	v_dot4c_i32_i8_e32 v28, v24, v34
	v_lshrrev_b32_e32 v24, 4, v27
	v_and_b32_e32 v24, 0xf0f0f0f, v24
	v_dot4c_i32_i8_e32 v28, v24, v35
	v_add_u32_e32 v26, v49, v48
	v_sub_u32_e32 v26, v26, v171
	v_and_b32_e32 v25, 0xffff0000, v43
	v_add_u32_e32 v27, v29, v28
	v_sub_u32_e32 v28, v27, v171
	v_cvt_f32_i32_e32 v27, v26
	v_cvt_f32_i32_e32 v26, v28
	v_lshlrev_b32_e32 v24, 16, v43
	s_cmp_eq_u32 s44, 0x3c000
	v_pk_fma_f32 v[158:159], v[24:25], v[26:27], v[158:159]
	s_waitcnt vmcnt(21)
	v_and_b32_e32 v24, 0xf0f0f0f, v20
	v_mov_b32_e32 v25, 0
	v_lshrrev_b32_e32 v20, 4, v20
	v_dot4c_i32_i8_e32 v25, v24, v36
	v_and_b32_e32 v20, 0xf0f0f0f, v20
	v_dot4c_i32_i8_e32 v25, v20, v37
	v_and_b32_e32 v20, 0xf0f0f0f, v21
	v_mov_b32_e32 v24, 0
	v_dot4c_i32_i8_e32 v24, v20, v38
	v_lshrrev_b32_e32 v20, 4, v21
	v_and_b32_e32 v20, 0xf0f0f0f, v20
	v_dot4c_i32_i8_e32 v24, v20, v39
	v_and_b32_e32 v20, 0xf0f0f0f, v22
	v_dot4c_i32_i8_e32 v25, v20, v32
	v_lshrrev_b32_e32 v20, 4, v22
	v_and_b32_e32 v20, 0xf0f0f0f, v20
	v_dot4c_i32_i8_e32 v25, v20, v33
	v_and_b32_e32 v20, 0xf0f0f0f, v23
	v_dot4c_i32_i8_e32 v24, v20, v34
	v_lshrrev_b32_e32 v20, 4, v23
	v_and_b32_e32 v20, 0xf0f0f0f, v20
	v_dot4c_i32_i8_e32 v24, v20, v35
	s_waitcnt vmcnt(20)
	v_and_b32_e32 v20, 0xf0f0f0f, v16
	v_mov_b32_e32 v21, 0
	v_lshrrev_b32_e32 v16, 4, v16
	v_dot4c_i32_i8_e32 v21, v20, v36
	v_and_b32_e32 v16, 0xf0f0f0f, v16
	v_dot4c_i32_i8_e32 v21, v16, v37
	v_and_b32_e32 v16, 0xf0f0f0f, v17
	v_mov_b32_e32 v20, 0
	v_dot4c_i32_i8_e32 v20, v16, v38
	v_lshrrev_b32_e32 v16, 4, v17
	v_and_b32_e32 v16, 0xf0f0f0f, v16
	v_dot4c_i32_i8_e32 v20, v16, v39
	v_and_b32_e32 v16, 0xf0f0f0f, v18
	v_dot4c_i32_i8_e32 v21, v16, v32
	v_lshrrev_b32_e32 v16, 4, v18
	v_and_b32_e32 v16, 0xf0f0f0f, v16
	v_dot4c_i32_i8_e32 v21, v16, v33
	v_and_b32_e32 v16, 0xf0f0f0f, v19
	v_dot4c_i32_i8_e32 v20, v16, v34
	v_lshrrev_b32_e32 v16, 4, v19
	v_and_b32_e32 v16, 0xf0f0f0f, v16
	v_dot4c_i32_i8_e32 v20, v16, v35
	v_add_u32_e32 v18, v25, v24
	v_sub_u32_e32 v18, v18, v171
	v_and_b32_e32 v17, 0xffff0000, v42
	v_add_u32_e32 v19, v21, v20
	v_sub_u32_e32 v20, v19, v171
	v_cvt_f32_i32_e32 v19, v18
	v_cvt_f32_i32_e32 v18, v20
	v_lshlrev_b32_e32 v16, 16, v42
	v_pk_fma_f32 v[156:157], v[16:17], v[18:19], v[156:157]
	s_waitcnt vmcnt(19)
	v_and_b32_e32 v16, 0xf0f0f0f, v12
	v_mov_b32_e32 v17, 0
	v_lshrrev_b32_e32 v12, 4, v12
	v_dot4c_i32_i8_e32 v17, v16, v36
	v_and_b32_e32 v12, 0xf0f0f0f, v12
	v_dot4c_i32_i8_e32 v17, v12, v37
	v_and_b32_e32 v12, 0xf0f0f0f, v13
	v_mov_b32_e32 v16, 0
	v_dot4c_i32_i8_e32 v16, v12, v38
	v_lshrrev_b32_e32 v12, 4, v13
	v_and_b32_e32 v12, 0xf0f0f0f, v12
	v_dot4c_i32_i8_e32 v16, v12, v39
	v_and_b32_e32 v12, 0xf0f0f0f, v14
	v_dot4c_i32_i8_e32 v17, v12, v32
	v_lshrrev_b32_e32 v12, 4, v14
	v_and_b32_e32 v12, 0xf0f0f0f, v12
	v_dot4c_i32_i8_e32 v17, v12, v33
	v_and_b32_e32 v12, 0xf0f0f0f, v15
	v_dot4c_i32_i8_e32 v16, v12, v34
	v_lshrrev_b32_e32 v12, 4, v15
	v_and_b32_e32 v12, 0xf0f0f0f, v12
	v_dot4c_i32_i8_e32 v16, v12, v35
	s_waitcnt vmcnt(18)
	v_and_b32_e32 v12, 0xf0f0f0f, v8
	v_mov_b32_e32 v13, 0
	v_lshrrev_b32_e32 v8, 4, v8
	v_dot4c_i32_i8_e32 v13, v12, v36
	v_and_b32_e32 v8, 0xf0f0f0f, v8
	v_dot4c_i32_i8_e32 v13, v8, v37
	v_and_b32_e32 v8, 0xf0f0f0f, v9
	v_mov_b32_e32 v12, 0
	v_dot4c_i32_i8_e32 v12, v8, v38
	v_lshrrev_b32_e32 v8, 4, v9
	v_and_b32_e32 v8, 0xf0f0f0f, v8
	v_dot4c_i32_i8_e32 v12, v8, v39
	v_and_b32_e32 v8, 0xf0f0f0f, v10
	v_dot4c_i32_i8_e32 v13, v8, v32
	v_lshrrev_b32_e32 v8, 4, v10
	v_and_b32_e32 v8, 0xf0f0f0f, v8
	v_dot4c_i32_i8_e32 v13, v8, v33
	v_and_b32_e32 v8, 0xf0f0f0f, v11
	v_dot4c_i32_i8_e32 v12, v8, v34
	v_lshrrev_b32_e32 v8, 4, v11
	v_and_b32_e32 v8, 0xf0f0f0f, v8
	v_dot4c_i32_i8_e32 v12, v8, v35
	v_add_u32_e32 v10, v17, v16
	v_sub_u32_e32 v10, v10, v171
	v_and_b32_e32 v9, 0xffff0000, v41
	v_add_u32_e32 v11, v13, v12
	v_sub_u32_e32 v12, v11, v171
	v_cvt_f32_i32_e32 v11, v10
	v_cvt_f32_i32_e32 v10, v12
	v_lshlrev_b32_e32 v8, 16, v41
	v_pk_fma_f32 v[154:155], v[8:9], v[10:11], v[154:155]
	s_waitcnt vmcnt(17)
; #define P12_ISSUE(c_, i_, h_, CW_, SC_) do { _Pragma("unroll") for (int bb = 0; bb < 8; ++bb) { const unsigned ro = (unsigned)(c_) * 16384u + (unsigned)EL[(i_) * 128 + ((h_) * 8 + bb) * 8 + g8]; \
;         CW_[bb] = *(const v4u*)(U4 + (size_t)(ro * 128u + 16u * (unsigned)k8)); SC_[bb] = USS[(size_t)(ro * 8u + (unsigned)k8)]; } } while (0)
; #define P12_COMP(i_, h_, CW_, SC_) do { _Pragma("unroll") for (int bb = 0; bb < 8; ++bb) { int a0 = 0, a1 = 0; P12_U4(CW_[bb].x, xa.x, xa.y, a0); P12_U4(CW_[bb].y, xa.z, xa.w, a1); P12_U4(CW_[bb].z, xb.x, xb.y, a0); P12_U4(CW_[bb].w, xb.z, xb.w, a1); \
;         psum[(i_)][(h_) * 8 + bb] += __uint_as_float(SC_[bb] << 16) * (float)((a0 + a1) - xo); } } while (0)
; #define P12_BAR() asm volatile("" ::: "memory")
; __device__ __forceinline__ void p12_peer(Frame& F) {
;     ...
;     { v4u cwA[8], cwB[8]; unsigned scA[8], scB[8]; v4u xa, xb; int xo;
;       P12_ISSUE(0, 0, 0, cwA, scA);
; _Pragma("nounroll")
;       for (int c = 0; c < 16; ++c) { const int cn = c + 1 < 16 ? c + 1 : 15;
;           P12_XQ(c, 0); P12_ISSUE(c, 0, 1, cwB, scB); P12_BAR(); P12_COMP(0, 0, cwA, scA); P12_ISSUE(c, 1, 0, cwA, scA); P12_BAR(); P12_COMP(0, 1, cwB, scB);
;           P12_XQ(c, 1); P12_ISSUE(c, 1, 1, cwB, scB); P12_BAR(); P12_COMP(1, 0, cwA, scA); P12_ISSUE(c, 2, 0, cwA, scA); P12_BAR(); P12_COMP(1, 1, cwB, scB);
;           P12_XQ(c, 2); P12_ISSUE(c, 2, 1, cwB, scB); P12_BAR(); P12_COMP(2, 0, cwA, scA); P12_ISSUE(c, 3, 0, cwA, scA); P12_BAR(); P12_COMP(2, 1, cwB, scB);
;           P12_XQ(c, 3); P12_ISSUE(c, 3, 1, cwB, scB); P12_BAR(); P12_COMP(3, 0, cwA, scA); P12_ISSUE(cn, 0, 0, cwA, scA); P12_BAR(); P12_COMP(3, 1, cwB, scB);
;       } }
	v_and_b32_e32 v8, 0xf0f0f0f, v4
	v_mov_b32_e32 v9, 0
	v_lshrrev_b32_e32 v4, 4, v4
	v_dot4c_i32_i8_e32 v9, v8, v36
	v_and_b32_e32 v4, 0xf0f0f0f, v4
	v_dot4c_i32_i8_e32 v9, v4, v37
	v_and_b32_e32 v4, 0xf0f0f0f, v5
	v_mov_b32_e32 v8, 0
	v_dot4c_i32_i8_e32 v8, v4, v38
	v_lshrrev_b32_e32 v4, 4, v5
	v_and_b32_e32 v4, 0xf0f0f0f, v4
	v_dot4c_i32_i8_e32 v8, v4, v39
	v_and_b32_e32 v4, 0xf0f0f0f, v6
	v_dot4c_i32_i8_e32 v9, v4, v32
	v_lshrrev_b32_e32 v4, 4, v6
	v_and_b32_e32 v4, 0xf0f0f0f, v4
	v_dot4c_i32_i8_e32 v9, v4, v33
	v_and_b32_e32 v4, 0xf0f0f0f, v7
	v_dot4c_i32_i8_e32 v8, v4, v34
	v_lshrrev_b32_e32 v4, 4, v7
	v_and_b32_e32 v4, 0xf0f0f0f, v4
	v_dot4c_i32_i8_e32 v8, v4, v35
	s_waitcnt vmcnt(16)
	v_and_b32_e32 v4, 0xf0f0f0f, v0
	v_mov_b32_e32 v5, 0
	v_lshrrev_b32_e32 v0, 4, v0
	v_dot4c_i32_i8_e32 v5, v4, v36
	v_and_b32_e32 v0, 0xf0f0f0f, v0
	v_dot4c_i32_i8_e32 v5, v0, v37
	v_and_b32_e32 v0, 0xf0f0f0f, v1
	v_mov_b32_e32 v4, 0
	v_dot4c_i32_i8_e32 v4, v0, v38
	v_lshrrev_b32_e32 v0, 4, v1
	v_and_b32_e32 v0, 0xf0f0f0f, v0
	v_dot4c_i32_i8_e32 v4, v0, v39
	v_and_b32_e32 v0, 0xf0f0f0f, v2
	v_dot4c_i32_i8_e32 v5, v0, v32
	v_lshrrev_b32_e32 v0, 4, v2
	v_and_b32_e32 v0, 0xf0f0f0f, v0
	v_dot4c_i32_i8_e32 v5, v0, v33
	v_and_b32_e32 v0, 0xf0f0f0f, v3
	v_dot4c_i32_i8_e32 v4, v0, v34
	v_lshrrev_b32_e32 v0, 4, v3
	v_and_b32_e32 v0, 0xf0f0f0f, v0
	v_dot4c_i32_i8_e32 v4, v0, v35
	v_add_u32_e32 v2, v9, v8
	v_sub_u32_e32 v2, v2, v171
	v_and_b32_e32 v1, 0xffff0000, v40
	v_add_u32_e32 v3, v5, v4
	v_sub_u32_e32 v4, v3, v171
	v_cvt_f32_i32_e32 v3, v2
	v_cvt_f32_i32_e32 v2, v4
	v_lshlrev_b32_e32 v0, 16, v40
	v_pk_fma_f32 v[152:153], v[0:1], v[2:3], v[152:153]
	v_add_u32_e32 v0, s44, v200
	v_lshl_or_b32 v4, v0, 7, v165
	v_add_u32_e32 v1, s44, v201
	global_load_dwordx4 v[72:75], v4, s[0:1]
	v_lshl_or_b32 v4, v1, 7, v165
	v_add_u32_e32 v2, s44, v202
	global_load_dwordx4 v[64:67], v4, s[0:1]
	v_lshl_or_b32 v4, v2, 7, v165
	v_add_u32_e32 v3, s44, v203
	global_load_dwordx4 v[56:59], v4, s[0:1]
	v_lshl_or_b32 v4, v3, 7, v165
	global_load_dwordx4 v[48:51], v4, s[0:1]
	v_lshl_or_b32 v0, v0, 4, v95
	v_lshl_or_b32 v1, v1, 4, v95
	v_lshl_or_b32 v2, v2, 4, v95
	v_lshl_or_b32 v3, v3, 4, v95
	v_add_u32_e32 v4, s44, v204
	v_lshl_or_b32 v5, v4, 7, v165
	global_load_dwordx4 v[40:43], v5, s[0:1]
	v_lshl_or_b32 v4, v4, 4, v95
	v_add_u32_e32 v5, s44, v205
	v_lshl_or_b32 v6, v5, 7, v165
	global_load_dwordx4 v[24:27], v6, s[0:1]
	v_lshl_or_b32 v5, v5, 4, v95
	v_add_u32_e32 v6, s44, v206
	v_lshl_or_b32 v7, v6, 7, v165
	global_load_dwordx4 v[12:15], v7, s[0:1]
	v_lshl_or_b32 v6, v6, 4, v95
	v_add_u32_e32 v7, s44, v207
	v_lshl_or_b32 v8, v7, 7, v165
	global_load_dwordx4 v[8:11], v8, s[0:1]
	v_lshl_or_b32 v7, v7, 4, v95
	global_load_ushort v178, v1, s[18:19]
	global_load_ushort v179, v0, s[18:19]
	global_load_ushort v174, v3, s[18:19]
	global_load_ushort v175, v2, s[18:19]
	global_load_ushort v169, v5, s[18:19]
	global_load_ushort v170, v4, s[18:19]
	global_load_ushort v167, v7, s[18:19]
	global_load_ushort v168, v6, s[18:19]
	s_waitcnt vmcnt(31)
	v_and_b32_e32 v0, 0xf0f0f0f, v88
	v_mov_b32_e32 v2, 0
	v_dot4c_i32_i8_e32 v2, v0, v36
	v_lshrrev_b32_e32 v0, 4, v88
	v_and_b32_e32 v0, 0xf0f0f0f, v0
	v_dot4c_i32_i8_e32 v2, v0, v37
	v_and_b32_e32 v0, 0xf0f0f0f, v89
	v_mov_b32_e32 v3, 0
	v_dot4c_i32_i8_e32 v3, v0, v38
	v_lshrrev_b32_e32 v0, 4, v89
	v_and_b32_e32 v0, 0xf0f0f0f, v0
	v_dot4c_i32_i8_e32 v3, v0, v39
	v_and_b32_e32 v0, 0xf0f0f0f, v90
	v_dot4c_i32_i8_e32 v2, v0, v32
	v_lshrrev_b32_e32 v0, 4, v90
	v_and_b32_e32 v0, 0xf0f0f0f, v0
	v_dot4c_i32_i8_e32 v2, v0, v33
	v_and_b32_e32 v0, 0xf0f0f0f, v91
	v_dot4c_i32_i8_e32 v3, v0, v34
	v_lshrrev_b32_e32 v0, 4, v91
	v_and_b32_e32 v0, 0xf0f0f0f, v0
	v_dot4c_i32_i8_e32 v3, v0, v35
	s_waitcnt vmcnt(30)
	v_and_b32_e32 v0, 0xf0f0f0f, v84
	v_mov_b32_e32 v4, 0
	v_dot4c_i32_i8_e32 v4, v0, v36
	v_lshrrev_b32_e32 v0, 4, v84
	v_and_b32_e32 v0, 0xf0f0f0f, v0
	v_dot4c_i32_i8_e32 v4, v0, v37
	v_and_b32_e32 v0, 0xf0f0f0f, v85
	v_mov_b32_e32 v5, 0
	v_dot4c_i32_i8_e32 v5, v0, v38
	v_lshrrev_b32_e32 v0, 4, v85
	v_and_b32_e32 v0, 0xf0f0f0f, v0
	v_dot4c_i32_i8_e32 v5, v0, v39
	v_and_b32_e32 v0, 0xf0f0f0f, v86
	v_dot4c_i32_i8_e32 v4, v0, v32
	v_lshrrev_b32_e32 v0, 4, v86
	v_and_b32_e32 v0, 0xf0f0f0f, v0
	v_dot4c_i32_i8_e32 v4, v0, v33
	v_and_b32_e32 v0, 0xf0f0f0f, v87
	v_dot4c_i32_i8_e32 v5, v0, v34
	v_lshrrev_b32_e32 v0, 4, v87
	v_and_b32_e32 v0, 0xf0f0f0f, v0
	v_dot4c_i32_i8_e32 v5, v0, v35
	v_add_u32_e32 v2, v2, v3
	v_sub_u32_e32 v2, v2, v171
	s_waitcnt vmcnt(22)
	v_lshlrev_b32_e32 v1, 16, v183
	v_sub_u32_e32 v3, v5, v171
	v_add_u32_e32 v4, v3, v4
	v_cvt_f32_i32_e32 v3, v2
	v_cvt_f32_i32_e32 v2, v4
	v_lshlrev_b32_e32 v0, 16, v182
	v_mov_b32_e32 v4, 0
	v_mov_b32_e32 v5, 0
	v_pk_fma_f32 v[150:151], v[0:1], v[2:3], v[150:151]
	v_and_b32_e32 v0, 0xf0f0f0f, v80
	v_mov_b32_e32 v2, 0
	v_dot4c_i32_i8_e32 v2, v0, v36
	v_lshrrev_b32_e32 v0, 4, v80
	v_and_b32_e32 v0, 0xf0f0f0f, v0
	v_dot4c_i32_i8_e32 v2, v0, v37
	v_and_b32_e32 v0, 0xf0f0f0f, v81
	v_mov_b32_e32 v3, 0
	v_dot4c_i32_i8_e32 v3, v0, v38
	v_lshrrev_b32_e32 v0, 4, v81
	v_and_b32_e32 v0, 0xf0f0f0f, v0
	v_dot4c_i32_i8_e32 v3, v0, v39
	v_and_b32_e32 v0, 0xf0f0f0f, v82
	v_dot4c_i32_i8_e32 v2, v0, v32
	v_lshrrev_b32_e32 v0, 4, v82
	v_and_b32_e32 v0, 0xf0f0f0f, v0
	v_dot4c_i32_i8_e32 v2, v0, v33
	v_and_b32_e32 v0, 0xf0f0f0f, v83
	v_dot4c_i32_i8_e32 v3, v0, v34
	v_lshrrev_b32_e32 v0, 4, v83
	v_and_b32_e32 v0, 0xf0f0f0f, v0
	v_dot4c_i32_i8_e32 v3, v0, v35
	v_and_b32_e32 v0, 0xf0f0f0f, v76
	v_dot4c_i32_i8_e32 v4, v0, v36
	v_lshrrev_b32_e32 v0, 4, v76
	v_and_b32_e32 v0, 0xf0f0f0f, v0
	v_dot4c_i32_i8_e32 v4, v0, v37
	v_and_b32_e32 v0, 0xf0f0f0f, v77
	v_dot4c_i32_i8_e32 v5, v0, v38
	v_lshrrev_b32_e32 v0, 4, v77
	v_and_b32_e32 v0, 0xf0f0f0f, v0
	v_dot4c_i32_i8_e32 v5, v0, v39
	v_and_b32_e32 v0, 0xf0f0f0f, v78
	v_dot4c_i32_i8_e32 v4, v0, v32
	v_lshrrev_b32_e32 v0, 4, v78
	v_and_b32_e32 v0, 0xf0f0f0f, v0
	v_dot4c_i32_i8_e32 v4, v0, v33
	v_and_b32_e32 v0, 0xf0f0f0f, v79
	v_dot4c_i32_i8_e32 v5, v0, v34
	v_lshrrev_b32_e32 v0, 4, v79
	v_and_b32_e32 v0, 0xf0f0f0f, v0
	v_dot4c_i32_i8_e32 v5, v0, v35
	v_sub_u32_e32 v3, v3, v171
	v_add_u32_e32 v2, v3, v2
	v_cvt_f32_i32_e32 v3, v2
	v_sub_u32_e32 v5, v5, v171
	v_add_u32_e32 v4, v5, v4
	v_cvt_f32_i32_e32 v2, v4
	s_waitcnt vmcnt(20)
; #define P12_ISSUE(c_, i_, h_, CW_, SC_) do { _Pragma("unroll") for (int bb = 0; bb < 8; ++bb) { const unsigned ro = (unsigned)(c_) * 16384u + (unsigned)EL[(i_) * 128 + ((h_) * 8 + bb) * 8 + g8]; \
;         CW_[bb] = *(const v4u*)(U4 + (size_t)(ro * 128u + 16u * (unsigned)k8)); SC_[bb] = USS[(size_t)(ro * 8u + (unsigned)k8)]; } } while (0)
; #define P12_COMP(i_, h_, CW_, SC_) do { _Pragma("unroll") for (int bb = 0; bb < 8; ++bb) { int a0 = 0, a1 = 0; P12_U4(CW_[bb].x, xa.x, xa.y, a0); P12_U4(CW_[bb].y, xa.z, xa.w, a1); P12_U4(CW_[bb].z, xb.x, xb.y, a0); P12_U4(CW_[bb].w, xb.z, xb.w, a1); \
;         psum[(i_)][(h_) * 8 + bb] += __uint_as_float(SC_[bb] << 16) * (float)((a0 + a1) - xo); } } while (0)
; #define P12_BAR() asm volatile("" ::: "memory")
; __device__ __forceinline__ void p12_peer(Frame& F) {
;     ...
;     { v4u cwA[8], cwB[8]; unsigned scA[8], scB[8]; v4u xa, xb; int xo;
;       P12_ISSUE(0, 0, 0, cwA, scA);
; _Pragma("nounroll")
;       for (int c = 0; c < 16; ++c) { const int cn = c + 1 < 16 ? c + 1 : 15;
;           P12_XQ(c, 0); P12_ISSUE(c, 0, 1, cwB, scB); P12_BAR(); P12_COMP(0, 0, cwA, scA); P12_ISSUE(c, 1, 0, cwA, scA); P12_BAR(); P12_COMP(0, 1, cwB, scB);
;           P12_XQ(c, 1); P12_ISSUE(c, 1, 1, cwB, scB); P12_BAR(); P12_COMP(1, 0, cwA, scA); P12_ISSUE(c, 2, 0, cwA, scA); P12_BAR(); P12_COMP(1, 1, cwB, scB);
;           P12_XQ(c, 2); P12_ISSUE(c, 2, 1, cwB, scB); P12_BAR(); P12_COMP(2, 0, cwA, scA); P12_ISSUE(c, 3, 0, cwA, scA); P12_BAR(); P12_COMP(2, 1, cwB, scB);
;           P12_XQ(c, 3); P12_ISSUE(c, 3, 1, cwB, scB); P12_BAR(); P12_COMP(3, 0, cwA, scA); P12_ISSUE(cn, 0, 0, cwA, scA); P12_BAR(); P12_COMP(3, 1, cwB, scB);
;       } }
	v_lshlrev_b32_e32 v1, 16, v181
	v_lshlrev_b32_e32 v0, 16, v180
	v_mov_b32_e32 v4, 0
	v_pk_fma_f32 v[148:149], v[0:1], v[2:3], v[148:149]
	v_and_b32_e32 v0, 0xf0f0f0f, v68
	v_mov_b32_e32 v2, 0
	v_dot4c_i32_i8_e32 v2, v0, v36
	v_lshrrev_b32_e32 v0, 4, v68
	v_and_b32_e32 v0, 0xf0f0f0f, v0
	v_dot4c_i32_i8_e32 v2, v0, v37
	v_and_b32_e32 v0, 0xf0f0f0f, v69
	v_mov_b32_e32 v3, 0
	v_dot4c_i32_i8_e32 v3, v0, v38
	v_lshrrev_b32_e32 v0, 4, v69
	v_and_b32_e32 v0, 0xf0f0f0f, v0
	v_dot4c_i32_i8_e32 v3, v0, v39
	v_and_b32_e32 v0, 0xf0f0f0f, v70
	v_dot4c_i32_i8_e32 v2, v0, v32
	v_lshrrev_b32_e32 v0, 4, v70
	v_and_b32_e32 v0, 0xf0f0f0f, v0
	v_dot4c_i32_i8_e32 v2, v0, v33
	v_and_b32_e32 v0, 0xf0f0f0f, v71
	v_dot4c_i32_i8_e32 v3, v0, v34
	v_lshrrev_b32_e32 v0, 4, v71
	v_and_b32_e32 v0, 0xf0f0f0f, v0
	v_dot4c_i32_i8_e32 v3, v0, v35
	v_and_b32_e32 v0, 0xf0f0f0f, v60
	v_dot4c_i32_i8_e32 v4, v0, v36
	v_lshrrev_b32_e32 v0, 4, v60
	v_and_b32_e32 v0, 0xf0f0f0f, v0
	v_dot4c_i32_i8_e32 v4, v0, v37
	v_and_b32_e32 v0, 0xf0f0f0f, v61
	v_mov_b32_e32 v5, 0
	v_dot4c_i32_i8_e32 v5, v0, v38
	v_lshrrev_b32_e32 v0, 4, v61
	v_and_b32_e32 v0, 0xf0f0f0f, v0
	v_dot4c_i32_i8_e32 v5, v0, v39
	v_and_b32_e32 v0, 0xf0f0f0f, v62
	v_dot4c_i32_i8_e32 v4, v0, v32
	v_lshrrev_b32_e32 v0, 4, v62
	v_and_b32_e32 v0, 0xf0f0f0f, v0
	v_dot4c_i32_i8_e32 v4, v0, v33
	v_and_b32_e32 v0, 0xf0f0f0f, v63
	v_dot4c_i32_i8_e32 v5, v0, v34
	v_lshrrev_b32_e32 v0, 4, v63
	v_and_b32_e32 v0, 0xf0f0f0f, v0
	v_dot4c_i32_i8_e32 v5, v0, v35
	v_sub_u32_e32 v3, v3, v171
	v_add_u32_e32 v2, v3, v2
	v_cvt_f32_i32_e32 v3, v2
	v_sub_u32_e32 v5, v5, v171
	v_add_u32_e32 v4, v5, v4
	v_cvt_f32_i32_e32 v2, v4
	s_waitcnt vmcnt(18)
	v_lshlrev_b32_e32 v1, 16, v177
	v_lshlrev_b32_e32 v0, 16, v176
	v_mov_b32_e32 v4, 0
	v_pk_fma_f32 v[146:147], v[0:1], v[2:3], v[146:147]
	v_and_b32_e32 v0, 0xf0f0f0f, v52
	v_mov_b32_e32 v2, 0
	v_dot4c_i32_i8_e32 v2, v0, v36
	v_lshrrev_b32_e32 v0, 4, v52
	v_and_b32_e32 v0, 0xf0f0f0f, v0
	v_dot4c_i32_i8_e32 v2, v0, v37
	v_and_b32_e32 v0, 0xf0f0f0f, v53
	v_mov_b32_e32 v3, 0
	v_dot4c_i32_i8_e32 v3, v0, v38
	v_lshrrev_b32_e32 v0, 4, v53
	v_and_b32_e32 v0, 0xf0f0f0f, v0
	v_dot4c_i32_i8_e32 v3, v0, v39
	v_and_b32_e32 v0, 0xf0f0f0f, v54
	v_dot4c_i32_i8_e32 v2, v0, v32
	v_lshrrev_b32_e32 v0, 4, v54
	v_and_b32_e32 v0, 0xf0f0f0f, v0
	v_dot4c_i32_i8_e32 v2, v0, v33
	v_and_b32_e32 v0, 0xf0f0f0f, v55
	v_dot4c_i32_i8_e32 v3, v0, v34
	v_lshrrev_b32_e32 v0, 4, v55
	v_and_b32_e32 v0, 0xf0f0f0f, v0
	v_dot4c_i32_i8_e32 v3, v0, v35
	v_and_b32_e32 v0, 0xf0f0f0f, v44
	v_dot4c_i32_i8_e32 v4, v0, v36
	v_lshrrev_b32_e32 v0, 4, v44
	v_and_b32_e32 v0, 0xf0f0f0f, v0
	v_dot4c_i32_i8_e32 v4, v0, v37
	v_and_b32_e32 v0, 0xf0f0f0f, v45
	v_mov_b32_e32 v5, 0
	v_dot4c_i32_i8_e32 v5, v0, v38
	v_lshrrev_b32_e32 v0, 4, v45
	v_and_b32_e32 v0, 0xf0f0f0f, v0
	v_dot4c_i32_i8_e32 v5, v0, v39
	v_and_b32_e32 v0, 0xf0f0f0f, v46
	v_dot4c_i32_i8_e32 v4, v0, v32
	v_lshrrev_b32_e32 v0, 4, v46
	v_and_b32_e32 v0, 0xf0f0f0f, v0
	v_dot4c_i32_i8_e32 v4, v0, v33
	v_and_b32_e32 v0, 0xf0f0f0f, v47
	v_dot4c_i32_i8_e32 v5, v0, v34
	v_lshrrev_b32_e32 v0, 4, v47
	v_and_b32_e32 v0, 0xf0f0f0f, v0
	v_dot4c_i32_i8_e32 v5, v0, v35
	v_sub_u32_e32 v3, v3, v171
	v_add_u32_e32 v2, v3, v2
	v_cvt_f32_i32_e32 v3, v2
	v_sub_u32_e32 v5, v5, v171
	v_add_u32_e32 v4, v5, v4
	v_cvt_f32_i32_e32 v2, v4
	s_waitcnt vmcnt(16)
	v_lshlrev_b32_e32 v1, 16, v173
	v_lshlrev_b32_e32 v0, 16, v172
	v_pk_fma_f32 v[144:145], v[0:1], v[2:3], v[144:145]
	ds_read_b128 v[4:7], v166 offset:4096
	ds_read_b128 v[0:3], v166 offset:4112
	v_mov_b32_e32 v44, 0
	v_add_u32_e32 v16, s44, v208
	v_lshl_or_b32 v20, v16, 7, v165
	v_lshl_or_b32 v45, v16, 4, v95
	v_add_u32_e32 v16, s44, v209
	v_lshl_or_b32 v17, v16, 7, v165
	v_lshl_or_b32 v46, v16, 4, v95
	v_add_u32_e32 v16, s44, v210
	global_load_dwordx4 v[80:83], v20, s[0:1]
	global_load_dwordx4 v[68:71], v17, s[0:1]
	v_lshl_or_b32 v17, v16, 7, v165
	v_lshl_or_b32 v47, v16, 4, v95
	v_add_u32_e32 v16, s44, v211
	global_load_dwordx4 v[52:55], v17, s[0:1]
	v_lshl_or_b32 v17, v16, 7, v165
	v_lshl_or_b32 v60, v16, 4, v95
	global_load_dwordx4 v[36:39], v17, s[0:1]
	s_waitcnt lgkmcnt(0)
	v_dot4c_i32_i8_e32 v44, 0x1010101, v4
	v_dot4c_i32_i8_e32 v44, 0x1010101, v5
	v_dot4c_i32_i8_e32 v44, 0x1010101, v6
	v_add_u32_e32 v16, s44, v212
	v_lshl_or_b32 v17, v16, 7, v165
	v_lshl_or_b32 v61, v16, 4, v95
	global_load_dwordx4 v[32:35], v17, s[0:1]
	v_dot4c_i32_i8_e32 v44, 0x1010101, v7
	v_dot4c_i32_i8_e32 v44, 0x1010101, v0
	v_dot4c_i32_i8_e32 v44, 0x1010101, v1
	v_add_u32_e32 v16, s44, v213
	v_lshl_or_b32 v17, v16, 7, v165
	v_lshl_or_b32 v62, v16, 4, v95
	global_load_dwordx4 v[28:31], v17, s[0:1]
	v_dot4c_i32_i8_e32 v44, 0x1010101, v2
	v_dot4c_i32_i8_e32 v44, 0x1010101, v3
	v_add_u32_e32 v16, s44, v214
	v_lshl_or_b32 v17, v16, 7, v165
	v_lshl_or_b32 v63, v16, 4, v95
	global_load_dwordx4 v[20:23], v17, s[0:1]
	v_lshlrev_b32_e32 v84, 3, v44
	s_waitcnt vmcnt(22)
	v_and_b32_e32 v44, 0xf0f0f0f, v72
	v_add_u32_e32 v76, s44, v215
	v_lshl_or_b32 v16, v76, 7, v165
	global_load_dwordx4 v[16:19], v16, s[0:1]
	v_lshl_or_b32 v76, v76, 4, v95
	global_load_ushort v180, v46, s[18:19]
	global_load_ushort v181, v45, s[18:19]
	global_load_ushort v172, v60, s[18:19]
	global_load_ushort v173, v47, s[18:19]
	global_load_ushort v87, v62, s[18:19]
	global_load_ushort v171, v61, s[18:19]
	global_load_ushort v85, v76, s[18:19]
	global_load_ushort v86, v63, s[18:19]
	v_mov_b32_e32 v46, 0
	v_dot4c_i32_i8_e32 v46, v44, v4
	v_lshrrev_b32_e32 v44, 4, v72
	v_and_b32_e32 v44, 0xf0f0f0f, v44
	v_dot4c_i32_i8_e32 v46, v44, v5
	v_and_b32_e32 v44, 0xf0f0f0f, v73
	v_mov_b32_e32 v47, 0
	v_dot4c_i32_i8_e32 v47, v44, v6
	v_lshrrev_b32_e32 v44, 4, v73
	v_and_b32_e32 v44, 0xf0f0f0f, v44
	v_dot4c_i32_i8_e32 v47, v44, v7
	v_and_b32_e32 v44, 0xf0f0f0f, v74
	v_dot4c_i32_i8_e32 v46, v44, v0
	v_lshrrev_b32_e32 v44, 4, v74
	v_and_b32_e32 v44, 0xf0f0f0f, v44
	v_dot4c_i32_i8_e32 v46, v44, v1
	v_and_b32_e32 v44, 0xf0f0f0f, v75
	v_dot4c_i32_i8_e32 v47, v44, v2
	v_lshrrev_b32_e32 v44, 4, v75
	v_and_b32_e32 v44, 0xf0f0f0f, v44
	v_dot4c_i32_i8_e32 v47, v44, v3
	s_waitcnt vmcnt(30)
	v_and_b32_e32 v44, 0xf0f0f0f, v64
	v_mov_b32_e32 v60, 0
	v_dot4c_i32_i8_e32 v60, v44, v4
	v_lshrrev_b32_e32 v44, 4, v64
	v_and_b32_e32 v44, 0xf0f0f0f, v44
	v_dot4c_i32_i8_e32 v60, v44, v5
	v_and_b32_e32 v44, 0xf0f0f0f, v65
	v_mov_b32_e32 v61, 0
	v_dot4c_i32_i8_e32 v61, v44, v6
	v_lshrrev_b32_e32 v44, 4, v65
	v_and_b32_e32 v44, 0xf0f0f0f, v44
	v_dot4c_i32_i8_e32 v61, v44, v7
	v_and_b32_e32 v44, 0xf0f0f0f, v66
	v_dot4c_i32_i8_e32 v60, v44, v0
	v_lshrrev_b32_e32 v44, 4, v66
	v_and_b32_e32 v44, 0xf0f0f0f, v44
	v_dot4c_i32_i8_e32 v60, v44, v1
	v_and_b32_e32 v44, 0xf0f0f0f, v67
	v_dot4c_i32_i8_e32 v61, v44, v2
	v_lshrrev_b32_e32 v44, 4, v67
	v_and_b32_e32 v44, 0xf0f0f0f, v44
	v_dot4c_i32_i8_e32 v61, v44, v3
	v_add_u32_e32 v46, v46, v47
	v_sub_u32_e32 v46, v46, v84
	s_waitcnt vmcnt(22)
	v_lshlrev_b32_e32 v45, 16, v179
	v_add_u32_e32 v47, v60, v61
	v_sub_u32_e32 v60, v47, v84
	v_cvt_f32_i32_e32 v47, v46
	v_cvt_f32_i32_e32 v46, v60
	v_lshlrev_b32_e32 v44, 16, v178
	v_pk_fma_f32 v[142:143], v[44:45], v[46:47], v[142:143]
	v_and_b32_e32 v44, 0xf0f0f0f, v56
	v_mov_b32_e32 v46, 0
	v_dot4c_i32_i8_e32 v46, v44, v4
	v_lshrrev_b32_e32 v44, 4, v56
	v_and_b32_e32 v44, 0xf0f0f0f, v44
	v_dot4c_i32_i8_e32 v46, v44, v5
	v_and_b32_e32 v44, 0xf0f0f0f, v57
	v_mov_b32_e32 v47, 0
	v_dot4c_i32_i8_e32 v47, v44, v6
	v_lshrrev_b32_e32 v44, 4, v57
	v_and_b32_e32 v44, 0xf0f0f0f, v44
	v_dot4c_i32_i8_e32 v47, v44, v7
	v_and_b32_e32 v44, 0xf0f0f0f, v58
	v_dot4c_i32_i8_e32 v46, v44, v0
	v_lshrrev_b32_e32 v44, 4, v58
	v_and_b32_e32 v44, 0xf0f0f0f, v44
	v_dot4c_i32_i8_e32 v46, v44, v1
	v_and_b32_e32 v44, 0xf0f0f0f, v59
	v_dot4c_i32_i8_e32 v47, v44, v2
	v_lshrrev_b32_e32 v44, 4, v59
	v_and_b32_e32 v44, 0xf0f0f0f, v44
	v_dot4c_i32_i8_e32 v47, v44, v3
	v_and_b32_e32 v44, 0xf0f0f0f, v48
	v_mov_b32_e32 v56, 0
	v_dot4c_i32_i8_e32 v56, v44, v4
	v_lshrrev_b32_e32 v44, 4, v48
	v_and_b32_e32 v44, 0xf0f0f0f, v44
	v_dot4c_i32_i8_e32 v56, v44, v5
	v_and_b32_e32 v44, 0xf0f0f0f, v49
	v_mov_b32_e32 v48, 0
	v_dot4c_i32_i8_e32 v48, v44, v6
	v_lshrrev_b32_e32 v44, 4, v49
	v_and_b32_e32 v44, 0xf0f0f0f, v44
	v_dot4c_i32_i8_e32 v48, v44, v7
	v_and_b32_e32 v44, 0xf0f0f0f, v50
	v_dot4c_i32_i8_e32 v56, v44, v0
	v_lshrrev_b32_e32 v44, 4, v50
	v_and_b32_e32 v44, 0xf0f0f0f, v44
	v_dot4c_i32_i8_e32 v56, v44, v1
	v_and_b32_e32 v44, 0xf0f0f0f, v51
	v_dot4c_i32_i8_e32 v48, v44, v2
	v_lshrrev_b32_e32 v44, 4, v51
	v_and_b32_e32 v44, 0xf0f0f0f, v44
	v_dot4c_i32_i8_e32 v48, v44, v3
	v_add_u32_e32 v46, v46, v47
	v_sub_u32_e32 v46, v46, v84
	s_waitcnt vmcnt(20)
	v_lshlrev_b32_e32 v45, 16, v175
	v_add_u32_e32 v47, v56, v48
	v_sub_u32_e32 v48, v47, v84
	v_cvt_f32_i32_e32 v47, v46
	v_cvt_f32_i32_e32 v46, v48
	v_lshlrev_b32_e32 v44, 16, v174
	v_pk_fma_f32 v[140:141], v[44:45], v[46:47], v[140:141]
	v_and_b32_e32 v44, 0xf0f0f0f, v40
	v_mov_b32_e32 v45, 0
	v_lshrrev_b32_e32 v40, 4, v40
	v_dot4c_i32_i8_e32 v45, v44, v4
	v_and_b32_e32 v40, 0xf0f0f0f, v40
	v_dot4c_i32_i8_e32 v45, v40, v5
	v_and_b32_e32 v40, 0xf0f0f0f, v41
	v_mov_b32_e32 v44, 0
	v_dot4c_i32_i8_e32 v44, v40, v6
	v_lshrrev_b32_e32 v40, 4, v41
	v_and_b32_e32 v40, 0xf0f0f0f, v40
	v_dot4c_i32_i8_e32 v44, v40, v7
	v_and_b32_e32 v40, 0xf0f0f0f, v42
	v_dot4c_i32_i8_e32 v45, v40, v0
	v_lshrrev_b32_e32 v40, 4, v42
	v_and_b32_e32 v40, 0xf0f0f0f, v40
	v_dot4c_i32_i8_e32 v45, v40, v1
	v_and_b32_e32 v40, 0xf0f0f0f, v43
	v_dot4c_i32_i8_e32 v44, v40, v2
	v_lshrrev_b32_e32 v40, 4, v43
	v_and_b32_e32 v40, 0xf0f0f0f, v40
	v_dot4c_i32_i8_e32 v44, v40, v3
	v_and_b32_e32 v40, 0xf0f0f0f, v24
	v_mov_b32_e32 v41, 0
	v_lshrrev_b32_e32 v24, 4, v24
	v_dot4c_i32_i8_e32 v41, v40, v4
	v_and_b32_e32 v24, 0xf0f0f0f, v24
	v_dot4c_i32_i8_e32 v41, v24, v5
	v_and_b32_e32 v24, 0xf0f0f0f, v25
	v_mov_b32_e32 v40, 0
	v_dot4c_i32_i8_e32 v40, v24, v6
	v_lshrrev_b32_e32 v24, 4, v25
	v_and_b32_e32 v24, 0xf0f0f0f, v24
	v_dot4c_i32_i8_e32 v40, v24, v7
	v_and_b32_e32 v24, 0xf0f0f0f, v26
	v_dot4c_i32_i8_e32 v41, v24, v0
	v_lshrrev_b32_e32 v24, 4, v26
	v_and_b32_e32 v24, 0xf0f0f0f, v24
	v_dot4c_i32_i8_e32 v41, v24, v1
	v_and_b32_e32 v24, 0xf0f0f0f, v27
	v_dot4c_i32_i8_e32 v40, v24, v2
	v_lshrrev_b32_e32 v24, 4, v27
	v_and_b32_e32 v24, 0xf0f0f0f, v24
	v_dot4c_i32_i8_e32 v40, v24, v3
	v_add_u32_e32 v26, v45, v44
	v_sub_u32_e32 v26, v26, v84
	s_waitcnt vmcnt(18)
	v_lshlrev_b32_e32 v25, 16, v170
	v_add_u32_e32 v27, v41, v40
	v_sub_u32_e32 v40, v27, v84
	v_cvt_f32_i32_e32 v27, v26
	v_cvt_f32_i32_e32 v26, v40
	v_lshlrev_b32_e32 v24, 16, v169
	v_pk_fma_f32 v[138:139], v[24:25], v[26:27], v[138:139]
	v_and_b32_e32 v24, 0xf0f0f0f, v12
	v_mov_b32_e32 v25, 0
	v_lshrrev_b32_e32 v12, 4, v12
	v_dot4c_i32_i8_e32 v25, v24, v4
	v_and_b32_e32 v12, 0xf0f0f0f, v12
	v_dot4c_i32_i8_e32 v25, v12, v5
	v_and_b32_e32 v12, 0xf0f0f0f, v13
	v_mov_b32_e32 v24, 0
	v_dot4c_i32_i8_e32 v24, v12, v6
	v_lshrrev_b32_e32 v12, 4, v13
	v_and_b32_e32 v12, 0xf0f0f0f, v12
	v_dot4c_i32_i8_e32 v24, v12, v7
	v_and_b32_e32 v12, 0xf0f0f0f, v14
	v_dot4c_i32_i8_e32 v25, v12, v0
	v_lshrrev_b32_e32 v12, 4, v14
	v_and_b32_e32 v12, 0xf0f0f0f, v12
	v_dot4c_i32_i8_e32 v25, v12, v1
	v_and_b32_e32 v12, 0xf0f0f0f, v15
	v_dot4c_i32_i8_e32 v24, v12, v2
	v_lshrrev_b32_e32 v12, 4, v15
	v_and_b32_e32 v12, 0xf0f0f0f, v12
	v_dot4c_i32_i8_e32 v24, v12, v3
	v_and_b32_e32 v12, 0xf0f0f0f, v8
	v_mov_b32_e32 v13, 0
	v_lshrrev_b32_e32 v8, 4, v8
	v_dot4c_i32_i8_e32 v13, v12, v4
	v_and_b32_e32 v8, 0xf0f0f0f, v8
	v_dot4c_i32_i8_e32 v13, v8, v5
	v_and_b32_e32 v8, 0xf0f0f0f, v9
	v_mov_b32_e32 v12, 0
	v_dot4c_i32_i8_e32 v12, v8, v6
	v_lshrrev_b32_e32 v8, 4, v9
	v_and_b32_e32 v8, 0xf0f0f0f, v8
	v_dot4c_i32_i8_e32 v12, v8, v7
	v_and_b32_e32 v8, 0xf0f0f0f, v10
	v_dot4c_i32_i8_e32 v13, v8, v0
	v_lshrrev_b32_e32 v8, 4, v10
	v_and_b32_e32 v8, 0xf0f0f0f, v8
	v_dot4c_i32_i8_e32 v13, v8, v1
	v_and_b32_e32 v8, 0xf0f0f0f, v11
	v_dot4c_i32_i8_e32 v12, v8, v2
	v_lshrrev_b32_e32 v8, 4, v11
	v_and_b32_e32 v8, 0xf0f0f0f, v8
	v_dot4c_i32_i8_e32 v12, v8, v3
	v_add_u32_e32 v10, v25, v24
	v_sub_u32_e32 v10, v10, v84
	s_waitcnt vmcnt(16)
; #define P12_ISSUE(c_, i_, h_, CW_, SC_) do { _Pragma("unroll") for (int bb = 0; bb < 8; ++bb) { const unsigned ro = (unsigned)(c_) * 16384u + (unsigned)EL[(i_) * 128 + ((h_) * 8 + bb) * 8 + g8]; \
;         CW_[bb] = *(const v4u*)(U4 + (size_t)(ro * 128u + 16u * (unsigned)k8)); SC_[bb] = USS[(size_t)(ro * 8u + (unsigned)k8)]; } } while (0)
; #define P12_COMP(i_, h_, CW_, SC_) do { _Pragma("unroll") for (int bb = 0; bb < 8; ++bb) { int a0 = 0, a1 = 0; P12_U4(CW_[bb].x, xa.x, xa.y, a0); P12_U4(CW_[bb].y, xa.z, xa.w, a1); P12_U4(CW_[bb].z, xb.x, xb.y, a0); P12_U4(CW_[bb].w, xb.z, xb.w, a1); \
;         psum[(i_)][(h_) * 8 + bb] += __uint_as_float(SC_[bb] << 16) * (float)((a0 + a1) - xo); } } while (0)
; #define P12_BAR() asm volatile("" ::: "memory")
; __device__ __forceinline__ void p12_peer(Frame& F) {
;     ...
;     { v4u cwA[8], cwB[8]; unsigned scA[8], scB[8]; v4u xa, xb; int xo;
;       P12_ISSUE(0, 0, 0, cwA, scA);
; _Pragma("nounroll")
;       for (int c = 0; c < 16; ++c) { const int cn = c + 1 < 16 ? c + 1 : 15;
;           P12_XQ(c, 0); P12_ISSUE(c, 0, 1, cwB, scB); P12_BAR(); P12_COMP(0, 0, cwA, scA); P12_ISSUE(c, 1, 0, cwA, scA); P12_BAR(); P12_COMP(0, 1, cwB, scB);
;           P12_XQ(c, 1); P12_ISSUE(c, 1, 1, cwB, scB); P12_BAR(); P12_COMP(1, 0, cwA, scA); P12_ISSUE(c, 2, 0, cwA, scA); P12_BAR(); P12_COMP(1, 1, cwB, scB);
;           P12_XQ(c, 2); P12_ISSUE(c, 2, 1, cwB, scB); P12_BAR(); P12_COMP(2, 0, cwA, scA); P12_ISSUE(c, 3, 0, cwA, scA); P12_BAR(); P12_COMP(2, 1, cwB, scB);
;           P12_XQ(c, 3); P12_ISSUE(c, 3, 1, cwB, scB); P12_BAR(); P12_COMP(3, 0, cwA, scA); P12_ISSUE(cn, 0, 0, cwA, scA); P12_BAR(); P12_COMP(3, 1, cwB, scB);
;       } }
	v_lshlrev_b32_e32 v9, 16, v168
	v_add_u32_e32 v11, v13, v12
	v_sub_u32_e32 v12, v11, v84
	v_cvt_f32_i32_e32 v11, v10
	v_cvt_f32_i32_e32 v10, v12
	v_lshlrev_b32_e32 v8, 16, v167
	v_pk_fma_f32 v[136:137], v[8:9], v[10:11], v[136:137]
	v_add_u32_e32 v8, s44, v216
	v_lshl_or_b32 v12, v8, 7, v165
	v_lshl_or_b32 v40, v8, 4, v95
	v_add_u32_e32 v8, s44, v217
	v_lshl_or_b32 v9, v8, 7, v165
	v_lshl_or_b32 v41, v8, 4, v95
	v_add_u32_e32 v8, s44, v218
	global_load_dwordx4 v[76:79], v12, s[0:1]
	global_load_dwordx4 v[72:75], v9, s[0:1]
	v_lshl_or_b32 v9, v8, 7, v165
	v_lshl_or_b32 v42, v8, 4, v95
	v_add_u32_e32 v8, s44, v219
	global_load_dwordx4 v[60:63], v9, s[0:1]
	v_lshl_or_b32 v9, v8, 7, v165
	v_lshl_or_b32 v43, v8, 4, v95
	global_load_dwordx4 v[56:59], v9, s[0:1]
	v_add_u32_e32 v8, s44, v220
	v_lshl_or_b32 v9, v8, 7, v165
	v_lshl_or_b32 v48, v8, 4, v95
	global_load_dwordx4 v[44:47], v9, s[0:1]
	v_add_u32_e32 v8, s44, v221
	v_lshl_or_b32 v9, v8, 7, v165
	v_lshl_or_b32 v49, v8, 4, v95
	global_load_dwordx4 v[24:27], v9, s[0:1]
	v_add_u32_e32 v8, s44, v222
	v_lshl_or_b32 v9, v8, 7, v165
	v_lshl_or_b32 v50, v8, 4, v95
	global_load_dwordx4 v[12:15], v9, s[0:1]
	v_add_u32_e32 v51, s44, v223
	v_lshl_or_b32 v8, v51, 7, v165
	global_load_dwordx4 v[8:11], v8, s[0:1]
	v_lshl_or_b32 v51, v51, 4, v95
	global_load_ushort v176, v41, s[18:19]
	global_load_ushort v177, v40, s[18:19]
	global_load_ushort v167, v43, s[18:19]
	global_load_ushort v168, v42, s[18:19]
	global_load_ushort v90, v49, s[18:19]
	global_load_ushort v91, v48, s[18:19]
	global_load_ushort v88, v51, s[18:19]
	global_load_ushort v89, v50, s[18:19]
	s_waitcnt vmcnt(31)
	v_and_b32_e32 v40, 0xf0f0f0f, v80
	v_mov_b32_e32 v42, 0
	v_dot4c_i32_i8_e32 v42, v40, v4
	v_lshrrev_b32_e32 v40, 4, v80
	v_and_b32_e32 v40, 0xf0f0f0f, v40
	v_dot4c_i32_i8_e32 v42, v40, v5
	v_and_b32_e32 v40, 0xf0f0f0f, v81
	v_mov_b32_e32 v43, 0
	v_dot4c_i32_i8_e32 v43, v40, v6
	v_lshrrev_b32_e32 v40, 4, v81
	v_and_b32_e32 v40, 0xf0f0f0f, v40
	v_dot4c_i32_i8_e32 v43, v40, v7
	v_and_b32_e32 v40, 0xf0f0f0f, v82
	v_dot4c_i32_i8_e32 v42, v40, v0
	v_lshrrev_b32_e32 v40, 4, v82
	v_and_b32_e32 v40, 0xf0f0f0f, v40
	v_dot4c_i32_i8_e32 v42, v40, v1
	v_and_b32_e32 v40, 0xf0f0f0f, v83
	v_dot4c_i32_i8_e32 v43, v40, v2
	v_lshrrev_b32_e32 v40, 4, v83
	v_and_b32_e32 v40, 0xf0f0f0f, v40
	v_dot4c_i32_i8_e32 v43, v40, v3
	s_waitcnt vmcnt(30)
	v_and_b32_e32 v40, 0xf0f0f0f, v68
	v_mov_b32_e32 v48, 0
	v_dot4c_i32_i8_e32 v48, v40, v4
	v_lshrrev_b32_e32 v40, 4, v68
	v_and_b32_e32 v40, 0xf0f0f0f, v40
	v_dot4c_i32_i8_e32 v48, v40, v5
	v_and_b32_e32 v40, 0xf0f0f0f, v69
	v_mov_b32_e32 v49, 0
	v_dot4c_i32_i8_e32 v49, v40, v6
	v_lshrrev_b32_e32 v40, 4, v69
	v_and_b32_e32 v40, 0xf0f0f0f, v40
	v_dot4c_i32_i8_e32 v49, v40, v7
	v_and_b32_e32 v40, 0xf0f0f0f, v70
	v_dot4c_i32_i8_e32 v48, v40, v0
	v_lshrrev_b32_e32 v40, 4, v70
	v_and_b32_e32 v40, 0xf0f0f0f, v40
	v_dot4c_i32_i8_e32 v48, v40, v1
	v_and_b32_e32 v40, 0xf0f0f0f, v71
	v_dot4c_i32_i8_e32 v49, v40, v2
	v_lshrrev_b32_e32 v40, 4, v71
	v_and_b32_e32 v40, 0xf0f0f0f, v40
	v_dot4c_i32_i8_e32 v49, v40, v3
	v_add_u32_e32 v42, v42, v43
	v_sub_u32_e32 v42, v42, v84
	s_waitcnt vmcnt(22)
	v_lshlrev_b32_e32 v41, 16, v181
	v_sub_u32_e32 v43, v49, v84
	v_add_u32_e32 v48, v43, v48
	v_cvt_f32_i32_e32 v43, v42
	v_cvt_f32_i32_e32 v42, v48
	v_lshlrev_b32_e32 v40, 16, v180
	v_pk_fma_f32 v[134:135], v[40:41], v[42:43], v[134:135]
	v_and_b32_e32 v40, 0xf0f0f0f, v52
	v_mov_b32_e32 v41, 0
	v_dot4c_i32_i8_e32 v41, v40, v4
	v_lshrrev_b32_e32 v40, 4, v52
	v_and_b32_e32 v40, 0xf0f0f0f, v40
	v_dot4c_i32_i8_e32 v41, v40, v5
	v_and_b32_e32 v40, 0xf0f0f0f, v53
	v_mov_b32_e32 v42, 0
	v_dot4c_i32_i8_e32 v42, v40, v6
	v_lshrrev_b32_e32 v40, 4, v53
	v_and_b32_e32 v40, 0xf0f0f0f, v40
	v_dot4c_i32_i8_e32 v42, v40, v7
	v_and_b32_e32 v40, 0xf0f0f0f, v54
	v_dot4c_i32_i8_e32 v41, v40, v0
	v_lshrrev_b32_e32 v40, 4, v54
	v_and_b32_e32 v40, 0xf0f0f0f, v40
	v_dot4c_i32_i8_e32 v41, v40, v1
	v_and_b32_e32 v40, 0xf0f0f0f, v55
	v_dot4c_i32_i8_e32 v42, v40, v2
	v_lshrrev_b32_e32 v40, 4, v55
	v_and_b32_e32 v40, 0xf0f0f0f, v40
	v_dot4c_i32_i8_e32 v42, v40, v3
	v_and_b32_e32 v40, 0xf0f0f0f, v36
	v_mov_b32_e32 v43, 0
	v_lshrrev_b32_e32 v36, 4, v36
	v_dot4c_i32_i8_e32 v43, v40, v4
	v_and_b32_e32 v36, 0xf0f0f0f, v36
	v_dot4c_i32_i8_e32 v43, v36, v5
	v_and_b32_e32 v36, 0xf0f0f0f, v37
	v_mov_b32_e32 v40, 0
	v_dot4c_i32_i8_e32 v40, v36, v6
	v_lshrrev_b32_e32 v36, 4, v37
	v_and_b32_e32 v36, 0xf0f0f0f, v36
	v_dot4c_i32_i8_e32 v40, v36, v7
	v_and_b32_e32 v36, 0xf0f0f0f, v38
	v_dot4c_i32_i8_e32 v43, v36, v0
	v_lshrrev_b32_e32 v36, 4, v38
	v_and_b32_e32 v36, 0xf0f0f0f, v36
	v_dot4c_i32_i8_e32 v43, v36, v1
	v_and_b32_e32 v36, 0xf0f0f0f, v39
	v_dot4c_i32_i8_e32 v40, v36, v2
	v_lshrrev_b32_e32 v36, 4, v39
	v_and_b32_e32 v36, 0xf0f0f0f, v36
	v_dot4c_i32_i8_e32 v40, v36, v3
	v_sub_u32_e32 v38, v42, v84
	v_add_u32_e32 v38, v38, v41
	s_waitcnt vmcnt(20)
; #define P12_ISSUE(c_, i_, h_, CW_, SC_) do { _Pragma("unroll") for (int bb = 0; bb < 8; ++bb) { const unsigned ro = (unsigned)(c_) * 16384u + (unsigned)EL[(i_) * 128 + ((h_) * 8 + bb) * 8 + g8]; \
;         CW_[bb] = *(const v4u*)(U4 + (size_t)(ro * 128u + 16u * (unsigned)k8)); SC_[bb] = USS[(size_t)(ro * 8u + (unsigned)k8)]; } } while (0)
; #define P12_COMP(i_, h_, CW_, SC_) do { _Pragma("unroll") for (int bb = 0; bb < 8; ++bb) { int a0 = 0, a1 = 0; P12_U4(CW_[bb].x, xa.x, xa.y, a0); P12_U4(CW_[bb].y, xa.z, xa.w, a1); P12_U4(CW_[bb].z, xb.x, xb.y, a0); P12_U4(CW_[bb].w, xb.z, xb.w, a1); \
;         psum[(i_)][(h_) * 8 + bb] += __uint_as_float(SC_[bb] << 16) * (float)((a0 + a1) - xo); } } while (0)
; #define P12_BAR() asm volatile("" ::: "memory")
; __device__ __forceinline__ void p12_peer(Frame& F) {
;     ...
;     { v4u cwA[8], cwB[8]; unsigned scA[8], scB[8]; v4u xa, xb; int xo;
;       P12_ISSUE(0, 0, 0, cwA, scA);
; _Pragma("nounroll")
;       for (int c = 0; c < 16; ++c) { const int cn = c + 1 < 16 ? c + 1 : 15;
;           P12_XQ(c, 0); P12_ISSUE(c, 0, 1, cwB, scB); P12_BAR(); P12_COMP(0, 0, cwA, scA); P12_ISSUE(c, 1, 0, cwA, scA); P12_BAR(); P12_COMP(0, 1, cwB, scB);
;           P12_XQ(c, 1); P12_ISSUE(c, 1, 1, cwB, scB); P12_BAR(); P12_COMP(1, 0, cwA, scA); P12_ISSUE(c, 2, 0, cwA, scA); P12_BAR(); P12_COMP(1, 1, cwB, scB);
;           P12_XQ(c, 2); P12_ISSUE(c, 2, 1, cwB, scB); P12_BAR(); P12_COMP(2, 0, cwA, scA); P12_ISSUE(c, 3, 0, cwA, scA); P12_BAR(); P12_COMP(2, 1, cwB, scB);
;           P12_XQ(c, 3); P12_ISSUE(c, 3, 1, cwB, scB); P12_BAR(); P12_COMP(3, 0, cwA, scA); P12_ISSUE(cn, 0, 0, cwA, scA); P12_BAR(); P12_COMP(3, 1, cwB, scB);
;       } }
	v_lshlrev_b32_e32 v37, 16, v173
	v_sub_u32_e32 v39, v40, v84
	v_add_u32_e32 v40, v39, v43
	v_cvt_f32_i32_e32 v39, v38
	v_cvt_f32_i32_e32 v38, v40
	v_lshlrev_b32_e32 v36, 16, v172
	v_pk_fma_f32 v[132:133], v[36:37], v[38:39], v[132:133]
	v_and_b32_e32 v36, 0xf0f0f0f, v32
	v_mov_b32_e32 v37, 0
	v_lshrrev_b32_e32 v32, 4, v32
	v_dot4c_i32_i8_e32 v37, v36, v4
	v_and_b32_e32 v32, 0xf0f0f0f, v32
	v_dot4c_i32_i8_e32 v37, v32, v5
	v_and_b32_e32 v32, 0xf0f0f0f, v33
	v_mov_b32_e32 v36, 0
	v_dot4c_i32_i8_e32 v36, v32, v6
	v_lshrrev_b32_e32 v32, 4, v33
	v_and_b32_e32 v32, 0xf0f0f0f, v32
	v_dot4c_i32_i8_e32 v36, v32, v7
	v_and_b32_e32 v32, 0xf0f0f0f, v34
	v_dot4c_i32_i8_e32 v37, v32, v0
	v_lshrrev_b32_e32 v32, 4, v34
	v_and_b32_e32 v32, 0xf0f0f0f, v32
	v_dot4c_i32_i8_e32 v37, v32, v1
	v_and_b32_e32 v32, 0xf0f0f0f, v35
	v_dot4c_i32_i8_e32 v36, v32, v2
	v_lshrrev_b32_e32 v32, 4, v35
	v_and_b32_e32 v32, 0xf0f0f0f, v32
	v_dot4c_i32_i8_e32 v36, v32, v3
	v_and_b32_e32 v32, 0xf0f0f0f, v28
	v_mov_b32_e32 v33, 0
	v_lshrrev_b32_e32 v28, 4, v28
	v_dot4c_i32_i8_e32 v33, v32, v4
	v_and_b32_e32 v28, 0xf0f0f0f, v28
	v_dot4c_i32_i8_e32 v33, v28, v5
	v_and_b32_e32 v28, 0xf0f0f0f, v29
	v_mov_b32_e32 v32, 0
	v_dot4c_i32_i8_e32 v32, v28, v6
	v_lshrrev_b32_e32 v28, 4, v29
	v_and_b32_e32 v28, 0xf0f0f0f, v28
	v_dot4c_i32_i8_e32 v32, v28, v7
	v_and_b32_e32 v28, 0xf0f0f0f, v30
	v_dot4c_i32_i8_e32 v33, v28, v0
	v_lshrrev_b32_e32 v28, 4, v30
	v_and_b32_e32 v28, 0xf0f0f0f, v28
	v_dot4c_i32_i8_e32 v33, v28, v1
	v_and_b32_e32 v28, 0xf0f0f0f, v31
	v_dot4c_i32_i8_e32 v32, v28, v2
	v_lshrrev_b32_e32 v28, 4, v31
	v_and_b32_e32 v28, 0xf0f0f0f, v28
	v_dot4c_i32_i8_e32 v32, v28, v3
	v_sub_u32_e32 v30, v36, v84
	v_add_u32_e32 v30, v30, v37
	s_waitcnt vmcnt(18)
	v_lshlrev_b32_e32 v29, 16, v171
	v_sub_u32_e32 v31, v32, v84
	v_add_u32_e32 v32, v31, v33
	v_cvt_f32_i32_e32 v31, v30
	v_cvt_f32_i32_e32 v30, v32
	v_lshlrev_b32_e32 v28, 16, v87
	v_pk_fma_f32 v[130:131], v[28:29], v[30:31], v[130:131]
	v_and_b32_e32 v28, 0xf0f0f0f, v20
	v_mov_b32_e32 v29, 0
	v_lshrrev_b32_e32 v20, 4, v20
	v_dot4c_i32_i8_e32 v29, v28, v4
	v_and_b32_e32 v20, 0xf0f0f0f, v20
	v_dot4c_i32_i8_e32 v29, v20, v5
	v_and_b32_e32 v20, 0xf0f0f0f, v21
	v_mov_b32_e32 v28, 0
	v_dot4c_i32_i8_e32 v28, v20, v6
	v_lshrrev_b32_e32 v20, 4, v21
	v_and_b32_e32 v20, 0xf0f0f0f, v20
	v_dot4c_i32_i8_e32 v28, v20, v7
	v_and_b32_e32 v20, 0xf0f0f0f, v22
	v_dot4c_i32_i8_e32 v29, v20, v0
	v_lshrrev_b32_e32 v20, 4, v22
	v_and_b32_e32 v20, 0xf0f0f0f, v20
	v_dot4c_i32_i8_e32 v29, v20, v1
	v_and_b32_e32 v20, 0xf0f0f0f, v23
	v_dot4c_i32_i8_e32 v28, v20, v2
	v_lshrrev_b32_e32 v20, 4, v23
	v_and_b32_e32 v20, 0xf0f0f0f, v20
	v_dot4c_i32_i8_e32 v28, v20, v3
	v_and_b32_e32 v20, 0xf0f0f0f, v16
	v_mov_b32_e32 v21, 0
	v_dot4c_i32_i8_e32 v21, v20, v4
	v_lshrrev_b32_e32 v4, 4, v16
	v_and_b32_e32 v4, 0xf0f0f0f, v4
	v_dot4c_i32_i8_e32 v21, v4, v5
	v_and_b32_e32 v4, 0xf0f0f0f, v17
	v_mov_b32_e32 v5, 0
	v_dot4c_i32_i8_e32 v5, v4, v6
	v_lshrrev_b32_e32 v4, 4, v17
	v_and_b32_e32 v4, 0xf0f0f0f, v4
	v_dot4c_i32_i8_e32 v5, v4, v7
	v_and_b32_e32 v4, 0xf0f0f0f, v18
	v_dot4c_i32_i8_e32 v21, v4, v0
	v_lshrrev_b32_e32 v0, 4, v18
	v_and_b32_e32 v0, 0xf0f0f0f, v0
	v_dot4c_i32_i8_e32 v21, v0, v1
	v_and_b32_e32 v0, 0xf0f0f0f, v19
	v_dot4c_i32_i8_e32 v5, v0, v2
	v_lshrrev_b32_e32 v0, 4, v19
	v_and_b32_e32 v0, 0xf0f0f0f, v0
	v_dot4c_i32_i8_e32 v5, v0, v3
	v_sub_u32_e32 v2, v28, v84
	v_add_u32_e32 v2, v2, v29
	s_waitcnt vmcnt(16)
	v_lshlrev_b32_e32 v1, 16, v86
	v_sub_u32_e32 v3, v5, v84
	v_add_u32_e32 v4, v3, v21
	v_cvt_f32_i32_e32 v3, v2
	v_cvt_f32_i32_e32 v2, v4
	v_lshlrev_b32_e32 v0, 16, v85
	ds_read_b128 v[32:35], v166 offset:8192
	ds_read_b128 v[28:31], v166 offset:8208
	v_pk_fma_f32 v[128:129], v[0:1], v[2:3], v[128:129]
	v_mov_b32_e32 v0, 0
	v_add_u32_e32 v1, s44, v224
	v_lshl_or_b32 v5, v1, 7, v165
	v_add_u32_e32 v2, s44, v225
	global_load_dwordx4 v[84:87], v5, s[0:1]
	v_lshl_or_b32 v5, v2, 7, v165
	v_add_u32_e32 v3, s44, v226
	global_load_dwordx4 v[80:83], v5, s[0:1]
	v_lshl_or_b32 v5, v3, 7, v165
	v_add_u32_e32 v4, s44, v227
	global_load_dwordx4 v[68:71], v5, s[0:1]
	v_lshl_or_b32 v5, v4, 7, v165
	global_load_dwordx4 v[64:67], v5, s[0:1]
	s_waitcnt lgkmcnt(0)
	v_dot4c_i32_i8_e32 v0, 0x1010101, v32
	v_dot4c_i32_i8_e32 v0, 0x1010101, v33
	v_dot4c_i32_i8_e32 v0, 0x1010101, v34
	v_dot4c_i32_i8_e32 v0, 0x1010101, v35
	v_add_u32_e32 v5, s44, v228
	v_lshl_or_b32 v6, v5, 7, v165
	global_load_dwordx4 v[52:55], v6, s[0:1]
	v_dot4c_i32_i8_e32 v0, 0x1010101, v28
	v_dot4c_i32_i8_e32 v0, 0x1010101, v29
	v_dot4c_i32_i8_e32 v0, 0x1010101, v30
	v_dot4c_i32_i8_e32 v0, 0x1010101, v31
	v_add_u32_e32 v6, s44, v229
	v_lshl_or_b32 v7, v6, 7, v165
	global_load_dwordx4 v[48:51], v7, s[0:1]
	v_lshl_or_b32 v2, v2, 4, v95
	v_lshl_or_b32 v1, v1, 4, v95
	v_lshl_or_b32 v3, v3, 4, v95
	v_lshl_or_b32 v4, v4, 4, v95
	v_add_u32_e32 v7, s44, v230
	v_lshl_or_b32 v16, v7, 7, v165
	global_load_dwordx4 v[40:43], v16, s[0:1]
	v_lshl_or_b32 v5, v5, 4, v95
	v_lshl_or_b32 v6, v6, 4, v95
	v_lshl_or_b32 v7, v7, 4, v95
	v_lshlrev_b32_e32 v169, 3, v0
	v_add_u32_e32 v16, s44, v231
	v_lshl_or_b32 v17, v16, 7, v165
	global_load_dwordx4 v[36:39], v17, s[0:1]
	v_lshl_or_b32 v16, v16, 4, v95
	global_load_ushort v178, v2, s[18:19]
	global_load_ushort v179, v1, s[18:19]
	global_load_ushort v174, v4, s[18:19]
	global_load_ushort v175, v3, s[18:19]
	global_load_ushort v172, v6, s[18:19]
	global_load_ushort v173, v5, s[18:19]
	global_load_ushort v170, v16, s[18:19]
	global_load_ushort v171, v7, s[18:19]
	s_waitcnt vmcnt(31)
	v_and_b32_e32 v0, 0xf0f0f0f, v76
	v_mov_b32_e32 v2, 0
	v_dot4c_i32_i8_e32 v2, v0, v32
	v_lshrrev_b32_e32 v0, 4, v76
	v_and_b32_e32 v0, 0xf0f0f0f, v0
	v_dot4c_i32_i8_e32 v2, v0, v33
	v_and_b32_e32 v0, 0xf0f0f0f, v77
	v_mov_b32_e32 v3, 0
	v_dot4c_i32_i8_e32 v3, v0, v34
	v_lshrrev_b32_e32 v0, 4, v77
	v_and_b32_e32 v0, 0xf0f0f0f, v0
	v_dot4c_i32_i8_e32 v3, v0, v35
	v_and_b32_e32 v0, 0xf0f0f0f, v78
	v_dot4c_i32_i8_e32 v2, v0, v28
	v_lshrrev_b32_e32 v0, 4, v78
	v_and_b32_e32 v0, 0xf0f0f0f, v0
	v_dot4c_i32_i8_e32 v2, v0, v29
	v_and_b32_e32 v0, 0xf0f0f0f, v79
	v_dot4c_i32_i8_e32 v3, v0, v30
	v_lshrrev_b32_e32 v0, 4, v79
	v_and_b32_e32 v0, 0xf0f0f0f, v0
	v_dot4c_i32_i8_e32 v3, v0, v31
	s_waitcnt vmcnt(30)
	v_and_b32_e32 v0, 0xf0f0f0f, v72
	v_mov_b32_e32 v4, 0
	v_dot4c_i32_i8_e32 v4, v0, v32
	v_lshrrev_b32_e32 v0, 4, v72
	v_and_b32_e32 v0, 0xf0f0f0f, v0
	v_dot4c_i32_i8_e32 v4, v0, v33
	v_and_b32_e32 v0, 0xf0f0f0f, v73
	v_mov_b32_e32 v5, 0
	v_dot4c_i32_i8_e32 v5, v0, v34
	v_lshrrev_b32_e32 v0, 4, v73
	v_and_b32_e32 v0, 0xf0f0f0f, v0
	v_dot4c_i32_i8_e32 v5, v0, v35
	v_and_b32_e32 v0, 0xf0f0f0f, v74
	v_dot4c_i32_i8_e32 v4, v0, v28
	v_lshrrev_b32_e32 v0, 4, v74
	v_and_b32_e32 v0, 0xf0f0f0f, v0
	v_dot4c_i32_i8_e32 v4, v0, v29
	v_and_b32_e32 v0, 0xf0f0f0f, v75
	v_dot4c_i32_i8_e32 v5, v0, v30
	v_lshrrev_b32_e32 v0, 4, v75
	v_and_b32_e32 v0, 0xf0f0f0f, v0
	v_dot4c_i32_i8_e32 v5, v0, v31
	v_add_u32_e32 v2, v2, v3
	v_sub_u32_e32 v2, v2, v169
	s_waitcnt vmcnt(22)
	v_lshlrev_b32_e32 v1, 16, v177
	v_add_u32_e32 v3, v4, v5
	v_sub_u32_e32 v4, v3, v169
	v_cvt_f32_i32_e32 v3, v2
	v_cvt_f32_i32_e32 v2, v4
	v_lshlrev_b32_e32 v0, 16, v176
	v_mov_b32_e32 v4, 0
	v_mov_b32_e32 v5, 0
	v_pk_fma_f32 v[126:127], v[0:1], v[2:3], v[126:127]
	v_and_b32_e32 v0, 0xf0f0f0f, v60
	v_mov_b32_e32 v2, 0
	v_dot4c_i32_i8_e32 v2, v0, v32
	v_lshrrev_b32_e32 v0, 4, v60
	v_and_b32_e32 v0, 0xf0f0f0f, v0
	v_dot4c_i32_i8_e32 v2, v0, v33
	v_and_b32_e32 v0, 0xf0f0f0f, v61
	v_mov_b32_e32 v3, 0
	v_dot4c_i32_i8_e32 v3, v0, v34
	v_lshrrev_b32_e32 v0, 4, v61
	v_and_b32_e32 v0, 0xf0f0f0f, v0
	v_dot4c_i32_i8_e32 v3, v0, v35
	v_and_b32_e32 v0, 0xf0f0f0f, v62
	v_dot4c_i32_i8_e32 v2, v0, v28
	v_lshrrev_b32_e32 v0, 4, v62
	v_and_b32_e32 v0, 0xf0f0f0f, v0
	v_dot4c_i32_i8_e32 v2, v0, v29
	v_and_b32_e32 v0, 0xf0f0f0f, v63
	v_dot4c_i32_i8_e32 v3, v0, v30
	v_lshrrev_b32_e32 v0, 4, v63
	v_and_b32_e32 v0, 0xf0f0f0f, v0
	v_dot4c_i32_i8_e32 v3, v0, v31
	v_and_b32_e32 v0, 0xf0f0f0f, v56
	v_dot4c_i32_i8_e32 v4, v0, v32
	v_lshrrev_b32_e32 v0, 4, v56
	v_and_b32_e32 v0, 0xf0f0f0f, v0
	v_dot4c_i32_i8_e32 v4, v0, v33
	v_and_b32_e32 v0, 0xf0f0f0f, v57
	v_dot4c_i32_i8_e32 v5, v0, v34
	v_lshrrev_b32_e32 v0, 4, v57
	v_and_b32_e32 v0, 0xf0f0f0f, v0
	v_dot4c_i32_i8_e32 v5, v0, v35
	v_and_b32_e32 v0, 0xf0f0f0f, v58
	v_dot4c_i32_i8_e32 v4, v0, v28
	v_lshrrev_b32_e32 v0, 4, v58
	v_and_b32_e32 v0, 0xf0f0f0f, v0
	v_dot4c_i32_i8_e32 v4, v0, v29
	v_and_b32_e32 v0, 0xf0f0f0f, v59
	v_dot4c_i32_i8_e32 v5, v0, v30
	v_lshrrev_b32_e32 v0, 4, v59
	v_and_b32_e32 v0, 0xf0f0f0f, v0
	v_dot4c_i32_i8_e32 v5, v0, v31
	v_add_u32_e32 v2, v2, v3
	v_sub_u32_e32 v2, v2, v169
	s_waitcnt vmcnt(20)
	v_lshlrev_b32_e32 v1, 16, v168
	v_add_u32_e32 v3, v4, v5
	v_sub_u32_e32 v4, v3, v169
	v_cvt_f32_i32_e32 v3, v2
	v_cvt_f32_i32_e32 v2, v4
	v_lshlrev_b32_e32 v0, 16, v167
	v_mov_b32_e32 v4, 0
	v_mov_b32_e32 v5, 0
	v_pk_fma_f32 v[124:125], v[0:1], v[2:3], v[124:125]
	v_and_b32_e32 v0, 0xf0f0f0f, v44
	v_mov_b32_e32 v2, 0
	v_dot4c_i32_i8_e32 v2, v0, v32
	v_lshrrev_b32_e32 v0, 4, v44
	v_and_b32_e32 v0, 0xf0f0f0f, v0
	v_dot4c_i32_i8_e32 v2, v0, v33
	v_and_b32_e32 v0, 0xf0f0f0f, v45
	v_mov_b32_e32 v3, 0
	v_dot4c_i32_i8_e32 v3, v0, v34
	v_lshrrev_b32_e32 v0, 4, v45
	v_and_b32_e32 v0, 0xf0f0f0f, v0
	v_dot4c_i32_i8_e32 v3, v0, v35
	v_and_b32_e32 v0, 0xf0f0f0f, v46
	v_dot4c_i32_i8_e32 v2, v0, v28
	v_lshrrev_b32_e32 v0, 4, v46
	v_and_b32_e32 v0, 0xf0f0f0f, v0
	v_dot4c_i32_i8_e32 v2, v0, v29
	v_and_b32_e32 v0, 0xf0f0f0f, v47
	v_dot4c_i32_i8_e32 v3, v0, v30
	v_lshrrev_b32_e32 v0, 4, v47
	v_and_b32_e32 v0, 0xf0f0f0f, v0
	v_dot4c_i32_i8_e32 v3, v0, v31
	v_and_b32_e32 v0, 0xf0f0f0f, v24
	v_dot4c_i32_i8_e32 v4, v0, v32
	v_lshrrev_b32_e32 v0, 4, v24
	v_and_b32_e32 v0, 0xf0f0f0f, v0
	v_dot4c_i32_i8_e32 v4, v0, v33
	v_and_b32_e32 v0, 0xf0f0f0f, v25
	v_dot4c_i32_i8_e32 v5, v0, v34
	v_lshrrev_b32_e32 v0, 4, v25
	v_and_b32_e32 v0, 0xf0f0f0f, v0
	v_dot4c_i32_i8_e32 v5, v0, v35
	v_and_b32_e32 v0, 0xf0f0f0f, v26
	v_dot4c_i32_i8_e32 v4, v0, v28
	v_lshrrev_b32_e32 v0, 4, v26
	v_and_b32_e32 v0, 0xf0f0f0f, v0
	v_dot4c_i32_i8_e32 v4, v0, v29
	v_and_b32_e32 v0, 0xf0f0f0f, v27
	v_dot4c_i32_i8_e32 v5, v0, v30
	v_lshrrev_b32_e32 v0, 4, v27
	v_and_b32_e32 v0, 0xf0f0f0f, v0
	v_dot4c_i32_i8_e32 v5, v0, v31
	v_add_u32_e32 v2, v2, v3
	v_sub_u32_e32 v2, v2, v169
	s_waitcnt vmcnt(18)
; #define P12_ISSUE(c_, i_, h_, CW_, SC_) do { _Pragma("unroll") for (int bb = 0; bb < 8; ++bb) { const unsigned ro = (unsigned)(c_) * 16384u + (unsigned)EL[(i_) * 128 + ((h_) * 8 + bb) * 8 + g8]; \
;         CW_[bb] = *(const v4u*)(U4 + (size_t)(ro * 128u + 16u * (unsigned)k8)); SC_[bb] = USS[(size_t)(ro * 8u + (unsigned)k8)]; } } while (0)
; #define P12_COMP(i_, h_, CW_, SC_) do { _Pragma("unroll") for (int bb = 0; bb < 8; ++bb) { int a0 = 0, a1 = 0; P12_U4(CW_[bb].x, xa.x, xa.y, a0); P12_U4(CW_[bb].y, xa.z, xa.w, a1); P12_U4(CW_[bb].z, xb.x, xb.y, a0); P12_U4(CW_[bb].w, xb.z, xb.w, a1); \
;         psum[(i_)][(h_) * 8 + bb] += __uint_as_float(SC_[bb] << 16) * (float)((a0 + a1) - xo); } } while (0)
; #define P12_BAR() asm volatile("" ::: "memory")
; __device__ __forceinline__ void p12_peer(Frame& F) {
;     ...
;     { v4u cwA[8], cwB[8]; unsigned scA[8], scB[8]; v4u xa, xb; int xo;
;       P12_ISSUE(0, 0, 0, cwA, scA);
; _Pragma("nounroll")
;       for (int c = 0; c < 16; ++c) { const int cn = c + 1 < 16 ? c + 1 : 15;
;           P12_XQ(c, 0); P12_ISSUE(c, 0, 1, cwB, scB); P12_BAR(); P12_COMP(0, 0, cwA, scA); P12_ISSUE(c, 1, 0, cwA, scA); P12_BAR(); P12_COMP(0, 1, cwB, scB);
;           P12_XQ(c, 1); P12_ISSUE(c, 1, 1, cwB, scB); P12_BAR(); P12_COMP(1, 0, cwA, scA); P12_ISSUE(c, 2, 0, cwA, scA); P12_BAR(); P12_COMP(1, 1, cwB, scB);
;           P12_XQ(c, 2); P12_ISSUE(c, 2, 1, cwB, scB); P12_BAR(); P12_COMP(2, 0, cwA, scA); P12_ISSUE(c, 3, 0, cwA, scA); P12_BAR(); P12_COMP(2, 1, cwB, scB);
;           P12_XQ(c, 3); P12_ISSUE(c, 3, 1, cwB, scB); P12_BAR(); P12_COMP(3, 0, cwA, scA); P12_ISSUE(cn, 0, 0, cwA, scA); P12_BAR(); P12_COMP(3, 1, cwB, scB);
;       } }
	v_lshlrev_b32_e32 v1, 16, v91
	v_add_u32_e32 v3, v4, v5
	v_sub_u32_e32 v4, v3, v169
	v_cvt_f32_i32_e32 v3, v2
	v_cvt_f32_i32_e32 v2, v4
	v_lshlrev_b32_e32 v0, 16, v90
	v_mov_b32_e32 v4, 0
	v_mov_b32_e32 v5, 0
	v_pk_fma_f32 v[122:123], v[0:1], v[2:3], v[122:123]
	v_and_b32_e32 v0, 0xf0f0f0f, v12
	v_mov_b32_e32 v2, 0
	v_dot4c_i32_i8_e32 v2, v0, v32
	v_lshrrev_b32_e32 v0, 4, v12
	v_and_b32_e32 v0, 0xf0f0f0f, v0
	v_dot4c_i32_i8_e32 v2, v0, v33
	v_and_b32_e32 v0, 0xf0f0f0f, v13
	v_mov_b32_e32 v3, 0
	v_dot4c_i32_i8_e32 v3, v0, v34
	v_lshrrev_b32_e32 v0, 4, v13
	v_and_b32_e32 v0, 0xf0f0f0f, v0
	v_dot4c_i32_i8_e32 v3, v0, v35
	v_and_b32_e32 v0, 0xf0f0f0f, v14
	v_dot4c_i32_i8_e32 v2, v0, v28
	v_lshrrev_b32_e32 v0, 4, v14
	v_and_b32_e32 v0, 0xf0f0f0f, v0
	v_dot4c_i32_i8_e32 v2, v0, v29
	v_and_b32_e32 v0, 0xf0f0f0f, v15
	v_dot4c_i32_i8_e32 v3, v0, v30
	v_lshrrev_b32_e32 v0, 4, v15
	v_and_b32_e32 v0, 0xf0f0f0f, v0
	v_dot4c_i32_i8_e32 v3, v0, v31
	v_and_b32_e32 v0, 0xf0f0f0f, v8
	v_dot4c_i32_i8_e32 v4, v0, v32
	v_lshrrev_b32_e32 v0, 4, v8
	v_and_b32_e32 v0, 0xf0f0f0f, v0
	v_dot4c_i32_i8_e32 v4, v0, v33
	v_and_b32_e32 v0, 0xf0f0f0f, v9
	v_dot4c_i32_i8_e32 v5, v0, v34
	v_lshrrev_b32_e32 v0, 4, v9
	v_and_b32_e32 v0, 0xf0f0f0f, v0
	v_dot4c_i32_i8_e32 v5, v0, v35
	v_and_b32_e32 v0, 0xf0f0f0f, v10
	v_dot4c_i32_i8_e32 v4, v0, v28
	v_lshrrev_b32_e32 v0, 4, v10
	v_and_b32_e32 v0, 0xf0f0f0f, v0
	v_dot4c_i32_i8_e32 v4, v0, v29
	v_and_b32_e32 v0, 0xf0f0f0f, v11
	v_dot4c_i32_i8_e32 v5, v0, v30
	v_lshrrev_b32_e32 v0, 4, v11
	v_and_b32_e32 v0, 0xf0f0f0f, v0
	v_dot4c_i32_i8_e32 v5, v0, v31
	v_add_u32_e32 v2, v2, v3
	v_sub_u32_e32 v2, v2, v169
	s_waitcnt vmcnt(16)
	v_lshlrev_b32_e32 v1, 16, v89
	v_add_u32_e32 v3, v4, v5
	v_sub_u32_e32 v4, v3, v169
	v_cvt_f32_i32_e32 v3, v2
	v_cvt_f32_i32_e32 v2, v4
	v_lshlrev_b32_e32 v0, 16, v88
	v_pk_fma_f32 v[120:121], v[0:1], v[2:3], v[120:121]
	v_add_u32_e32 v0, s44, v232
	v_lshl_or_b32 v4, v0, 7, v165
	v_lshl_or_b32 v44, v0, 4, v95
	v_add_u32_e32 v0, s44, v233
	v_lshl_or_b32 v1, v0, 7, v165
	v_lshl_or_b32 v45, v0, 4, v95
	v_add_u32_e32 v0, s44, v234
	global_load_dwordx4 v[72:75], v4, s[0:1]
	global_load_dwordx4 v[24:27], v1, s[0:1]
	v_lshl_or_b32 v1, v0, 7, v165
	v_lshl_or_b32 v46, v0, 4, v95
	v_add_u32_e32 v0, s44, v235
	global_load_dwordx4 v[20:23], v1, s[0:1]
	v_lshl_or_b32 v1, v0, 7, v165
	v_lshl_or_b32 v47, v0, 4, v95
	global_load_dwordx4 v[16:19], v1, s[0:1]
	v_add_u32_e32 v0, s44, v236
	v_lshl_or_b32 v1, v0, 7, v165
	v_lshl_or_b32 v56, v0, 4, v95
	global_load_dwordx4 v[12:15], v1, s[0:1]
	v_add_u32_e32 v0, s44, v237
	v_lshl_or_b32 v1, v0, 7, v165
	v_lshl_or_b32 v57, v0, 4, v95
	global_load_dwordx4 v[8:11], v1, s[0:1]
	v_add_u32_e32 v0, s44, v238
	v_lshl_or_b32 v1, v0, 7, v165
	v_lshl_or_b32 v58, v0, 4, v95
	global_load_dwordx4 v[4:7], v1, s[0:1]
	v_add_u32_e32 v59, s44, v239
	v_lshl_or_b32 v0, v59, 7, v165
	global_load_dwordx4 v[0:3], v0, s[0:1]
	v_lshl_or_b32 v59, v59, 4, v95
	global_load_ushort v167, v45, s[18:19]
	global_load_ushort v168, v44, s[18:19]
	global_load_ushort v90, v47, s[18:19]
	global_load_ushort v91, v46, s[18:19]
	global_load_ushort v88, v56, s[18:19]
	global_load_ushort v89, v57, s[18:19]
	global_load_ushort v76, v58, s[18:19]
	global_load_ushort v77, v59, s[18:19]
	s_waitcnt vmcnt(31)
	v_and_b32_e32 v44, 0xf0f0f0f, v84
	v_mov_b32_e32 v46, 0
	v_dot4c_i32_i8_e32 v46, v44, v32
	v_lshrrev_b32_e32 v44, 4, v84
	v_and_b32_e32 v44, 0xf0f0f0f, v44
	v_dot4c_i32_i8_e32 v46, v44, v33
	v_and_b32_e32 v44, 0xf0f0f0f, v85
	v_mov_b32_e32 v47, 0
	v_dot4c_i32_i8_e32 v47, v44, v34
	v_lshrrev_b32_e32 v44, 4, v85
	v_and_b32_e32 v44, 0xf0f0f0f, v44
	v_dot4c_i32_i8_e32 v47, v44, v35
	v_and_b32_e32 v44, 0xf0f0f0f, v86
	v_dot4c_i32_i8_e32 v46, v44, v28
	v_lshrrev_b32_e32 v44, 4, v86
	v_and_b32_e32 v44, 0xf0f0f0f, v44
	v_dot4c_i32_i8_e32 v46, v44, v29
	v_and_b32_e32 v44, 0xf0f0f0f, v87
	v_dot4c_i32_i8_e32 v47, v44, v30
	v_lshrrev_b32_e32 v44, 4, v87
	v_and_b32_e32 v44, 0xf0f0f0f, v44
	v_dot4c_i32_i8_e32 v47, v44, v31
	s_waitcnt vmcnt(30)
	v_and_b32_e32 v44, 0xf0f0f0f, v80
	v_mov_b32_e32 v56, 0
	v_dot4c_i32_i8_e32 v56, v44, v32
	v_lshrrev_b32_e32 v44, 4, v80
	v_and_b32_e32 v44, 0xf0f0f0f, v44
	v_dot4c_i32_i8_e32 v56, v44, v33
	v_and_b32_e32 v44, 0xf0f0f0f, v81
	v_mov_b32_e32 v57, 0
	v_dot4c_i32_i8_e32 v57, v44, v34
	v_lshrrev_b32_e32 v44, 4, v81
	v_and_b32_e32 v44, 0xf0f0f0f, v44
	v_dot4c_i32_i8_e32 v57, v44, v35
	v_and_b32_e32 v44, 0xf0f0f0f, v82
	v_dot4c_i32_i8_e32 v56, v44, v28
	v_lshrrev_b32_e32 v44, 4, v82
	v_and_b32_e32 v44, 0xf0f0f0f, v44
	v_dot4c_i32_i8_e32 v56, v44, v29
	v_and_b32_e32 v44, 0xf0f0f0f, v83
	v_dot4c_i32_i8_e32 v57, v44, v30
	v_lshrrev_b32_e32 v44, 4, v83
	v_and_b32_e32 v44, 0xf0f0f0f, v44
	v_dot4c_i32_i8_e32 v57, v44, v31
	v_add_u32_e32 v46, v46, v47
	v_sub_u32_e32 v46, v46, v169
	s_waitcnt vmcnt(22)
	v_lshlrev_b32_e32 v45, 16, v179
	v_sub_u32_e32 v47, v57, v169
	v_add_u32_e32 v56, v47, v56
	v_cvt_f32_i32_e32 v47, v46
	v_cvt_f32_i32_e32 v46, v56
	v_lshlrev_b32_e32 v44, 16, v178
	v_mov_b32_e32 v56, 0
	v_mov_b32_e32 v57, 0
	v_pk_fma_f32 v[118:119], v[44:45], v[46:47], v[118:119]
	v_and_b32_e32 v44, 0xf0f0f0f, v68
	v_mov_b32_e32 v46, 0
	v_dot4c_i32_i8_e32 v46, v44, v32
	v_lshrrev_b32_e32 v44, 4, v68
	v_and_b32_e32 v44, 0xf0f0f0f, v44
	v_dot4c_i32_i8_e32 v46, v44, v33
	v_and_b32_e32 v44, 0xf0f0f0f, v69
	v_mov_b32_e32 v47, 0
	v_dot4c_i32_i8_e32 v47, v44, v34
	v_lshrrev_b32_e32 v44, 4, v69
	v_and_b32_e32 v44, 0xf0f0f0f, v44
	v_dot4c_i32_i8_e32 v47, v44, v35
	v_and_b32_e32 v44, 0xf0f0f0f, v70
	v_dot4c_i32_i8_e32 v46, v44, v28
	v_lshrrev_b32_e32 v44, 4, v70
	v_and_b32_e32 v44, 0xf0f0f0f, v44
	v_dot4c_i32_i8_e32 v46, v44, v29
	v_and_b32_e32 v44, 0xf0f0f0f, v71
	v_dot4c_i32_i8_e32 v47, v44, v30
	v_lshrrev_b32_e32 v44, 4, v71
	v_and_b32_e32 v44, 0xf0f0f0f, v44
	v_dot4c_i32_i8_e32 v47, v44, v31
	v_and_b32_e32 v44, 0xf0f0f0f, v64
	v_dot4c_i32_i8_e32 v56, v44, v32
	v_lshrrev_b32_e32 v44, 4, v64
	v_and_b32_e32 v44, 0xf0f0f0f, v44
	v_dot4c_i32_i8_e32 v56, v44, v33
	v_and_b32_e32 v44, 0xf0f0f0f, v65
	v_dot4c_i32_i8_e32 v57, v44, v34
	v_lshrrev_b32_e32 v44, 4, v65
	v_and_b32_e32 v44, 0xf0f0f0f, v44
	v_dot4c_i32_i8_e32 v57, v44, v35
	v_and_b32_e32 v44, 0xf0f0f0f, v66
	v_dot4c_i32_i8_e32 v56, v44, v28
	v_lshrrev_b32_e32 v44, 4, v66
	v_and_b32_e32 v44, 0xf0f0f0f, v44
	v_dot4c_i32_i8_e32 v56, v44, v29
	v_and_b32_e32 v44, 0xf0f0f0f, v67
	v_dot4c_i32_i8_e32 v57, v44, v30
	v_lshrrev_b32_e32 v44, 4, v67
	v_and_b32_e32 v44, 0xf0f0f0f, v44
	v_dot4c_i32_i8_e32 v57, v44, v31
	v_sub_u32_e32 v47, v47, v169
	v_add_u32_e32 v46, v47, v46
	v_cvt_f32_i32_e32 v47, v46
	v_sub_u32_e32 v57, v57, v169
	v_add_u32_e32 v56, v57, v56
	v_cvt_f32_i32_e32 v46, v56
	s_waitcnt vmcnt(20)
	v_lshlrev_b32_e32 v45, 16, v175
	v_lshlrev_b32_e32 v44, 16, v174
	v_pk_fma_f32 v[116:117], v[44:45], v[46:47], v[116:117]
	v_and_b32_e32 v44, 0xf0f0f0f, v52
	v_mov_b32_e32 v46, 0
	v_dot4c_i32_i8_e32 v46, v44, v32
	v_lshrrev_b32_e32 v44, 4, v52
	v_and_b32_e32 v44, 0xf0f0f0f, v44
	v_dot4c_i32_i8_e32 v46, v44, v33
	v_and_b32_e32 v44, 0xf0f0f0f, v53
	v_mov_b32_e32 v47, 0
	v_dot4c_i32_i8_e32 v47, v44, v34
	v_lshrrev_b32_e32 v44, 4, v53
	v_and_b32_e32 v44, 0xf0f0f0f, v44
	v_dot4c_i32_i8_e32 v47, v44, v35
	v_and_b32_e32 v44, 0xf0f0f0f, v54
	v_dot4c_i32_i8_e32 v46, v44, v28
	v_lshrrev_b32_e32 v44, 4, v54
	v_and_b32_e32 v44, 0xf0f0f0f, v44
	v_dot4c_i32_i8_e32 v46, v44, v29
	v_and_b32_e32 v44, 0xf0f0f0f, v55
	v_dot4c_i32_i8_e32 v47, v44, v30
	v_lshrrev_b32_e32 v44, 4, v55
	v_and_b32_e32 v44, 0xf0f0f0f, v44
	v_dot4c_i32_i8_e32 v47, v44, v31
	v_and_b32_e32 v44, 0xf0f0f0f, v48
	v_mov_b32_e32 v52, 0
	v_dot4c_i32_i8_e32 v52, v44, v32
	v_lshrrev_b32_e32 v44, 4, v48
	v_and_b32_e32 v44, 0xf0f0f0f, v44
	v_dot4c_i32_i8_e32 v52, v44, v33
	v_and_b32_e32 v44, 0xf0f0f0f, v49
	v_mov_b32_e32 v48, 0
	v_dot4c_i32_i8_e32 v48, v44, v34
	v_lshrrev_b32_e32 v44, 4, v49
	v_and_b32_e32 v44, 0xf0f0f0f, v44
	v_dot4c_i32_i8_e32 v48, v44, v35
	v_and_b32_e32 v44, 0xf0f0f0f, v50
	v_dot4c_i32_i8_e32 v52, v44, v28
	v_lshrrev_b32_e32 v44, 4, v50
	v_and_b32_e32 v44, 0xf0f0f0f, v44
	v_dot4c_i32_i8_e32 v52, v44, v29
	v_and_b32_e32 v44, 0xf0f0f0f, v51
	v_dot4c_i32_i8_e32 v48, v44, v30
	v_lshrrev_b32_e32 v44, 4, v51
	v_and_b32_e32 v44, 0xf0f0f0f, v44
	v_dot4c_i32_i8_e32 v48, v44, v31
	v_sub_u32_e32 v47, v47, v169
	v_add_u32_e32 v46, v47, v46
	v_cvt_f32_i32_e32 v47, v46
	v_sub_u32_e32 v48, v48, v169
	v_add_u32_e32 v48, v48, v52
	v_cvt_f32_i32_e32 v46, v48
	s_waitcnt vmcnt(18)
	v_lshlrev_b32_e32 v45, 16, v173
	v_lshlrev_b32_e32 v44, 16, v172
	v_pk_fma_f32 v[114:115], v[44:45], v[46:47], v[114:115]
	v_and_b32_e32 v44, 0xf0f0f0f, v40
	v_mov_b32_e32 v45, 0
	v_lshrrev_b32_e32 v40, 4, v40
	v_dot4c_i32_i8_e32 v45, v44, v32
	v_and_b32_e32 v40, 0xf0f0f0f, v40
	v_dot4c_i32_i8_e32 v45, v40, v33
	v_and_b32_e32 v40, 0xf0f0f0f, v41
	v_mov_b32_e32 v44, 0
	v_dot4c_i32_i8_e32 v44, v40, v34
	v_lshrrev_b32_e32 v40, 4, v41
	v_and_b32_e32 v40, 0xf0f0f0f, v40
	v_dot4c_i32_i8_e32 v44, v40, v35
	v_and_b32_e32 v40, 0xf0f0f0f, v42
	v_dot4c_i32_i8_e32 v45, v40, v28
	v_lshrrev_b32_e32 v40, 4, v42
	v_and_b32_e32 v40, 0xf0f0f0f, v40
	v_dot4c_i32_i8_e32 v45, v40, v29
	v_and_b32_e32 v40, 0xf0f0f0f, v43
	v_dot4c_i32_i8_e32 v44, v40, v30
	v_lshrrev_b32_e32 v40, 4, v43
	v_and_b32_e32 v40, 0xf0f0f0f, v40
	v_dot4c_i32_i8_e32 v44, v40, v31
	v_and_b32_e32 v40, 0xf0f0f0f, v36
	v_mov_b32_e32 v41, 0
	v_dot4c_i32_i8_e32 v41, v40, v32
	v_lshrrev_b32_e32 v32, 4, v36
	v_and_b32_e32 v32, 0xf0f0f0f, v32
	v_dot4c_i32_i8_e32 v41, v32, v33
	v_and_b32_e32 v32, 0xf0f0f0f, v37
	v_mov_b32_e32 v33, 0
	v_dot4c_i32_i8_e32 v33, v32, v34
	v_lshrrev_b32_e32 v32, 4, v37
	v_and_b32_e32 v32, 0xf0f0f0f, v32
	v_dot4c_i32_i8_e32 v33, v32, v35
	v_and_b32_e32 v32, 0xf0f0f0f, v38
	v_dot4c_i32_i8_e32 v41, v32, v28
	v_lshrrev_b32_e32 v28, 4, v38
	v_and_b32_e32 v28, 0xf0f0f0f, v28
	v_dot4c_i32_i8_e32 v41, v28, v29
	v_and_b32_e32 v28, 0xf0f0f0f, v39
	v_dot4c_i32_i8_e32 v33, v28, v30
	v_lshrrev_b32_e32 v28, 4, v39
	v_and_b32_e32 v28, 0xf0f0f0f, v28
	v_dot4c_i32_i8_e32 v33, v28, v31
	v_sub_u32_e32 v30, v44, v169
	v_add_u32_e32 v30, v30, v45
	s_waitcnt vmcnt(16)
; #define P12_ISSUE(c_, i_, h_, CW_, SC_) do { _Pragma("unroll") for (int bb = 0; bb < 8; ++bb) { const unsigned ro = (unsigned)(c_) * 16384u + (unsigned)EL[(i_) * 128 + ((h_) * 8 + bb) * 8 + g8]; \
;         CW_[bb] = *(const v4u*)(U4 + (size_t)(ro * 128u + 16u * (unsigned)k8)); SC_[bb] = USS[(size_t)(ro * 8u + (unsigned)k8)]; } } while (0)
; #define P12_COMP(i_, h_, CW_, SC_) do { _Pragma("unroll") for (int bb = 0; bb < 8; ++bb) { int a0 = 0, a1 = 0; P12_U4(CW_[bb].x, xa.x, xa.y, a0); P12_U4(CW_[bb].y, xa.z, xa.w, a1); P12_U4(CW_[bb].z, xb.x, xb.y, a0); P12_U4(CW_[bb].w, xb.z, xb.w, a1); \
;         psum[(i_)][(h_) * 8 + bb] += __uint_as_float(SC_[bb] << 16) * (float)((a0 + a1) - xo); } } while (0)
; #define P12_BAR() asm volatile("" ::: "memory")
; __device__ __forceinline__ void p12_peer(Frame& F) {
;     ...
;     { v4u cwA[8], cwB[8]; unsigned scA[8], scB[8]; v4u xa, xb; int xo;
;       P12_ISSUE(0, 0, 0, cwA, scA);
; _Pragma("nounroll")
;       for (int c = 0; c < 16; ++c) { const int cn = c + 1 < 16 ? c + 1 : 15;
;           P12_XQ(c, 0); P12_ISSUE(c, 0, 1, cwB, scB); P12_BAR(); P12_COMP(0, 0, cwA, scA); P12_ISSUE(c, 1, 0, cwA, scA); P12_BAR(); P12_COMP(0, 1, cwB, scB);
;           P12_XQ(c, 1); P12_ISSUE(c, 1, 1, cwB, scB); P12_BAR(); P12_COMP(1, 0, cwA, scA); P12_ISSUE(c, 2, 0, cwA, scA); P12_BAR(); P12_COMP(1, 1, cwB, scB);
;           P12_XQ(c, 2); P12_ISSUE(c, 2, 1, cwB, scB); P12_BAR(); P12_COMP(2, 0, cwA, scA); P12_ISSUE(c, 3, 0, cwA, scA); P12_BAR(); P12_COMP(2, 1, cwB, scB);
;           P12_XQ(c, 3); P12_ISSUE(c, 3, 1, cwB, scB); P12_BAR(); P12_COMP(3, 0, cwA, scA); P12_ISSUE(cn, 0, 0, cwA, scA); P12_BAR(); P12_COMP(3, 1, cwB, scB);
;       } }
	v_lshlrev_b32_e32 v29, 16, v171
	v_sub_u32_e32 v31, v33, v169
	v_add_u32_e32 v32, v31, v41
	v_cvt_f32_i32_e32 v31, v30
	v_cvt_f32_i32_e32 v30, v32
	v_lshlrev_b32_e32 v28, 16, v170
	ds_read_b128 v[36:39], v166 offset:12288
	ds_read_b128 v[32:35], v166 offset:12304
	v_add_u32_e32 v166, 0x100, v166
	v_pk_fma_f32 v[112:113], v[28:29], v[30:31], v[112:113]
	v_mov_b32_e32 v28, 0
	v_add_u32_e32 v29, s44, v240
	v_lshl_or_b32 v41, v29, 7, v165
	v_add_u32_e32 v30, s44, v241
	global_load_dwordx4 v[68:71], v41, s[0:1]
	v_lshl_or_b32 v41, v30, 7, v165
	v_add_u32_e32 v31, s44, v242
	global_load_dwordx4 v[64:67], v41, s[0:1]
	v_lshl_or_b32 v41, v31, 7, v165
	v_add_u32_e32 v40, s44, v243
	global_load_dwordx4 v[60:63], v41, s[0:1]
	v_lshl_or_b32 v41, v40, 7, v165
	v_lshl_or_b32 v79, v40, 4, v95
	global_load_dwordx4 v[56:59], v41, s[0:1]
	s_waitcnt lgkmcnt(0)
	v_dot4c_i32_i8_e32 v28, 0x1010101, v36
	v_dot4c_i32_i8_e32 v28, 0x1010101, v37
	v_dot4c_i32_i8_e32 v28, 0x1010101, v38
	v_add_u32_e32 v40, s44, v244
	v_lshl_or_b32 v41, v40, 7, v165
	v_lshl_or_b32 v80, v40, 4, v95
	global_load_dwordx4 v[52:55], v41, s[0:1]
	v_dot4c_i32_i8_e32 v28, 0x1010101, v39
	v_dot4c_i32_i8_e32 v28, 0x1010101, v32
	v_dot4c_i32_i8_e32 v28, 0x1010101, v33
	v_add_u32_e32 v40, s44, v245
	v_lshl_or_b32 v41, v40, 7, v165
	v_lshl_or_b32 v82, v40, 4, v95
	global_load_dwordx4 v[48:51], v41, s[0:1]
	v_dot4c_i32_i8_e32 v28, 0x1010101, v34
	v_dot4c_i32_i8_e32 v28, 0x1010101, v35
	v_lshl_or_b32 v29, v29, 4, v95
	v_add_u32_e32 v40, s44, v246
	v_lshl_or_b32 v41, v40, 7, v165
	v_lshl_or_b32 v87, v40, 4, v95
	v_lshl_or_b32 v30, v30, 4, v95
	v_lshl_or_b32 v31, v31, 4, v95
	global_load_dwordx4 v[44:47], v41, s[0:1]
	v_add_u32_e32 v78, s44, v247
	v_lshl_or_b32 v40, v78, 7, v165
	global_load_dwordx4 v[40:43], v40, s[0:1]
	v_lshl_or_b32 v169, v78, 4, v95
	v_lshlrev_b32_e32 v78, 3, v28
	global_load_ushort v85, v29, s[18:19]
	global_load_ushort v86, v30, s[18:19]
	global_load_ushort v83, v31, s[18:19]
	global_load_ushort v84, v79, s[18:19]
	global_load_ushort v81, v80, s[18:19]
	s_nop 0
	global_load_ushort v82, v82, s[18:19]
	s_nop 0
	global_load_ushort v79, v87, s[18:19]
	global_load_ushort v80, v169, s[18:19]
	s_waitcnt vmcnt(31)
	v_and_b32_e32 v29, 0xf0f0f0f, v72
	v_mov_b32_e32 v28, 0
	v_dot4c_i32_i8_e32 v28, v29, v36
	v_lshrrev_b32_e32 v29, 4, v72
	v_and_b32_e32 v29, 0xf0f0f0f, v29
	v_dot4c_i32_i8_e32 v28, v29, v37
	v_and_b32_e32 v30, 0xf0f0f0f, v73
	v_mov_b32_e32 v29, 0
	v_dot4c_i32_i8_e32 v29, v30, v38
	v_lshrrev_b32_e32 v30, 4, v73
	v_and_b32_e32 v30, 0xf0f0f0f, v30
	v_dot4c_i32_i8_e32 v29, v30, v39
	v_and_b32_e32 v30, 0xf0f0f0f, v74
	v_dot4c_i32_i8_e32 v28, v30, v32
	v_lshrrev_b32_e32 v30, 4, v74
	v_and_b32_e32 v30, 0xf0f0f0f, v30
	v_dot4c_i32_i8_e32 v28, v30, v33
	v_and_b32_e32 v30, 0xf0f0f0f, v75
	v_dot4c_i32_i8_e32 v29, v30, v34
	v_lshrrev_b32_e32 v30, 4, v75
	v_and_b32_e32 v30, 0xf0f0f0f, v30
	v_dot4c_i32_i8_e32 v29, v30, v35
	s_waitcnt vmcnt(30)
	v_and_b32_e32 v31, 0xf0f0f0f, v24
	v_mov_b32_e32 v30, 0
	v_lshrrev_b32_e32 v24, 4, v24
	v_dot4c_i32_i8_e32 v30, v31, v36
	v_and_b32_e32 v24, 0xf0f0f0f, v24
	v_dot4c_i32_i8_e32 v30, v24, v37
	v_and_b32_e32 v24, 0xf0f0f0f, v25
	v_mov_b32_e32 v31, 0
	v_dot4c_i32_i8_e32 v31, v24, v38
	v_lshrrev_b32_e32 v24, 4, v25
	v_and_b32_e32 v24, 0xf0f0f0f, v24
	v_dot4c_i32_i8_e32 v31, v24, v39
	v_and_b32_e32 v24, 0xf0f0f0f, v26
	v_dot4c_i32_i8_e32 v30, v24, v32
	v_lshrrev_b32_e32 v24, 4, v26
	v_and_b32_e32 v24, 0xf0f0f0f, v24
	v_dot4c_i32_i8_e32 v30, v24, v33
	v_and_b32_e32 v24, 0xf0f0f0f, v27
	v_dot4c_i32_i8_e32 v31, v24, v34
	v_lshrrev_b32_e32 v24, 4, v27
	v_and_b32_e32 v24, 0xf0f0f0f, v24
	v_dot4c_i32_i8_e32 v31, v24, v35
	v_add_u32_e32 v26, v28, v29
	v_sub_u32_e32 v26, v26, v78
	s_waitcnt vmcnt(22)
	v_lshlrev_b32_e32 v25, 16, v168
	v_add_u32_e32 v27, v30, v31
	v_sub_u32_e32 v28, v27, v78
	v_cvt_f32_i32_e32 v27, v26
	v_cvt_f32_i32_e32 v26, v28
	v_lshlrev_b32_e32 v24, 16, v167
	s_cselect_b32 s44, s44, s45
	v_pk_fma_f32 v[110:111], v[24:25], v[26:27], v[110:111]
	v_and_b32_e32 v24, 0xf0f0f0f, v20
	v_mov_b32_e32 v25, 0
	v_lshrrev_b32_e32 v20, 4, v20
	v_dot4c_i32_i8_e32 v25, v24, v36
	v_and_b32_e32 v20, 0xf0f0f0f, v20
	v_dot4c_i32_i8_e32 v25, v20, v37
	v_and_b32_e32 v20, 0xf0f0f0f, v21
	v_mov_b32_e32 v24, 0
	v_dot4c_i32_i8_e32 v24, v20, v38
	v_lshrrev_b32_e32 v20, 4, v21
	v_and_b32_e32 v20, 0xf0f0f0f, v20
	v_dot4c_i32_i8_e32 v24, v20, v39
	v_and_b32_e32 v20, 0xf0f0f0f, v22
	v_dot4c_i32_i8_e32 v25, v20, v32
	v_lshrrev_b32_e32 v20, 4, v22
	v_and_b32_e32 v20, 0xf0f0f0f, v20
	v_dot4c_i32_i8_e32 v25, v20, v33
	v_and_b32_e32 v20, 0xf0f0f0f, v23
	v_dot4c_i32_i8_e32 v24, v20, v34
	v_lshrrev_b32_e32 v20, 4, v23
	v_and_b32_e32 v20, 0xf0f0f0f, v20
	v_dot4c_i32_i8_e32 v24, v20, v35
	v_and_b32_e32 v20, 0xf0f0f0f, v16
	v_mov_b32_e32 v21, 0
	v_lshrrev_b32_e32 v16, 4, v16
	v_dot4c_i32_i8_e32 v21, v20, v36
	v_and_b32_e32 v16, 0xf0f0f0f, v16
	v_dot4c_i32_i8_e32 v21, v16, v37
	v_and_b32_e32 v16, 0xf0f0f0f, v17
	v_mov_b32_e32 v20, 0
	v_dot4c_i32_i8_e32 v20, v16, v38
	v_lshrrev_b32_e32 v16, 4, v17
	v_and_b32_e32 v16, 0xf0f0f0f, v16
	v_dot4c_i32_i8_e32 v20, v16, v39
	v_and_b32_e32 v16, 0xf0f0f0f, v18
	v_dot4c_i32_i8_e32 v21, v16, v32
	v_lshrrev_b32_e32 v16, 4, v18
	v_and_b32_e32 v16, 0xf0f0f0f, v16
	v_dot4c_i32_i8_e32 v21, v16, v33
	v_and_b32_e32 v16, 0xf0f0f0f, v19
	v_dot4c_i32_i8_e32 v20, v16, v34
	v_lshrrev_b32_e32 v16, 4, v19
	v_and_b32_e32 v16, 0xf0f0f0f, v16
	v_dot4c_i32_i8_e32 v20, v16, v35
	v_add_u32_e32 v18, v25, v24
	v_sub_u32_e32 v18, v18, v78
	s_waitcnt vmcnt(20)
; #define P12_ISSUE(c_, i_, h_, CW_, SC_) do { _Pragma("unroll") for (int bb = 0; bb < 8; ++bb) { const unsigned ro = (unsigned)(c_) * 16384u + (unsigned)EL[(i_) * 128 + ((h_) * 8 + bb) * 8 + g8]; \
;         CW_[bb] = *(const v4u*)(U4 + (size_t)(ro * 128u + 16u * (unsigned)k8)); SC_[bb] = USS[(size_t)(ro * 8u + (unsigned)k8)]; } } while (0)
; #define P12_COMP(i_, h_, CW_, SC_) do { _Pragma("unroll") for (int bb = 0; bb < 8; ++bb) { int a0 = 0, a1 = 0; P12_U4(CW_[bb].x, xa.x, xa.y, a0); P12_U4(CW_[bb].y, xa.z, xa.w, a1); P12_U4(CW_[bb].z, xb.x, xb.y, a0); P12_U4(CW_[bb].w, xb.z, xb.w, a1); \
;         psum[(i_)][(h_) * 8 + bb] += __uint_as_float(SC_[bb] << 16) * (float)((a0 + a1) - xo); } } while (0)
; #define P12_BAR() asm volatile("" ::: "memory")
; __device__ __forceinline__ void p12_peer(Frame& F) {
;     ...
;     { v4u cwA[8], cwB[8]; unsigned scA[8], scB[8]; v4u xa, xb; int xo;
;       P12_ISSUE(0, 0, 0, cwA, scA);
; _Pragma("nounroll")
;       for (int c = 0; c < 16; ++c) { const int cn = c + 1 < 16 ? c + 1 : 15;
;           P12_XQ(c, 0); P12_ISSUE(c, 0, 1, cwB, scB); P12_BAR(); P12_COMP(0, 0, cwA, scA); P12_ISSUE(c, 1, 0, cwA, scA); P12_BAR(); P12_COMP(0, 1, cwB, scB);
;           P12_XQ(c, 1); P12_ISSUE(c, 1, 1, cwB, scB); P12_BAR(); P12_COMP(1, 0, cwA, scA); P12_ISSUE(c, 2, 0, cwA, scA); P12_BAR(); P12_COMP(1, 1, cwB, scB);
;           P12_XQ(c, 2); P12_ISSUE(c, 2, 1, cwB, scB); P12_BAR(); P12_COMP(2, 0, cwA, scA); P12_ISSUE(c, 3, 0, cwA, scA); P12_BAR(); P12_COMP(2, 1, cwB, scB);
;           P12_XQ(c, 3); P12_ISSUE(c, 3, 1, cwB, scB); P12_BAR(); P12_COMP(3, 0, cwA, scA); P12_ISSUE(cn, 0, 0, cwA, scA); P12_BAR(); P12_COMP(3, 1, cwB, scB);
;       } }
	v_lshlrev_b32_e32 v17, 16, v91
	v_add_u32_e32 v19, v21, v20
	v_sub_u32_e32 v20, v19, v78
	v_cvt_f32_i32_e32 v19, v18
	v_cvt_f32_i32_e32 v18, v20
	v_lshlrev_b32_e32 v16, 16, v90
	v_mov_b32_e32 v90, 0
	s_cmp_eq_u32 s45, 0x40000
	v_pk_fma_f32 v[108:109], v[16:17], v[18:19], v[108:109]
	v_and_b32_e32 v16, 0xf0f0f0f, v12
	v_mov_b32_e32 v17, 0
	v_lshrrev_b32_e32 v12, 4, v12
	v_dot4c_i32_i8_e32 v17, v16, v36
	v_and_b32_e32 v12, 0xf0f0f0f, v12
	v_dot4c_i32_i8_e32 v17, v12, v37
	v_and_b32_e32 v12, 0xf0f0f0f, v13
	v_mov_b32_e32 v16, 0
	v_dot4c_i32_i8_e32 v16, v12, v38
	v_lshrrev_b32_e32 v12, 4, v13
	v_and_b32_e32 v12, 0xf0f0f0f, v12
	v_dot4c_i32_i8_e32 v16, v12, v39
	v_and_b32_e32 v12, 0xf0f0f0f, v14
	v_dot4c_i32_i8_e32 v17, v12, v32
	v_lshrrev_b32_e32 v12, 4, v14
	v_and_b32_e32 v12, 0xf0f0f0f, v12
	v_dot4c_i32_i8_e32 v17, v12, v33
	v_and_b32_e32 v12, 0xf0f0f0f, v15
	v_dot4c_i32_i8_e32 v16, v12, v34
	v_lshrrev_b32_e32 v12, 4, v15
	v_and_b32_e32 v12, 0xf0f0f0f, v12
	v_dot4c_i32_i8_e32 v16, v12, v35
	v_and_b32_e32 v12, 0xf0f0f0f, v8
	v_mov_b32_e32 v13, 0
	v_lshrrev_b32_e32 v8, 4, v8
	v_dot4c_i32_i8_e32 v13, v12, v36
	v_and_b32_e32 v8, 0xf0f0f0f, v8
	v_dot4c_i32_i8_e32 v13, v8, v37
	v_and_b32_e32 v8, 0xf0f0f0f, v9
	v_mov_b32_e32 v12, 0
	v_dot4c_i32_i8_e32 v12, v8, v38
	v_lshrrev_b32_e32 v8, 4, v9
	v_and_b32_e32 v8, 0xf0f0f0f, v8
	v_dot4c_i32_i8_e32 v12, v8, v39
	v_and_b32_e32 v8, 0xf0f0f0f, v10
	v_dot4c_i32_i8_e32 v13, v8, v32
	v_lshrrev_b32_e32 v8, 4, v10
	v_and_b32_e32 v8, 0xf0f0f0f, v8
	v_dot4c_i32_i8_e32 v13, v8, v33
	v_and_b32_e32 v8, 0xf0f0f0f, v11
	v_dot4c_i32_i8_e32 v12, v8, v34
	v_lshrrev_b32_e32 v8, 4, v11
	v_and_b32_e32 v8, 0xf0f0f0f, v8
	v_dot4c_i32_i8_e32 v12, v8, v35
	v_add_u32_e32 v11, v17, v16
	s_waitcnt vmcnt(18)
	v_lshlrev_b32_e32 v9, 16, v89
	v_lshlrev_b32_e32 v8, 16, v88
	v_add_u32_e32 v10, v13, v12
	v_sub_u32_e32 v12, v11, v78
	v_sub_u32_e32 v10, v10, v78
	v_cvt_f32_i32_e32 v11, v10
	v_cvt_f32_i32_e32 v10, v12
	s_waitcnt vmcnt(15)
	v_and_b32_e32 v89, 0xf0f0f0f, v68
	v_lshrrev_b32_e32 v68, 4, v68
	v_dot4c_i32_i8_e32 v90, v89, v36
	v_pk_fma_f32 v[106:107], v[8:9], v[10:11], v[106:107]
	v_and_b32_e32 v8, 0xf0f0f0f, v4
	v_mov_b32_e32 v9, 0
	v_lshrrev_b32_e32 v4, 4, v4
	v_dot4c_i32_i8_e32 v9, v8, v36
	v_and_b32_e32 v4, 0xf0f0f0f, v4
	v_dot4c_i32_i8_e32 v9, v4, v37
	v_and_b32_e32 v4, 0xf0f0f0f, v5
	v_mov_b32_e32 v8, 0
	v_dot4c_i32_i8_e32 v8, v4, v38
	v_lshrrev_b32_e32 v4, 4, v5
	v_and_b32_e32 v4, 0xf0f0f0f, v4
	v_dot4c_i32_i8_e32 v8, v4, v39
	v_and_b32_e32 v4, 0xf0f0f0f, v6
	v_dot4c_i32_i8_e32 v9, v4, v32
	v_lshrrev_b32_e32 v4, 4, v6
	v_and_b32_e32 v4, 0xf0f0f0f, v4
	v_dot4c_i32_i8_e32 v9, v4, v33
	v_and_b32_e32 v4, 0xf0f0f0f, v7
	v_dot4c_i32_i8_e32 v8, v4, v34
	v_lshrrev_b32_e32 v4, 4, v7
	v_and_b32_e32 v4, 0xf0f0f0f, v4
	v_dot4c_i32_i8_e32 v8, v4, v35
	v_and_b32_e32 v4, 0xf0f0f0f, v0
	v_mov_b32_e32 v5, 0
	v_lshrrev_b32_e32 v0, 4, v0
	v_dot4c_i32_i8_e32 v5, v4, v36
	v_and_b32_e32 v0, 0xf0f0f0f, v0
	v_dot4c_i32_i8_e32 v5, v0, v37
	v_and_b32_e32 v0, 0xf0f0f0f, v1
	v_mov_b32_e32 v4, 0
	v_dot4c_i32_i8_e32 v4, v0, v38
	v_lshrrev_b32_e32 v0, 4, v1
	v_and_b32_e32 v0, 0xf0f0f0f, v0
	v_dot4c_i32_i8_e32 v4, v0, v39
	v_and_b32_e32 v0, 0xf0f0f0f, v2
	v_dot4c_i32_i8_e32 v5, v0, v32
	v_lshrrev_b32_e32 v0, 4, v2
	v_and_b32_e32 v0, 0xf0f0f0f, v0
	v_dot4c_i32_i8_e32 v5, v0, v33
	v_and_b32_e32 v0, 0xf0f0f0f, v3
	v_dot4c_i32_i8_e32 v4, v0, v34
	v_lshrrev_b32_e32 v0, 4, v3
	v_and_b32_e32 v0, 0xf0f0f0f, v0
	v_dot4c_i32_i8_e32 v4, v0, v35
	v_add_u32_e32 v3, v9, v8
	v_lshlrev_b32_e32 v1, 16, v77
	v_lshlrev_b32_e32 v0, 16, v76
	v_add_u32_e32 v2, v5, v4
	v_sub_u32_e32 v4, v3, v78
	v_sub_u32_e32 v2, v2, v78
	v_cvt_f32_i32_e32 v3, v2
	v_cvt_f32_i32_e32 v2, v4
	v_and_b32_e32 v68, 0xf0f0f0f, v68
	v_dot4c_i32_i8_e32 v90, v68, v37
	v_and_b32_e32 v68, 0xf0f0f0f, v69
	v_pk_fma_f32 v[104:105], v[0:1], v[2:3], v[104:105]
	v_mov_b32_e32 v89, 0
	v_add_u32_e32 v0, s44, v184
	v_lshl_or_b32 v4, v0, 7, v165
	v_lshl_or_b32 v0, v0, 4, v95
	global_load_dwordx4 v[28:31], v4, s[0:1]
	global_load_ushort v72, v0, s[18:19]
	v_add_u32_e32 v0, s44, v185
	v_dot4c_i32_i8_e32 v89, v68, v38
	v_lshrrev_b32_e32 v68, 4, v69
	v_lshl_or_b32 v1, v0, 7, v165
	v_lshl_or_b32 v0, v0, 4, v95
	v_and_b32_e32 v68, 0xf0f0f0f, v68
	global_load_dwordx4 v[24:27], v1, s[0:1]
	global_load_ushort v73, v0, s[18:19]
	v_add_u32_e32 v0, s44, v186
	v_dot4c_i32_i8_e32 v89, v68, v39
	v_and_b32_e32 v68, 0xf0f0f0f, v70
	v_lshl_or_b32 v1, v0, 7, v165
	v_lshl_or_b32 v0, v0, 4, v95
	v_dot4c_i32_i8_e32 v90, v68, v32
	v_lshrrev_b32_e32 v68, 4, v70
	global_load_dwordx4 v[20:23], v1, s[0:1]
	global_load_ushort v74, v0, s[18:19]
	v_add_u32_e32 v0, s44, v187
	v_and_b32_e32 v68, 0xf0f0f0f, v68
	v_lshl_or_b32 v1, v0, 7, v165
	v_lshl_or_b32 v0, v0, 4, v95
	v_dot4c_i32_i8_e32 v90, v68, v33
	v_and_b32_e32 v68, 0xf0f0f0f, v71
	global_load_dwordx4 v[16:19], v1, s[0:1]
	global_load_ushort v75, v0, s[18:19]
	v_dot4c_i32_i8_e32 v89, v68, v34
	v_lshrrev_b32_e32 v68, 4, v71
	v_and_b32_e32 v68, 0xf0f0f0f, v68
	v_dot4c_i32_i8_e32 v89, v68, v35
	s_waitcnt vmcnt(22)
; #define P12_ISSUE(c_, i_, h_, CW_, SC_) do { _Pragma("unroll") for (int bb = 0; bb < 8; ++bb) { const unsigned ro = (unsigned)(c_) * 16384u + (unsigned)EL[(i_) * 128 + ((h_) * 8 + bb) * 8 + g8]; \
;         CW_[bb] = *(const v4u*)(U4 + (size_t)(ro * 128u + 16u * (unsigned)k8)); SC_[bb] = USS[(size_t)(ro * 8u + (unsigned)k8)]; } } while (0)
; #define P12_COMP(i_, h_, CW_, SC_) do { _Pragma("unroll") for (int bb = 0; bb < 8; ++bb) { int a0 = 0, a1 = 0; P12_U4(CW_[bb].x, xa.x, xa.y, a0); P12_U4(CW_[bb].y, xa.z, xa.w, a1); P12_U4(CW_[bb].z, xb.x, xb.y, a0); P12_U4(CW_[bb].w, xb.z, xb.w, a1); \
;         psum[(i_)][(h_) * 8 + bb] += __uint_as_float(SC_[bb] << 16) * (float)((a0 + a1) - xo); } } while (0)
; #define P12_BAR() asm volatile("" ::: "memory")
; __device__ __forceinline__ void p12_peer(Frame& F) {
;     ...
;     { v4u cwA[8], cwB[8]; unsigned scA[8], scB[8]; v4u xa, xb; int xo;
;       P12_ISSUE(0, 0, 0, cwA, scA);
; _Pragma("nounroll")
;       for (int c = 0; c < 16; ++c) { const int cn = c + 1 < 16 ? c + 1 : 15;
;           P12_XQ(c, 0); P12_ISSUE(c, 0, 1, cwB, scB); P12_BAR(); P12_COMP(0, 0, cwA, scA); P12_ISSUE(c, 1, 0, cwA, scA); P12_BAR(); P12_COMP(0, 1, cwB, scB);
;           P12_XQ(c, 1); P12_ISSUE(c, 1, 1, cwB, scB); P12_BAR(); P12_COMP(1, 0, cwA, scA); P12_ISSUE(c, 2, 0, cwA, scA); P12_BAR(); P12_COMP(1, 1, cwB, scB);
;           P12_XQ(c, 2); P12_ISSUE(c, 2, 1, cwB, scB); P12_BAR(); P12_COMP(2, 0, cwA, scA); P12_ISSUE(c, 3, 0, cwA, scA); P12_BAR(); P12_COMP(2, 1, cwB, scB);
;           P12_XQ(c, 3); P12_ISSUE(c, 3, 1, cwB, scB); P12_BAR(); P12_COMP(3, 0, cwA, scA); P12_ISSUE(cn, 0, 0, cwA, scA); P12_BAR(); P12_COMP(3, 1, cwB, scB);
;       } }
	v_and_b32_e32 v68, 0xf0f0f0f, v64
	v_mov_b32_e32 v69, 0
	v_lshrrev_b32_e32 v64, 4, v64
	v_dot4c_i32_i8_e32 v69, v68, v36
	v_and_b32_e32 v64, 0xf0f0f0f, v64
	v_dot4c_i32_i8_e32 v69, v64, v37
	v_and_b32_e32 v64, 0xf0f0f0f, v65
	v_mov_b32_e32 v68, 0
	v_add_u32_e32 v0, s44, v188
	v_dot4c_i32_i8_e32 v68, v64, v38
	v_lshrrev_b32_e32 v64, 4, v65
	v_lshl_or_b32 v1, v0, 7, v165
	v_lshl_or_b32 v0, v0, 4, v95
	v_and_b32_e32 v64, 0xf0f0f0f, v64
	global_load_dwordx4 v[12:15], v1, s[0:1]
	global_load_ushort v76, v0, s[18:19]
	v_dot4c_i32_i8_e32 v68, v64, v39
	v_and_b32_e32 v64, 0xf0f0f0f, v66
	v_dot4c_i32_i8_e32 v69, v64, v32
	v_lshrrev_b32_e32 v64, 4, v66
	v_and_b32_e32 v64, 0xf0f0f0f, v64
	v_dot4c_i32_i8_e32 v69, v64, v33
	v_and_b32_e32 v64, 0xf0f0f0f, v67
	v_dot4c_i32_i8_e32 v68, v64, v34
	v_lshrrev_b32_e32 v64, 4, v67
	v_add_u32_e32 v0, s44, v189
	v_and_b32_e32 v64, 0xf0f0f0f, v64
	v_lshl_or_b32 v1, v0, 7, v165
	v_lshl_or_b32 v0, v0, 4, v95
	v_dot4c_i32_i8_e32 v68, v64, v35
	global_load_dwordx4 v[8:11], v1, s[0:1]
	global_load_ushort v77, v0, s[18:19]
	v_add_u32_e32 v66, v90, v89
	v_sub_u32_e32 v67, v68, v78
	v_add_u32_e32 v67, v67, v69
	v_sub_u32_e32 v66, v66, v78
	v_cvt_f32_i32_e32 v66, v66
	v_cvt_f32_i32_e32 v67, v67
	v_add_u32_e32 v0, s44, v190
	s_waitcnt vmcnt(18)
	v_lshlrev_b32_e32 v65, 16, v86
	v_lshlrev_b32_e32 v64, 16, v85
	v_lshl_or_b32 v1, v0, 7, v165
	v_lshl_or_b32 v0, v0, 4, v95
	v_pk_fma_f32 v[102:103], v[64:65], v[66:67], v[102:103]
	v_and_b32_e32 v64, 0xf0f0f0f, v60
	v_mov_b32_e32 v65, 0
	v_lshrrev_b32_e32 v60, 4, v60
	global_load_dwordx4 v[4:7], v1, s[0:1]
	global_load_ushort v87, v0, s[18:19]
	v_dot4c_i32_i8_e32 v65, v64, v36
	v_and_b32_e32 v60, 0xf0f0f0f, v60
	v_dot4c_i32_i8_e32 v65, v60, v37
	v_and_b32_e32 v60, 0xf0f0f0f, v61
	v_mov_b32_e32 v64, 0
	v_dot4c_i32_i8_e32 v64, v60, v38
	v_lshrrev_b32_e32 v60, 4, v61
	v_and_b32_e32 v60, 0xf0f0f0f, v60
	v_dot4c_i32_i8_e32 v64, v60, v39
	v_and_b32_e32 v60, 0xf0f0f0f, v62
	v_add_u32_e32 v88, s44, v191
	v_dot4c_i32_i8_e32 v65, v60, v32
	v_lshrrev_b32_e32 v60, 4, v62
	v_lshl_or_b32 v0, v88, 7, v165
	v_lshl_or_b32 v88, v88, 4, v95
	v_and_b32_e32 v60, 0xf0f0f0f, v60
	global_load_dwordx4 v[0:3], v0, s[0:1]
	v_dot4c_i32_i8_e32 v65, v60, v33
	global_load_ushort v88, v88, s[18:19]
	v_and_b32_e32 v60, 0xf0f0f0f, v63
	v_dot4c_i32_i8_e32 v64, v60, v34
	v_lshrrev_b32_e32 v60, 4, v63
	v_and_b32_e32 v60, 0xf0f0f0f, v60
	v_dot4c_i32_i8_e32 v64, v60, v35
	v_and_b32_e32 v60, 0xf0f0f0f, v56
	v_mov_b32_e32 v61, 0
	v_lshrrev_b32_e32 v56, 4, v56
	v_dot4c_i32_i8_e32 v61, v60, v36
	v_and_b32_e32 v56, 0xf0f0f0f, v56
	v_dot4c_i32_i8_e32 v61, v56, v37
	v_and_b32_e32 v56, 0xf0f0f0f, v57
	v_mov_b32_e32 v60, 0
	v_dot4c_i32_i8_e32 v60, v56, v38
	v_lshrrev_b32_e32 v56, 4, v57
	v_and_b32_e32 v56, 0xf0f0f0f, v56
	v_dot4c_i32_i8_e32 v60, v56, v39
	v_and_b32_e32 v56, 0xf0f0f0f, v58
	v_dot4c_i32_i8_e32 v61, v56, v32
	v_lshrrev_b32_e32 v56, 4, v58
	v_and_b32_e32 v56, 0xf0f0f0f, v56
	v_dot4c_i32_i8_e32 v61, v56, v33
	v_and_b32_e32 v56, 0xf0f0f0f, v59
	v_dot4c_i32_i8_e32 v60, v56, v34
	v_lshrrev_b32_e32 v56, 4, v59
	v_and_b32_e32 v56, 0xf0f0f0f, v56
	v_dot4c_i32_i8_e32 v60, v56, v35
	v_sub_u32_e32 v59, v64, v78
	s_waitcnt vmcnt(20)
	v_lshlrev_b32_e32 v57, 16, v84
	v_lshlrev_b32_e32 v56, 16, v83
	v_sub_u32_e32 v58, v60, v78
	v_add_u32_e32 v60, v59, v65
	v_add_u32_e32 v58, v58, v61
	v_cvt_f32_i32_e32 v59, v58
	v_cvt_f32_i32_e32 v58, v60
	s_mov_b32 s44, s45
	v_pk_fma_f32 v[100:101], v[56:57], v[58:59], v[100:101]
	v_and_b32_e32 v56, 0xf0f0f0f, v52
	v_mov_b32_e32 v57, 0
	v_lshrrev_b32_e32 v52, 4, v52
	v_dot4c_i32_i8_e32 v57, v56, v36
	v_and_b32_e32 v52, 0xf0f0f0f, v52
	v_dot4c_i32_i8_e32 v57, v52, v37
	v_and_b32_e32 v52, 0xf0f0f0f, v53
	v_mov_b32_e32 v56, 0
	v_dot4c_i32_i8_e32 v56, v52, v38
	v_lshrrev_b32_e32 v52, 4, v53
	v_and_b32_e32 v52, 0xf0f0f0f, v52
	v_dot4c_i32_i8_e32 v56, v52, v39
	v_and_b32_e32 v52, 0xf0f0f0f, v54
	v_dot4c_i32_i8_e32 v57, v52, v32
	v_lshrrev_b32_e32 v52, 4, v54
	v_and_b32_e32 v52, 0xf0f0f0f, v52
	v_dot4c_i32_i8_e32 v57, v52, v33
	v_and_b32_e32 v52, 0xf0f0f0f, v55
	v_dot4c_i32_i8_e32 v56, v52, v34
	v_lshrrev_b32_e32 v52, 4, v55
	v_and_b32_e32 v52, 0xf0f0f0f, v52
	v_dot4c_i32_i8_e32 v56, v52, v35
	v_and_b32_e32 v52, 0xf0f0f0f, v48
	v_mov_b32_e32 v53, 0
	v_lshrrev_b32_e32 v48, 4, v48
	v_dot4c_i32_i8_e32 v53, v52, v36
	v_and_b32_e32 v48, 0xf0f0f0f, v48
	v_dot4c_i32_i8_e32 v53, v48, v37
	v_and_b32_e32 v48, 0xf0f0f0f, v49
	v_mov_b32_e32 v52, 0
	v_dot4c_i32_i8_e32 v52, v48, v38
	v_lshrrev_b32_e32 v48, 4, v49
	v_and_b32_e32 v48, 0xf0f0f0f, v48
	v_dot4c_i32_i8_e32 v52, v48, v39
	v_and_b32_e32 v48, 0xf0f0f0f, v50
	v_dot4c_i32_i8_e32 v53, v48, v32
	v_lshrrev_b32_e32 v48, 4, v50
	v_and_b32_e32 v48, 0xf0f0f0f, v48
	v_dot4c_i32_i8_e32 v53, v48, v33
	v_and_b32_e32 v48, 0xf0f0f0f, v51
	v_dot4c_i32_i8_e32 v52, v48, v34
	v_lshrrev_b32_e32 v48, 4, v51
	v_and_b32_e32 v48, 0xf0f0f0f, v48
	v_dot4c_i32_i8_e32 v52, v48, v35
	v_sub_u32_e32 v51, v56, v78
	s_waitcnt vmcnt(18)
; #define P12_ISSUE(c_, i_, h_, CW_, SC_) do { _Pragma("unroll") for (int bb = 0; bb < 8; ++bb) { const unsigned ro = (unsigned)(c_) * 16384u + (unsigned)EL[(i_) * 128 + ((h_) * 8 + bb) * 8 + g8]; \
;         CW_[bb] = *(const v4u*)(U4 + (size_t)(ro * 128u + 16u * (unsigned)k8)); SC_[bb] = USS[(size_t)(ro * 8u + (unsigned)k8)]; } } while (0)
; #define P12_COMP(i_, h_, CW_, SC_) do { _Pragma("unroll") for (int bb = 0; bb < 8; ++bb) { int a0 = 0, a1 = 0; P12_U4(CW_[bb].x, xa.x, xa.y, a0); P12_U4(CW_[bb].y, xa.z, xa.w, a1); P12_U4(CW_[bb].z, xb.x, xb.y, a0); P12_U4(CW_[bb].w, xb.z, xb.w, a1); \
;         psum[(i_)][(h_) * 8 + bb] += __uint_as_float(SC_[bb] << 16) * (float)((a0 + a1) - xo); } } while (0)
; #define P12_BAR() asm volatile("" ::: "memory")
; __device__ __forceinline__ void p12_peer(Frame& F) {
;     ...
;     { v4u cwA[8], cwB[8]; unsigned scA[8], scB[8]; v4u xa, xb; int xo;
;       P12_ISSUE(0, 0, 0, cwA, scA);
; _Pragma("nounroll")
;       for (int c = 0; c < 16; ++c) { const int cn = c + 1 < 16 ? c + 1 : 15;
;           P12_XQ(c, 0); P12_ISSUE(c, 0, 1, cwB, scB); P12_BAR(); P12_COMP(0, 0, cwA, scA); P12_ISSUE(c, 1, 0, cwA, scA); P12_BAR(); P12_COMP(0, 1, cwB, scB);
;           P12_XQ(c, 1); P12_ISSUE(c, 1, 1, cwB, scB); P12_BAR(); P12_COMP(1, 0, cwA, scA); P12_ISSUE(c, 2, 0, cwA, scA); P12_BAR(); P12_COMP(1, 1, cwB, scB);
;           P12_XQ(c, 2); P12_ISSUE(c, 2, 1, cwB, scB); P12_BAR(); P12_COMP(2, 0, cwA, scA); P12_ISSUE(c, 3, 0, cwA, scA); P12_BAR(); P12_COMP(2, 1, cwB, scB);
;           P12_XQ(c, 3); P12_ISSUE(c, 3, 1, cwB, scB); P12_BAR(); P12_COMP(3, 0, cwA, scA); P12_ISSUE(cn, 0, 0, cwA, scA); P12_BAR(); P12_COMP(3, 1, cwB, scB);
;       } }
	v_lshlrev_b32_e32 v49, 16, v82
	v_lshlrev_b32_e32 v48, 16, v81
	v_sub_u32_e32 v50, v52, v78
	v_add_u32_e32 v52, v51, v57
	v_add_u32_e32 v50, v50, v53
	v_cvt_f32_i32_e32 v51, v50
	v_cvt_f32_i32_e32 v50, v52
	v_pk_fma_f32 v[98:99], v[48:49], v[50:51], v[98:99]
	v_and_b32_e32 v48, 0xf0f0f0f, v44
	v_mov_b32_e32 v49, 0
	v_lshrrev_b32_e32 v44, 4, v44
	v_dot4c_i32_i8_e32 v49, v48, v36
	v_and_b32_e32 v44, 0xf0f0f0f, v44
	v_dot4c_i32_i8_e32 v49, v44, v37
	v_and_b32_e32 v44, 0xf0f0f0f, v45
	v_mov_b32_e32 v48, 0
	v_dot4c_i32_i8_e32 v48, v44, v38
	v_lshrrev_b32_e32 v44, 4, v45
	v_and_b32_e32 v44, 0xf0f0f0f, v44
	v_dot4c_i32_i8_e32 v48, v44, v39
	v_and_b32_e32 v44, 0xf0f0f0f, v46
	v_dot4c_i32_i8_e32 v49, v44, v32
	v_lshrrev_b32_e32 v44, 4, v46
	v_and_b32_e32 v44, 0xf0f0f0f, v44
	v_dot4c_i32_i8_e32 v49, v44, v33
	v_and_b32_e32 v44, 0xf0f0f0f, v47
	v_dot4c_i32_i8_e32 v48, v44, v34
	v_lshrrev_b32_e32 v44, 4, v47
	v_and_b32_e32 v44, 0xf0f0f0f, v44
	v_dot4c_i32_i8_e32 v48, v44, v35
	v_and_b32_e32 v44, 0xf0f0f0f, v40
	v_mov_b32_e32 v45, 0
	v_dot4c_i32_i8_e32 v45, v44, v36
	v_lshrrev_b32_e32 v36, 4, v40
	v_and_b32_e32 v36, 0xf0f0f0f, v36
	v_dot4c_i32_i8_e32 v45, v36, v37
	v_and_b32_e32 v36, 0xf0f0f0f, v41
	v_mov_b32_e32 v37, 0
	v_dot4c_i32_i8_e32 v37, v36, v38
	v_lshrrev_b32_e32 v36, 4, v41
	v_and_b32_e32 v36, 0xf0f0f0f, v36
	v_dot4c_i32_i8_e32 v37, v36, v39
	v_and_b32_e32 v36, 0xf0f0f0f, v42
	v_dot4c_i32_i8_e32 v45, v36, v32
	v_lshrrev_b32_e32 v32, 4, v42
	v_and_b32_e32 v32, 0xf0f0f0f, v32
	v_dot4c_i32_i8_e32 v45, v32, v33
	v_and_b32_e32 v32, 0xf0f0f0f, v43
	v_dot4c_i32_i8_e32 v37, v32, v34
	v_lshrrev_b32_e32 v32, 4, v43
	v_and_b32_e32 v32, 0xf0f0f0f, v32
	v_dot4c_i32_i8_e32 v37, v32, v35
	v_sub_u32_e32 v35, v48, v78
	v_add_u32_e32 v36, v35, v49
	s_waitcnt vmcnt(16)
	v_lshlrev_b32_e32 v33, 16, v80
	v_sub_u32_e32 v34, v37, v78
	v_add_u32_e32 v34, v34, v45
	v_cvt_f32_i32_e32 v35, v34
	v_cvt_f32_i32_e32 v34, v36
	v_lshlrev_b32_e32 v32, 16, v79
	s_waitcnt vmcnt(0)
	v_perm_b32 v40, v87, v88, s43
	v_perm_b32 v41, v76, v77, s43
	v_pk_fma_f32 v[96:97], v[32:33], v[34:35], v[96:97]
	v_perm_b32 v42, v74, v75, s43
	v_perm_b32 v43, v72, v73, s43
	s_cbranch_scc0 .LBB0_3272
; #define LDS_WAIT() asm volatile("s_waitcnt lgkmcnt(0)" ::: "memory")
; __device__ __forceinline__ float wave_sum(float v) { v = dpp_add16(v); return (rdlane(v, 0) + rdlane(v, 16)) + (rdlane(v, 32) + rdlane(v, 48)); }
; __device__ __forceinline__ float wave_max(float v) { v = dpp_max16(v); return fmaxf(fmaxf(rdlane(v, 0), rdlane(v, 16)), fmaxf(rdlane(v, 32), rdlane(v, 48))); }
; __device__ __forceinline__ void p12_peer(Frame& F) {
;     ...
;         mxa = wave_max(mxa); const float inv = mxa > 0.f ? 127.0f / mxa : 0.f;
;         const float rsn = 1.0f / sqrtf(wave_sum(PSQ[(size_t)t * 64 + F.lane]) * (1.f / D_) + 1e-6f);
;         sx[i] = mxa * rsn * (1.0f / 127.0f);
;     ...
;     asm volatile("" ::: "memory"); LDS_WAIT();
; #pragma unroll
;     for (int i = 0; i < 4; ++i) { const int t = F.gw + i * F.NGW;
; #pragma unroll
;         for (int b = 0; b < 16; ++b) { float d = psum[i][b];
;             d += __builtin_bit_cast(float, __builtin_amdgcn_update_dpp(0, __builtin_bit_cast(int, d), 0xB1, 0xF, 0xF, false));
;             d += __builtin_bit_cast(float, __builtin_amdgcn_update_dpp(0, __builtin_bit_cast(int, d), 0x4E, 0xF, 0xF, false));
;             d += __builtin_bit_cast(float, __builtin_amdgcn_update_dpp(0, __builtin_bit_cast(int, d), 0x141, 0xF, 0xF, false));
;             const int idx = b * 8 + g8; const float w = PGT[(size_t)t * 128 + idx] * gelu_erf(sx[i] * d) * VSC[EL[i * 128 + idx]];
;             if (k8 == 0) WL[i * 128 + idx] = w; } }
	v_mov_b32_e32 v0, s41
	v_mov_b32_e32 v1, s42
	v_add_f32_e32 v0, s39, v0
	v_add_f32_e32 v1, s40, v1
	v_add_f32_e32 v0, v0, v1
	v_mov_b32_e32 v1, 0x358637bd
	v_fmac_f32_e32 v1, 0x39800000, v0
	s_mov_b32 s0, 0xf800000
	v_mul_f32_e32 v0, 0x4f800000, v1
	v_cmp_gt_f32_e32 vcc, s0, v1
	s_add_u32 s43, s68, 0x1200000
	s_addc_u32 s44, s69, 0
	v_cndmask_b32_e32 v0, v1, v0, vcc
	v_sqrt_f32_e32 v1, v0
	s_add_u32 s18, s68, 0xf000000
	s_addc_u32 s19, s69, 0
	v_add_u32_e32 v2, -1, v1
	v_fma_f32 v3, -v2, v1, v0
	v_cmp_ge_f32_e64 s[0:1], 0, v3
	v_add_u32_e32 v3, 1, v1
	s_add_u32 s2, s43, s2
	v_cndmask_b32_e64 v2, v1, v2, s[0:1]
	v_fma_f32 v1, -v3, v1, v0
	v_cmp_lt_f32_e64 s[0:1], 0, v1
	s_waitcnt lgkmcnt(0)
	s_addc_u32 s3, s44, s3
	v_ashrrev_i32_e32 v95, 31, v94
	v_cndmask_b32_e64 v1, v2, v3, s[0:1]
	v_mul_f32_e32 v2, 0x37800000, v1
	v_cndmask_b32_e32 v1, v1, v2, vcc
	v_mov_b32_e32 v2, 0x260
	v_cmp_class_f32_e32 vcc, v0, v2
	s_nop 1
	v_cndmask_b32_e32 v2, v1, v0, vcc
	v_div_scale_f32 v3, s[0:1], v2, v2, 1.0
	v_rcp_f32_e32 v4, v3
	v_lshl_add_u64 v[0:1], v[94:95], 2, s[2:3]
	ds_read_u16 v20, v93 offset:16384
	ds_read_u16 v21, v93 offset:16400
	ds_read_u16 v22, v93 offset:16416
	ds_read_u16 v23, v93 offset:16432
	ds_read_u16 v24, v93 offset:16448
	ds_read_u16 v25, v93 offset:16464
	ds_read_u16 v26, v93 offset:16480
	ds_read_u16 v27, v93 offset:16496
	s_waitcnt lgkmcnt(0)
	ds_read_u16 v28, v93 offset:16512
	ds_read_u16 v29, v93 offset:16528
	ds_read_u16 v30, v93 offset:16544
	ds_read_u16 v31, v93 offset:16560
	ds_read_u16 v32, v93 offset:16576
	ds_read_u16 v33, v93 offset:16592
	ds_read_u16 v34, v93 offset:16608
	ds_read_u16 v35, v93 offset:16624
	s_waitcnt lgkmcnt(0)
	v_lshlrev_b32_e32 v20, 2, v20
	v_lshlrev_b32_e32 v21, 2, v21
	v_lshlrev_b32_e32 v22, 2, v22
	v_lshlrev_b32_e32 v23, 2, v23
	v_lshlrev_b32_e32 v24, 2, v24
	v_lshlrev_b32_e32 v25, 2, v25
	v_lshlrev_b32_e32 v26, 2, v26
	v_lshlrev_b32_e32 v27, 2, v27
	v_lshlrev_b32_e32 v28, 2, v28
	v_lshlrev_b32_e32 v29, 2, v29
	v_lshlrev_b32_e32 v30, 2, v30
	v_lshlrev_b32_e32 v31, 2, v31
	v_lshlrev_b32_e32 v32, 2, v32
	v_lshlrev_b32_e32 v33, 2, v33
	v_lshlrev_b32_e32 v34, 2, v34
	v_lshlrev_b32_e32 v35, 2, v35
	global_load_dword v40, v[0:1], off offset:0
	global_load_dword v60, v20, s[18:19]
	global_load_dword v41, v[0:1], off offset:32
	global_load_dword v61, v21, s[18:19]
	global_load_dword v42, v[0:1], off offset:64
	global_load_dword v62, v22, s[18:19]
	global_load_dword v43, v[0:1], off offset:96
	global_load_dword v63, v23, s[18:19]
	global_load_dword v44, v[0:1], off offset:128
	global_load_dword v64, v24, s[18:19]
	global_load_dword v45, v[0:1], off offset:160
	global_load_dword v65, v25, s[18:19]
	global_load_dword v46, v[0:1], off offset:192
	global_load_dword v66, v26, s[18:19]
	global_load_dword v47, v[0:1], off offset:224
	global_load_dword v67, v27, s[18:19]
	global_load_dword v48, v[0:1], off offset:256
	global_load_dword v68, v28, s[18:19]
	global_load_dword v49, v[0:1], off offset:288
	global_load_dword v69, v29, s[18:19]
	global_load_dword v50, v[0:1], off offset:320
	global_load_dword v70, v30, s[18:19]
	global_load_dword v51, v[0:1], off offset:352
	global_load_dword v71, v31, s[18:19]
	global_load_dword v52, v[0:1], off offset:384
	global_load_dword v72, v32, s[18:19]
	global_load_dword v53, v[0:1], off offset:416
	global_load_dword v73, v33, s[18:19]
	global_load_dword v54, v[0:1], off offset:448
	global_load_dword v74, v34, s[18:19]
	global_load_dword v55, v[0:1], off offset:480
	global_load_dword v75, v35, s[18:19]
	s_waitcnt vmcnt(0)
	v_cmp_eq_u32_e64 s[0:1], 0, v164
	v_fma_f32 v5, -v3, v4, 1.0
	v_fmac_f32_e32 v4, v5, v4
	v_div_scale_f32 v5, vcc, 1.0, v2, 1.0
	v_mul_f32_e32 v6, v5, v4
	v_fma_f32 v7, -v3, v6, v5
	v_fmac_f32_e32 v6, v7, v4
	v_fma_f32 v3, -v3, v6, v5
	v_div_fmas_f32 v3, v3, v4, v6
	v_div_fixup_f32 v2, v3, v2, 1.0
	v_add_f32_dpp v5, v159, v159 quad_perm:[1,0,3,2] row_mask:0xf bank_mask:0xf bound_ctrl:1
	v_mul_f32_e32 v3, v163, v2
	v_mov_b32_e32 v6, 0
	v_add_f32_dpp v5, v5, v5 quad_perm:[2,3,0,1] row_mask:0xf bank_mask:0xf bound_ctrl:1
	v_mov_b32_e32 v4, 0
	v_lshl_add_u32 v2, v94, 2, s20
	v_mul_f32_e32 v3, 0x3c010204, v3
	v_mov_b32_dpp v6, v5 row_half_mirror row_mask:0xf bank_mask:0xf
	s_and_saveexec_b64 s[2:3], s[0:1]
	s_cbranch_execz .LBB0_3275
	v_add_f32_e32 v5, v5, v6
	v_mul_f32_e32 v5, v3, v5
	s_mov_b32 s39, 0x3e6d3388
	v_mul_f32_e32 v6, v5, v5
	s_waitcnt lgkmcnt(0)
	v_fma_f32 v7, |v5|, s39, 1.0
	v_rcp_f32_e32 v7, v7
	v_mov_b32_e32 v10, 0xbf3a00e3
	v_mul_f32_e32 v6, 0xbf38aa3b, v6
	v_exp_f32_e32 v6, v6
	v_fmac_f32_e32 v10, 0x3f07dc22, v7
	v_fmaak_f32 v10, v7, v10, 0x3f35f0e3
	v_fmaak_f32 v10, v7, v10, 0xbe11a98e
	v_fmaak_f32 v10, v7, v10, 0x3e027906
	v_mul_f32_e32 v7, v7, v10
	v_mul_f32_e32 v6, v6, v7
	v_mul_f32_e32 v7, v5, v6
	v_fma_f32 v6, -v5, v6, v5
	v_cmp_gt_f32_e32 vcc, 0, v5
	s_nop 1
	v_cndmask_b32_e32 v5, v6, v7, vcc
	s_waitcnt vmcnt(1)
	v_mul_f32_e32 v5, v5, v40
	s_waitcnt vmcnt(0)
	v_mul_f32_e32 v5, v5, v60
	ds_write_b32 v2, v5
